# GEMM K-loops: the vmcnt and lgkmcnt waits before each segment barrier merged into one s_waitcnt, on top of v144
# speedup vs baseline: 1.0010x; 1.0010x over previous
.LBB0_143:
	ds_read_b128 v[148:151], v142
	ds_read_b128 v[152:155], v142 offset:1024
	ds_read_b128 v[156:159], v142 offset:2048
	ds_read_b128 v[160:163], v142 offset:3072
	ds_read_b128 v[164:167], v143
	ds_read_b128 v[174:177], v143 offset:1024
	ds_read_b128 v[178:181], v143 offset:2048
	ds_read_b128 v[182:185], v143 offset:3072
	s_add_u32 s40, s22, 0x100
	s_addc_u32 s41, s23, 0
	s_cmp_eq_u32 s82, 12
	s_cselect_b32 s58, s33, s40
	s_cselect_b32 s59, s13, s41
	s_cselect_b32 s56, s79, s80
	s_cselect_b32 s57, s15, s81
	s_add_u32 s54, s58, 0x80
	s_addc_u32 s55, s59, 0
	ds_read_b128 v[186:189], v144
	ds_read_b128 v[190:193], v144 offset:1024
	ds_read_b128 v[194:197], v144 offset:2048
	ds_read_b128 v[198:201], v144 offset:3072
	ds_read_b128 v[202:205], v144 offset:4096
	ds_read_b128 v[206:209], v144 offset:5120
	ds_read_b128 v[210:213], v144 offset:6144
	ds_read_b128 v[214:217], v144 offset:7168
	s_add_u32 s22, s22, 0x40080
	s_addc_u32 s23, s23, 0
	s_mov_b32 s83, m0
	s_mov_b32 m0, s67
	s_nop 2
	global_load_lds_dwordx4 v136, s[22:23]
	s_mov_b32 m0, s83
	s_nop 0
	s_mov_b32 s83, m0
	s_mov_b32 m0, s76
	s_nop 2
	global_load_lds_dwordx4 v138, s[22:23]
	s_mov_b32 m0, s83
	s_waitcnt vmcnt(8) lgkmcnt(0)
	s_barrier
	s_setprio 1
	v_mfma_f32_16x16x32_bf16 v[126:129], v[148:151], v[186:189], v[126:129]
	v_mfma_f32_16x16x32_bf16 v[122:125], v[156:159], v[186:189], v[122:125]
	v_mfma_f32_16x16x32_bf16 v[110:113], v[148:151], v[194:197], v[110:113]
	v_mfma_f32_16x16x32_bf16 v[106:109], v[156:159], v[194:197], v[106:109]
	v_mfma_f32_16x16x32_bf16 v[94:97], v[148:151], v[202:205], v[94:97]
	v_mfma_f32_16x16x32_bf16 v[90:93], v[156:159], v[202:205], v[90:93]
	v_mfma_f32_16x16x32_bf16 v[78:81], v[148:151], v[210:213], v[78:81]
	v_mfma_f32_16x16x32_bf16 v[74:77], v[156:159], v[210:213], v[74:77]
	v_mfma_f32_16x16x32_bf16 v[126:129], v[152:155], v[190:193], v[126:129]
	v_mfma_f32_16x16x32_bf16 v[122:125], v[160:163], v[190:193], v[122:125]
	v_mfma_f32_16x16x32_bf16 v[110:113], v[152:155], v[198:201], v[110:113]
	v_mfma_f32_16x16x32_bf16 v[106:109], v[160:163], v[198:201], v[106:109]
	v_mfma_f32_16x16x32_bf16 v[94:97], v[152:155], v[206:209], v[94:97]
	v_mfma_f32_16x16x32_bf16 v[90:93], v[160:163], v[206:209], v[90:93]
	v_mfma_f32_16x16x32_bf16 v[78:81], v[152:155], v[214:217], v[78:81]
	v_mfma_f32_16x16x32_bf16 v[74:77], v[160:163], v[214:217], v[74:77]
	v_mfma_f32_16x16x32_bf16 v[118:121], v[164:167], v[186:189], v[118:121]
	v_mfma_f32_16x16x32_bf16 v[114:117], v[178:181], v[186:189], v[114:117]
	v_mfma_f32_16x16x32_bf16 v[102:105], v[164:167], v[194:197], v[102:105]
	v_mfma_f32_16x16x32_bf16 v[98:101], v[178:181], v[194:197], v[98:101]
	v_mfma_f32_16x16x32_bf16 v[86:89], v[164:167], v[202:205], v[86:89]
	v_mfma_f32_16x16x32_bf16 v[82:85], v[178:181], v[202:205], v[82:85]
	v_mfma_f32_16x16x32_bf16 v[70:73], v[164:167], v[210:213], v[70:73]
	v_mfma_f32_16x16x32_bf16 v[66:69], v[178:181], v[210:213], v[66:69]
	v_mfma_f32_16x16x32_bf16 v[118:121], v[174:177], v[190:193], v[118:121]
	v_mfma_f32_16x16x32_bf16 v[114:117], v[182:185], v[190:193], v[114:117]
	v_mfma_f32_16x16x32_bf16 v[102:105], v[174:177], v[198:201], v[102:105]
	v_mfma_f32_16x16x32_bf16 v[98:101], v[182:185], v[198:201], v[98:101]
	v_mfma_f32_16x16x32_bf16 v[86:89], v[174:177], v[206:209], v[86:89]
	v_mfma_f32_16x16x32_bf16 v[82:85], v[182:185], v[206:209], v[82:85]
	v_mfma_f32_16x16x32_bf16 v[70:73], v[174:177], v[214:217], v[70:73]
	v_mfma_f32_16x16x32_bf16 v[66:69], v[182:185], v[214:217], v[66:69]
	s_setprio 0
	s_barrier
	ds_read_b128 v[186:189], v144 offset:16384
	ds_read_b128 v[190:193], v144 offset:17408
	ds_read_b128 v[194:197], v144 offset:18432
	ds_read_b128 v[198:201], v144 offset:19456
	ds_read_b128 v[202:205], v144 offset:20480
	ds_read_b128 v[206:209], v144 offset:21504
	ds_read_b128 v[210:213], v144 offset:22528
	ds_read_b128 v[214:217], v144 offset:23552
	s_mov_b32 s22, m0
	s_mov_b32 m0, s30
	s_nop 2
	global_load_lds_dwordx4 v137, s[56:57]
	s_mov_b32 m0, s22
	s_nop 0
	s_mov_b32 s22, m0
	s_mov_b32 m0, s31
	s_nop 2
	global_load_lds_dwordx4 v139, s[56:57]
	s_mov_b32 m0, s22
	s_add_u32 s22, s56, 0x40000
	s_addc_u32 s23, s57, 0
	s_mov_b32 s83, m0
	s_mov_b32 m0, s34
	s_nop 2
	global_load_lds_dwordx4 v137, s[22:23]
	s_mov_b32 m0, s83
	s_nop 0
	s_mov_b32 s83, m0
	s_mov_b32 m0, s35
	s_nop 2
	global_load_lds_dwordx4 v139, s[22:23]
	s_mov_b32 m0, s83
	s_mov_b32 s22, m0
	s_mov_b32 m0, s21
	s_nop 2
	global_load_lds_dwordx4 v136, s[58:59]
	s_mov_b32 m0, s22
	s_nop 0
	s_mov_b32 s22, m0
	s_mov_b32 m0, s36
	s_nop 2
	global_load_lds_dwordx4 v138, s[58:59]
	s_mov_b32 m0, s22
	s_waitcnt vmcnt(8) lgkmcnt(0)
	s_barrier
	s_setprio 1
	v_mfma_f32_16x16x32_bf16 v[62:65], v[148:151], v[186:189], v[62:65]
	v_mfma_f32_16x16x32_bf16 v[58:61], v[156:159], v[186:189], v[58:61]
	v_mfma_f32_16x16x32_bf16 v[46:49], v[148:151], v[194:197], v[46:49]
	v_mfma_f32_16x16x32_bf16 v[42:45], v[156:159], v[194:197], v[42:45]
	v_mfma_f32_16x16x32_bf16 v[30:33], v[148:151], v[202:205], v[30:33]
	v_mfma_f32_16x16x32_bf16 v[26:29], v[156:159], v[202:205], v[26:29]
	v_mfma_f32_16x16x32_bf16 v[14:17], v[148:151], v[210:213], v[14:17]
	v_mfma_f32_16x16x32_bf16 v[10:13], v[156:159], v[210:213], v[10:13]
	v_mfma_f32_16x16x32_bf16 v[62:65], v[152:155], v[190:193], v[62:65]
	v_mfma_f32_16x16x32_bf16 v[58:61], v[160:163], v[190:193], v[58:61]
	v_mfma_f32_16x16x32_bf16 v[46:49], v[152:155], v[198:201], v[46:49]
	v_mfma_f32_16x16x32_bf16 v[42:45], v[160:163], v[198:201], v[42:45]
	v_mfma_f32_16x16x32_bf16 v[30:33], v[152:155], v[206:209], v[30:33]
	v_mfma_f32_16x16x32_bf16 v[26:29], v[160:163], v[206:209], v[26:29]
	v_mfma_f32_16x16x32_bf16 v[14:17], v[152:155], v[214:217], v[14:17]
	v_mfma_f32_16x16x32_bf16 v[10:13], v[160:163], v[214:217], v[10:13]
	v_mfma_f32_16x16x32_bf16 v[54:57], v[164:167], v[186:189], v[54:57]
	v_mfma_f32_16x16x32_bf16 v[50:53], v[178:181], v[186:189], v[50:53]
	v_mfma_f32_16x16x32_bf16 v[38:41], v[164:167], v[194:197], v[38:41]
	v_mfma_f32_16x16x32_bf16 v[34:37], v[178:181], v[194:197], v[34:37]
	v_mfma_f32_16x16x32_bf16 v[22:25], v[164:167], v[202:205], v[22:25]
	v_mfma_f32_16x16x32_bf16 v[18:21], v[178:181], v[202:205], v[18:21]
	v_mfma_f32_16x16x32_bf16 v[6:9], v[164:167], v[210:213], v[6:9]
	v_mfma_f32_16x16x32_bf16 v[2:5], v[178:181], v[210:213], v[2:5]
	v_mfma_f32_16x16x32_bf16 v[54:57], v[174:177], v[190:193], v[54:57]
	v_mfma_f32_16x16x32_bf16 v[50:53], v[182:185], v[190:193], v[50:53]
	v_mfma_f32_16x16x32_bf16 v[38:41], v[174:177], v[198:201], v[38:41]
	v_mfma_f32_16x16x32_bf16 v[34:37], v[182:185], v[198:201], v[34:37]
	v_mfma_f32_16x16x32_bf16 v[22:25], v[174:177], v[206:209], v[22:25]
	v_mfma_f32_16x16x32_bf16 v[18:21], v[182:185], v[206:209], v[18:21]
	v_mfma_f32_16x16x32_bf16 v[6:9], v[174:177], v[214:217], v[6:9]
	v_mfma_f32_16x16x32_bf16 v[2:5], v[182:185], v[214:217], v[2:5]
	s_setprio 0
	s_barrier
	ds_read_b128 v[148:151], v145
	ds_read_b128 v[152:155], v145 offset:1024
	ds_read_b128 v[156:159], v145 offset:2048
	ds_read_b128 v[160:163], v145 offset:3072
	ds_read_b128 v[164:167], v146
	ds_read_b128 v[174:177], v146 offset:1024
	ds_read_b128 v[178:181], v146 offset:2048
	ds_read_b128 v[182:185], v146 offset:3072
	ds_read_b128 v[186:189], v144 offset:32768
	ds_read_b128 v[190:193], v144 offset:33792
	ds_read_b128 v[194:197], v144 offset:34816
	ds_read_b128 v[198:201], v144 offset:35840
	ds_read_b128 v[202:205], v144 offset:36864
	ds_read_b128 v[206:209], v144 offset:37888
	ds_read_b128 v[210:213], v144 offset:38912
	ds_read_b128 v[214:217], v144 offset:39936
	s_add_u32 s22, s58, 0x40000
	s_addc_u32 s23, s59, 0
	s_mov_b32 s58, m0
	s_mov_b32 m0, s37
	s_nop 2
	global_load_lds_dwordx4 v136, s[22:23]
	s_mov_b32 m0, s58
	s_nop 0
	s_mov_b32 s58, m0
	s_mov_b32 m0, s52
	s_nop 2
	global_load_lds_dwordx4 v138, s[22:23]
	s_mov_b32 m0, s58
	s_waitcnt vmcnt(8) lgkmcnt(0)
	s_barrier
	s_setprio 1
	v_mfma_f32_16x16x32_bf16 v[126:129], v[148:151], v[186:189], v[126:129]
	v_mfma_f32_16x16x32_bf16 v[122:125], v[156:159], v[186:189], v[122:125]
	v_mfma_f32_16x16x32_bf16 v[110:113], v[148:151], v[194:197], v[110:113]
	v_mfma_f32_16x16x32_bf16 v[106:109], v[156:159], v[194:197], v[106:109]
	v_mfma_f32_16x16x32_bf16 v[94:97], v[148:151], v[202:205], v[94:97]
	v_mfma_f32_16x16x32_bf16 v[90:93], v[156:159], v[202:205], v[90:93]
	v_mfma_f32_16x16x32_bf16 v[78:81], v[148:151], v[210:213], v[78:81]
	v_mfma_f32_16x16x32_bf16 v[74:77], v[156:159], v[210:213], v[74:77]
	v_mfma_f32_16x16x32_bf16 v[126:129], v[152:155], v[190:193], v[126:129]
	v_mfma_f32_16x16x32_bf16 v[122:125], v[160:163], v[190:193], v[122:125]
	v_mfma_f32_16x16x32_bf16 v[110:113], v[152:155], v[198:201], v[110:113]
	v_mfma_f32_16x16x32_bf16 v[106:109], v[160:163], v[198:201], v[106:109]
	v_mfma_f32_16x16x32_bf16 v[94:97], v[152:155], v[206:209], v[94:97]
	v_mfma_f32_16x16x32_bf16 v[90:93], v[160:163], v[206:209], v[90:93]
	v_mfma_f32_16x16x32_bf16 v[78:81], v[152:155], v[214:217], v[78:81]
	v_mfma_f32_16x16x32_bf16 v[74:77], v[160:163], v[214:217], v[74:77]
	v_mfma_f32_16x16x32_bf16 v[118:121], v[164:167], v[186:189], v[118:121]
	v_mfma_f32_16x16x32_bf16 v[114:117], v[178:181], v[186:189], v[114:117]
	v_mfma_f32_16x16x32_bf16 v[102:105], v[164:167], v[194:197], v[102:105]
	v_mfma_f32_16x16x32_bf16 v[98:101], v[178:181], v[194:197], v[98:101]
	v_mfma_f32_16x16x32_bf16 v[86:89], v[164:167], v[202:205], v[86:89]
	v_mfma_f32_16x16x32_bf16 v[82:85], v[178:181], v[202:205], v[82:85]
	v_mfma_f32_16x16x32_bf16 v[70:73], v[164:167], v[210:213], v[70:73]
	v_mfma_f32_16x16x32_bf16 v[66:69], v[178:181], v[210:213], v[66:69]
	v_mfma_f32_16x16x32_bf16 v[118:121], v[174:177], v[190:193], v[118:121]
	v_mfma_f32_16x16x32_bf16 v[114:117], v[182:185], v[190:193], v[114:117]
	v_mfma_f32_16x16x32_bf16 v[102:105], v[174:177], v[198:201], v[102:105]
	v_mfma_f32_16x16x32_bf16 v[98:101], v[182:185], v[198:201], v[98:101]
	v_mfma_f32_16x16x32_bf16 v[86:89], v[174:177], v[206:209], v[86:89]
	v_mfma_f32_16x16x32_bf16 v[82:85], v[182:185], v[206:209], v[82:85]
	v_mfma_f32_16x16x32_bf16 v[70:73], v[174:177], v[214:217], v[70:73]
	v_mfma_f32_16x16x32_bf16 v[66:69], v[182:185], v[214:217], v[66:69]
	s_setprio 0
	s_barrier
	ds_read_b128 v[186:189], v144 offset:49152
	ds_read_b128 v[190:193], v144 offset:50176
	ds_read_b128 v[194:197], v144 offset:51200
	ds_read_b128 v[198:201], v144 offset:52224
	ds_read_b128 v[202:205], v144 offset:53248
	ds_read_b128 v[206:209], v144 offset:54272
	ds_read_b128 v[210:213], v144 offset:55296
	ds_read_b128 v[214:217], v144 offset:56320
	s_add_u32 s22, s56, 0x80
	s_addc_u32 s23, s57, 0
	s_mov_b32 s58, m0
	s_mov_b32 m0, s61
	s_nop 2
	global_load_lds_dwordx4 v137, s[22:23]
	s_mov_b32 m0, s58
	s_nop 0
	s_mov_b32 s58, m0
	s_mov_b32 m0, s62
	s_nop 2
	global_load_lds_dwordx4 v139, s[22:23]
	s_mov_b32 m0, s58
	s_add_u32 s22, s56, 0x40080
	s_addc_u32 s23, s57, 0
	s_mov_b32 s56, m0
	s_mov_b32 m0, s65
	s_nop 2
	global_load_lds_dwordx4 v137, s[22:23]
	s_mov_b32 m0, s56
	s_nop 0
	s_mov_b32 s56, m0
	s_mov_b32 m0, s66
	s_nop 2
	global_load_lds_dwordx4 v139, s[22:23]
	s_mov_b32 m0, s56
	s_mov_b32 s22, m0
	s_mov_b32 m0, s63
	s_nop 2
	global_load_lds_dwordx4 v136, s[54:55]
	s_mov_b32 m0, s22
	s_nop 0
	s_mov_b32 s22, m0
	s_mov_b32 m0, s64
	s_nop 2
	global_load_lds_dwordx4 v138, s[54:55]
	s_mov_b32 m0, s22
	s_waitcnt vmcnt(8) lgkmcnt(0)
	s_barrier
	s_setprio 1
	v_mfma_f32_16x16x32_bf16 v[62:65], v[148:151], v[186:189], v[62:65]
	v_mfma_f32_16x16x32_bf16 v[58:61], v[156:159], v[186:189], v[58:61]
	v_mfma_f32_16x16x32_bf16 v[46:49], v[148:151], v[194:197], v[46:49]
	v_mfma_f32_16x16x32_bf16 v[42:45], v[156:159], v[194:197], v[42:45]
	v_mfma_f32_16x16x32_bf16 v[30:33], v[148:151], v[202:205], v[30:33]
	v_mfma_f32_16x16x32_bf16 v[26:29], v[156:159], v[202:205], v[26:29]
	v_mfma_f32_16x16x32_bf16 v[14:17], v[148:151], v[210:213], v[14:17]
	v_mfma_f32_16x16x32_bf16 v[10:13], v[156:159], v[210:213], v[10:13]
	v_mfma_f32_16x16x32_bf16 v[62:65], v[152:155], v[190:193], v[62:65]
	v_mfma_f32_16x16x32_bf16 v[58:61], v[160:163], v[190:193], v[58:61]
	v_mfma_f32_16x16x32_bf16 v[46:49], v[152:155], v[198:201], v[46:49]
	v_mfma_f32_16x16x32_bf16 v[42:45], v[160:163], v[198:201], v[42:45]
	v_mfma_f32_16x16x32_bf16 v[30:33], v[152:155], v[206:209], v[30:33]
	v_mfma_f32_16x16x32_bf16 v[26:29], v[160:163], v[206:209], v[26:29]
	v_mfma_f32_16x16x32_bf16 v[14:17], v[152:155], v[214:217], v[14:17]
	v_mfma_f32_16x16x32_bf16 v[10:13], v[160:163], v[214:217], v[10:13]
	v_mfma_f32_16x16x32_bf16 v[54:57], v[164:167], v[186:189], v[54:57]
	v_mfma_f32_16x16x32_bf16 v[50:53], v[178:181], v[186:189], v[50:53]
	v_mfma_f32_16x16x32_bf16 v[38:41], v[164:167], v[194:197], v[38:41]
	v_mfma_f32_16x16x32_bf16 v[34:37], v[178:181], v[194:197], v[34:37]
	v_mfma_f32_16x16x32_bf16 v[22:25], v[164:167], v[202:205], v[22:25]
	v_mfma_f32_16x16x32_bf16 v[18:21], v[178:181], v[202:205], v[18:21]
	v_mfma_f32_16x16x32_bf16 v[6:9], v[164:167], v[210:213], v[6:9]
	v_mfma_f32_16x16x32_bf16 v[2:5], v[178:181], v[210:213], v[2:5]
	v_mfma_f32_16x16x32_bf16 v[54:57], v[174:177], v[190:193], v[54:57]
	v_mfma_f32_16x16x32_bf16 v[50:53], v[182:185], v[190:193], v[50:53]
	v_mfma_f32_16x16x32_bf16 v[38:41], v[174:177], v[198:201], v[38:41]
	v_mfma_f32_16x16x32_bf16 v[34:37], v[182:185], v[198:201], v[34:37]
	v_mfma_f32_16x16x32_bf16 v[22:25], v[174:177], v[206:209], v[22:25]
	v_mfma_f32_16x16x32_bf16 v[18:21], v[182:185], v[206:209], v[18:21]
	v_mfma_f32_16x16x32_bf16 v[6:9], v[174:177], v[214:217], v[6:9]
	v_mfma_f32_16x16x32_bf16 v[2:5], v[182:185], v[214:217], v[2:5]
	s_setprio 0
	s_barrier
	s_add_i32 s82, s82, 2
	s_add_u32 s80, s80, 0x100
	s_addc_u32 s81, s81, 0
	s_cmp_gt_u32 s82, 13
	s_mov_b64 s[22:23], s[40:41]
	s_cbranch_scc0 .LBB0_143
	s_and_b64 vcc, exec, s[10:11]
	s_cbranch_vccz .LBB0_146
	s_barrier

.Lpeel170:
	ds_read_b128 v[142:145], v136
	ds_read_b128 v[146:149], v136 offset:1024
	ds_read_b128 v[150:153], v136 offset:2048
	ds_read_b128 v[154:157], v136 offset:3072
	ds_read_b128 v[158:161], v137
	ds_read_b128 v[162:165], v137 offset:1024
	ds_read_b128 v[166:169], v137 offset:2048
	ds_read_b128 v[174:177], v137 offset:3072
	s_add_u32 s14, s12, 0x100
	s_addc_u32 s15, s13, 0
	s_cmp_eq_u32 s56, 12
	s_cselect_b32 s20, s10, s14
	s_cselect_b32 s21, s11, s15
	s_cselect_b32 s18, s8, s54
	s_cselect_b32 s19, s9, s55
	s_add_u32 s16, s20, 0x80
	s_addc_u32 s17, s21, 0
	ds_read_b128 v[178:181], v138
	ds_read_b128 v[182:185], v138 offset:1024
	ds_read_b128 v[186:189], v138 offset:2048
	ds_read_b128 v[190:193], v138 offset:3072
	ds_read_b128 v[194:197], v138 offset:4096
	ds_read_b128 v[198:201], v138 offset:5120
	ds_read_b128 v[202:205], v138 offset:6144
	ds_read_b128 v[206:209], v138 offset:7168
	s_add_u32 s12, s12, 0x40080
	s_addc_u32 s13, s13, 0
	s_mov_b32 s57, m0
	s_mov_b32 m0, s52
	s_nop 2
	global_load_lds_dwordx4 v132, s[12:13]
	s_mov_b32 m0, s57
	s_nop 0
	s_mov_b32 s57, m0
	s_mov_b32 m0, s53
	s_nop 2
	global_load_lds_dwordx4 v134, s[12:13]
	s_mov_b32 m0, s57
	s_waitcnt vmcnt(8) lgkmcnt(0)
	s_barrier
	s_setprio 1
	v_mfma_f32_16x16x32_bf16 v[126:129], v[142:145], v[178:181], 0
	v_mfma_f32_16x16x32_bf16 v[122:125], v[150:153], v[178:181], 0
	v_mfma_f32_16x16x32_bf16 v[110:113], v[142:145], v[186:189], 0
	v_mfma_f32_16x16x32_bf16 v[106:109], v[150:153], v[186:189], 0
	v_mfma_f32_16x16x32_bf16 v[94:97], v[142:145], v[194:197], 0
	v_mfma_f32_16x16x32_bf16 v[90:93], v[150:153], v[194:197], 0
	v_mfma_f32_16x16x32_bf16 v[78:81], v[142:145], v[202:205], 0
	v_mfma_f32_16x16x32_bf16 v[74:77], v[150:153], v[202:205], 0
	v_mfma_f32_16x16x32_bf16 v[126:129], v[146:149], v[182:185], v[126:129]
	v_mfma_f32_16x16x32_bf16 v[122:125], v[154:157], v[182:185], v[122:125]
	v_mfma_f32_16x16x32_bf16 v[110:113], v[146:149], v[190:193], v[110:113]
	v_mfma_f32_16x16x32_bf16 v[106:109], v[154:157], v[190:193], v[106:109]
	v_mfma_f32_16x16x32_bf16 v[94:97], v[146:149], v[198:201], v[94:97]
	v_mfma_f32_16x16x32_bf16 v[90:93], v[154:157], v[198:201], v[90:93]
	v_mfma_f32_16x16x32_bf16 v[78:81], v[146:149], v[206:209], v[78:81]
	v_mfma_f32_16x16x32_bf16 v[74:77], v[154:157], v[206:209], v[74:77]
	v_mfma_f32_16x16x32_bf16 v[118:121], v[158:161], v[178:181], 0
	v_mfma_f32_16x16x32_bf16 v[114:117], v[166:169], v[178:181], 0
	v_mfma_f32_16x16x32_bf16 v[102:105], v[158:161], v[186:189], 0
	v_mfma_f32_16x16x32_bf16 v[98:101], v[166:169], v[186:189], 0
	v_mfma_f32_16x16x32_bf16 v[86:89], v[158:161], v[194:197], 0
	v_mfma_f32_16x16x32_bf16 v[82:85], v[166:169], v[194:197], 0
	v_mfma_f32_16x16x32_bf16 v[70:73], v[158:161], v[202:205], 0
	v_mfma_f32_16x16x32_bf16 v[66:69], v[166:169], v[202:205], 0
	v_mfma_f32_16x16x32_bf16 v[118:121], v[162:165], v[182:185], v[118:121]
	v_mfma_f32_16x16x32_bf16 v[114:117], v[174:177], v[182:185], v[114:117]
	v_mfma_f32_16x16x32_bf16 v[102:105], v[162:165], v[190:193], v[102:105]
	v_mfma_f32_16x16x32_bf16 v[98:101], v[174:177], v[190:193], v[98:101]
	v_mfma_f32_16x16x32_bf16 v[86:89], v[162:165], v[198:201], v[86:89]
	v_mfma_f32_16x16x32_bf16 v[82:85], v[174:177], v[198:201], v[82:85]
	v_mfma_f32_16x16x32_bf16 v[70:73], v[162:165], v[206:209], v[70:73]
	v_mfma_f32_16x16x32_bf16 v[66:69], v[174:177], v[206:209], v[66:69]
	s_setprio 0
	s_barrier
	ds_read_b128 v[178:181], v138 offset:16384
	ds_read_b128 v[182:185], v138 offset:17408
	ds_read_b128 v[186:189], v138 offset:18432
	ds_read_b128 v[190:193], v138 offset:19456
	ds_read_b128 v[194:197], v138 offset:20480
	ds_read_b128 v[198:201], v138 offset:21504
	ds_read_b128 v[202:205], v138 offset:22528
	ds_read_b128 v[206:209], v138 offset:23552
	s_mov_b32 s12, m0
	s_mov_b32 m0, s24
	s_nop 2
	global_load_lds_dwordx4 v133, s[18:19]
	s_mov_b32 m0, s12
	s_nop 0
	s_mov_b32 s12, m0
	s_mov_b32 m0, s25
	s_nop 2
	global_load_lds_dwordx4 v135, s[18:19]
	s_mov_b32 m0, s12
	s_add_u32 s12, s18, 0x40000
	s_addc_u32 s13, s19, 0
	s_mov_b32 s57, m0
	s_mov_b32 m0, s28
	s_nop 2
	global_load_lds_dwordx4 v133, s[12:13]
	s_mov_b32 m0, s57
	s_nop 0
	s_mov_b32 s57, m0
	s_mov_b32 m0, s29
	s_nop 2
	global_load_lds_dwordx4 v135, s[12:13]
	s_mov_b32 m0, s57
	s_mov_b32 s12, m0
	s_mov_b32 m0, s5
	s_nop 2
	global_load_lds_dwordx4 v132, s[20:21]
	s_mov_b32 m0, s12
	s_nop 0
	s_mov_b32 s12, m0
	s_mov_b32 m0, s30
	s_nop 2
	global_load_lds_dwordx4 v134, s[20:21]
	s_mov_b32 m0, s12
	s_waitcnt vmcnt(8) lgkmcnt(0)
	s_barrier
	s_setprio 1
	v_mfma_f32_16x16x32_bf16 v[62:65], v[142:145], v[178:181], 0
	v_mfma_f32_16x16x32_bf16 v[58:61], v[150:153], v[178:181], 0
	v_mfma_f32_16x16x32_bf16 v[46:49], v[142:145], v[186:189], 0
	v_mfma_f32_16x16x32_bf16 v[42:45], v[150:153], v[186:189], 0
	v_mfma_f32_16x16x32_bf16 v[30:33], v[142:145], v[194:197], 0
	v_mfma_f32_16x16x32_bf16 v[26:29], v[150:153], v[194:197], 0
	v_mfma_f32_16x16x32_bf16 v[14:17], v[142:145], v[202:205], 0
	v_mfma_f32_16x16x32_bf16 v[10:13], v[150:153], v[202:205], 0
	v_mfma_f32_16x16x32_bf16 v[62:65], v[146:149], v[182:185], v[62:65]
	v_mfma_f32_16x16x32_bf16 v[58:61], v[154:157], v[182:185], v[58:61]
	v_mfma_f32_16x16x32_bf16 v[46:49], v[146:149], v[190:193], v[46:49]
	v_mfma_f32_16x16x32_bf16 v[42:45], v[154:157], v[190:193], v[42:45]
	v_mfma_f32_16x16x32_bf16 v[30:33], v[146:149], v[198:201], v[30:33]
	v_mfma_f32_16x16x32_bf16 v[26:29], v[154:157], v[198:201], v[26:29]
	v_mfma_f32_16x16x32_bf16 v[14:17], v[146:149], v[206:209], v[14:17]
	v_mfma_f32_16x16x32_bf16 v[10:13], v[154:157], v[206:209], v[10:13]
	v_mfma_f32_16x16x32_bf16 v[54:57], v[158:161], v[178:181], 0
	v_mfma_f32_16x16x32_bf16 v[50:53], v[166:169], v[178:181], 0
	v_mfma_f32_16x16x32_bf16 v[38:41], v[158:161], v[186:189], 0
	v_mfma_f32_16x16x32_bf16 v[34:37], v[166:169], v[186:189], 0
	v_mfma_f32_16x16x32_bf16 v[22:25], v[158:161], v[194:197], 0
	v_mfma_f32_16x16x32_bf16 v[18:21], v[166:169], v[194:197], 0
	v_mfma_f32_16x16x32_bf16 v[6:9], v[158:161], v[202:205], 0
	v_mfma_f32_16x16x32_bf16 v[2:5], v[166:169], v[202:205], 0
	v_mfma_f32_16x16x32_bf16 v[54:57], v[162:165], v[182:185], v[54:57]
	v_mfma_f32_16x16x32_bf16 v[50:53], v[174:177], v[182:185], v[50:53]
	v_mfma_f32_16x16x32_bf16 v[38:41], v[162:165], v[190:193], v[38:41]
	v_mfma_f32_16x16x32_bf16 v[34:37], v[174:177], v[190:193], v[34:37]
	v_mfma_f32_16x16x32_bf16 v[22:25], v[162:165], v[198:201], v[22:25]
	v_mfma_f32_16x16x32_bf16 v[18:21], v[174:177], v[198:201], v[18:21]
	v_mfma_f32_16x16x32_bf16 v[6:9], v[162:165], v[206:209], v[6:9]
	v_mfma_f32_16x16x32_bf16 v[2:5], v[174:177], v[206:209], v[2:5]
	s_setprio 0
	s_barrier
	s_branch .Lmid170
.LBB0_170:
	ds_read_b128 v[142:145], v136
	ds_read_b128 v[146:149], v136 offset:1024
	ds_read_b128 v[150:153], v136 offset:2048
	ds_read_b128 v[154:157], v136 offset:3072
	ds_read_b128 v[158:161], v137
	ds_read_b128 v[162:165], v137 offset:1024
	ds_read_b128 v[166:169], v137 offset:2048
	ds_read_b128 v[174:177], v137 offset:3072
	s_add_u32 s14, s12, 0x100
	s_addc_u32 s15, s13, 0
	s_cmp_eq_u32 s56, 12
	s_cselect_b32 s20, s10, s14
	s_cselect_b32 s21, s11, s15
	s_cselect_b32 s18, s8, s54
	s_cselect_b32 s19, s9, s55
	s_add_u32 s16, s20, 0x80
	s_addc_u32 s17, s21, 0
	ds_read_b128 v[178:181], v138
	ds_read_b128 v[182:185], v138 offset:1024
	ds_read_b128 v[186:189], v138 offset:2048
	ds_read_b128 v[190:193], v138 offset:3072
	ds_read_b128 v[194:197], v138 offset:4096
	ds_read_b128 v[198:201], v138 offset:5120
	ds_read_b128 v[202:205], v138 offset:6144
	ds_read_b128 v[206:209], v138 offset:7168
	s_add_u32 s12, s12, 0x40080
	s_addc_u32 s13, s13, 0
	s_mov_b32 s57, m0
	s_mov_b32 m0, s52
	s_nop 2
	global_load_lds_dwordx4 v132, s[12:13]
	s_mov_b32 m0, s57
	s_nop 0
	s_mov_b32 s57, m0
	s_mov_b32 m0, s53
	s_nop 2
	global_load_lds_dwordx4 v134, s[12:13]
	s_mov_b32 m0, s57
	s_waitcnt vmcnt(8) lgkmcnt(0)
	s_barrier
	s_setprio 1
	v_mfma_f32_16x16x32_bf16 v[126:129], v[142:145], v[178:181], v[126:129]
	v_mfma_f32_16x16x32_bf16 v[122:125], v[150:153], v[178:181], v[122:125]
	v_mfma_f32_16x16x32_bf16 v[110:113], v[142:145], v[186:189], v[110:113]
	v_mfma_f32_16x16x32_bf16 v[106:109], v[150:153], v[186:189], v[106:109]
	v_mfma_f32_16x16x32_bf16 v[94:97], v[142:145], v[194:197], v[94:97]
	v_mfma_f32_16x16x32_bf16 v[90:93], v[150:153], v[194:197], v[90:93]
	v_mfma_f32_16x16x32_bf16 v[78:81], v[142:145], v[202:205], v[78:81]
	v_mfma_f32_16x16x32_bf16 v[74:77], v[150:153], v[202:205], v[74:77]
	v_mfma_f32_16x16x32_bf16 v[126:129], v[146:149], v[182:185], v[126:129]
	v_mfma_f32_16x16x32_bf16 v[122:125], v[154:157], v[182:185], v[122:125]
	v_mfma_f32_16x16x32_bf16 v[110:113], v[146:149], v[190:193], v[110:113]
	v_mfma_f32_16x16x32_bf16 v[106:109], v[154:157], v[190:193], v[106:109]
	v_mfma_f32_16x16x32_bf16 v[94:97], v[146:149], v[198:201], v[94:97]
	v_mfma_f32_16x16x32_bf16 v[90:93], v[154:157], v[198:201], v[90:93]
	v_mfma_f32_16x16x32_bf16 v[78:81], v[146:149], v[206:209], v[78:81]
	v_mfma_f32_16x16x32_bf16 v[74:77], v[154:157], v[206:209], v[74:77]
	v_mfma_f32_16x16x32_bf16 v[118:121], v[158:161], v[178:181], v[118:121]
	v_mfma_f32_16x16x32_bf16 v[114:117], v[166:169], v[178:181], v[114:117]
	v_mfma_f32_16x16x32_bf16 v[102:105], v[158:161], v[186:189], v[102:105]
	v_mfma_f32_16x16x32_bf16 v[98:101], v[166:169], v[186:189], v[98:101]
	v_mfma_f32_16x16x32_bf16 v[86:89], v[158:161], v[194:197], v[86:89]
	v_mfma_f32_16x16x32_bf16 v[82:85], v[166:169], v[194:197], v[82:85]
	v_mfma_f32_16x16x32_bf16 v[70:73], v[158:161], v[202:205], v[70:73]
	v_mfma_f32_16x16x32_bf16 v[66:69], v[166:169], v[202:205], v[66:69]
	v_mfma_f32_16x16x32_bf16 v[118:121], v[162:165], v[182:185], v[118:121]
	v_mfma_f32_16x16x32_bf16 v[114:117], v[174:177], v[182:185], v[114:117]
	v_mfma_f32_16x16x32_bf16 v[102:105], v[162:165], v[190:193], v[102:105]
	v_mfma_f32_16x16x32_bf16 v[98:101], v[174:177], v[190:193], v[98:101]
	v_mfma_f32_16x16x32_bf16 v[86:89], v[162:165], v[198:201], v[86:89]
	v_mfma_f32_16x16x32_bf16 v[82:85], v[174:177], v[198:201], v[82:85]
	v_mfma_f32_16x16x32_bf16 v[70:73], v[162:165], v[206:209], v[70:73]
	v_mfma_f32_16x16x32_bf16 v[66:69], v[174:177], v[206:209], v[66:69]
	s_setprio 0
	s_barrier
	ds_read_b128 v[178:181], v138 offset:16384
	ds_read_b128 v[182:185], v138 offset:17408
	ds_read_b128 v[186:189], v138 offset:18432
	ds_read_b128 v[190:193], v138 offset:19456
	ds_read_b128 v[194:197], v138 offset:20480
	ds_read_b128 v[198:201], v138 offset:21504
	ds_read_b128 v[202:205], v138 offset:22528
	ds_read_b128 v[206:209], v138 offset:23552
	s_mov_b32 s12, m0
	s_mov_b32 m0, s24
	s_nop 2
	global_load_lds_dwordx4 v133, s[18:19]
	s_mov_b32 m0, s12
	s_nop 0
	s_mov_b32 s12, m0
	s_mov_b32 m0, s25
	s_nop 2
	global_load_lds_dwordx4 v135, s[18:19]
	s_mov_b32 m0, s12
	s_add_u32 s12, s18, 0x40000
	s_addc_u32 s13, s19, 0
	s_mov_b32 s57, m0
	s_mov_b32 m0, s28
	s_nop 2
	global_load_lds_dwordx4 v133, s[12:13]
	s_mov_b32 m0, s57
	s_nop 0
	s_mov_b32 s57, m0
	s_mov_b32 m0, s29
	s_nop 2
	global_load_lds_dwordx4 v135, s[12:13]
	s_mov_b32 m0, s57
	s_mov_b32 s12, m0
	s_mov_b32 m0, s5
	s_nop 2
	global_load_lds_dwordx4 v132, s[20:21]
	s_mov_b32 m0, s12
	s_nop 0
	s_mov_b32 s12, m0
	s_mov_b32 m0, s30
	s_nop 2
	global_load_lds_dwordx4 v134, s[20:21]
	s_mov_b32 m0, s12
	s_waitcnt vmcnt(8) lgkmcnt(0)
	s_barrier
	s_setprio 1
	v_mfma_f32_16x16x32_bf16 v[62:65], v[142:145], v[178:181], v[62:65]
	v_mfma_f32_16x16x32_bf16 v[58:61], v[150:153], v[178:181], v[58:61]
	v_mfma_f32_16x16x32_bf16 v[46:49], v[142:145], v[186:189], v[46:49]
	v_mfma_f32_16x16x32_bf16 v[42:45], v[150:153], v[186:189], v[42:45]
	v_mfma_f32_16x16x32_bf16 v[30:33], v[142:145], v[194:197], v[30:33]
	v_mfma_f32_16x16x32_bf16 v[26:29], v[150:153], v[194:197], v[26:29]
	v_mfma_f32_16x16x32_bf16 v[14:17], v[142:145], v[202:205], v[14:17]
	v_mfma_f32_16x16x32_bf16 v[10:13], v[150:153], v[202:205], v[10:13]
	v_mfma_f32_16x16x32_bf16 v[62:65], v[146:149], v[182:185], v[62:65]
	v_mfma_f32_16x16x32_bf16 v[58:61], v[154:157], v[182:185], v[58:61]
	v_mfma_f32_16x16x32_bf16 v[46:49], v[146:149], v[190:193], v[46:49]
	v_mfma_f32_16x16x32_bf16 v[42:45], v[154:157], v[190:193], v[42:45]
	v_mfma_f32_16x16x32_bf16 v[30:33], v[146:149], v[198:201], v[30:33]
	v_mfma_f32_16x16x32_bf16 v[26:29], v[154:157], v[198:201], v[26:29]
	v_mfma_f32_16x16x32_bf16 v[14:17], v[146:149], v[206:209], v[14:17]
	v_mfma_f32_16x16x32_bf16 v[10:13], v[154:157], v[206:209], v[10:13]
	v_mfma_f32_16x16x32_bf16 v[54:57], v[158:161], v[178:181], v[54:57]
	v_mfma_f32_16x16x32_bf16 v[50:53], v[166:169], v[178:181], v[50:53]
	v_mfma_f32_16x16x32_bf16 v[38:41], v[158:161], v[186:189], v[38:41]
	v_mfma_f32_16x16x32_bf16 v[34:37], v[166:169], v[186:189], v[34:37]
	v_mfma_f32_16x16x32_bf16 v[22:25], v[158:161], v[194:197], v[22:25]
	v_mfma_f32_16x16x32_bf16 v[18:21], v[166:169], v[194:197], v[18:21]
	v_mfma_f32_16x16x32_bf16 v[6:9], v[158:161], v[202:205], v[6:9]
	v_mfma_f32_16x16x32_bf16 v[2:5], v[166:169], v[202:205], v[2:5]
	v_mfma_f32_16x16x32_bf16 v[54:57], v[162:165], v[182:185], v[54:57]
	v_mfma_f32_16x16x32_bf16 v[50:53], v[174:177], v[182:185], v[50:53]
	v_mfma_f32_16x16x32_bf16 v[38:41], v[162:165], v[190:193], v[38:41]
	v_mfma_f32_16x16x32_bf16 v[34:37], v[174:177], v[190:193], v[34:37]
	v_mfma_f32_16x16x32_bf16 v[22:25], v[162:165], v[198:201], v[22:25]
	v_mfma_f32_16x16x32_bf16 v[18:21], v[174:177], v[198:201], v[18:21]
	v_mfma_f32_16x16x32_bf16 v[6:9], v[162:165], v[206:209], v[6:9]
	v_mfma_f32_16x16x32_bf16 v[2:5], v[174:177], v[206:209], v[2:5]
	s_setprio 0
	s_barrier
.Lmid170:
	ds_read_b128 v[142:145], v139
	ds_read_b128 v[146:149], v139 offset:1024
	ds_read_b128 v[150:153], v139 offset:2048
	ds_read_b128 v[154:157], v139 offset:3072
	ds_read_b128 v[158:161], v140
	ds_read_b128 v[162:165], v140 offset:1024
	ds_read_b128 v[166:169], v140 offset:2048
	ds_read_b128 v[174:177], v140 offset:3072
	ds_read_b128 v[178:181], v138 offset:32768
	ds_read_b128 v[182:185], v138 offset:33792
	ds_read_b128 v[186:189], v138 offset:34816
	ds_read_b128 v[190:193], v138 offset:35840
	ds_read_b128 v[194:197], v138 offset:36864
	ds_read_b128 v[198:201], v138 offset:37888
	ds_read_b128 v[202:205], v138 offset:38912
	ds_read_b128 v[206:209], v138 offset:39936
	s_add_u32 s12, s20, 0x40000
	s_addc_u32 s13, s21, 0
	s_mov_b32 s20, m0
	s_mov_b32 m0, s31
	s_nop 2
	global_load_lds_dwordx4 v132, s[12:13]
	s_mov_b32 m0, s20
	s_nop 0
	s_mov_b32 s20, m0
	s_mov_b32 m0, s33
	s_nop 2
	global_load_lds_dwordx4 v134, s[12:13]
	s_mov_b32 m0, s20
	s_waitcnt vmcnt(8) lgkmcnt(0)
	s_barrier
	s_setprio 1
	v_mfma_f32_16x16x32_bf16 v[126:129], v[142:145], v[178:181], v[126:129]
	v_mfma_f32_16x16x32_bf16 v[122:125], v[150:153], v[178:181], v[122:125]
	v_mfma_f32_16x16x32_bf16 v[110:113], v[142:145], v[186:189], v[110:113]
	v_mfma_f32_16x16x32_bf16 v[106:109], v[150:153], v[186:189], v[106:109]
	v_mfma_f32_16x16x32_bf16 v[94:97], v[142:145], v[194:197], v[94:97]
	v_mfma_f32_16x16x32_bf16 v[90:93], v[150:153], v[194:197], v[90:93]
	v_mfma_f32_16x16x32_bf16 v[78:81], v[142:145], v[202:205], v[78:81]
	v_mfma_f32_16x16x32_bf16 v[74:77], v[150:153], v[202:205], v[74:77]
	v_mfma_f32_16x16x32_bf16 v[126:129], v[146:149], v[182:185], v[126:129]
	v_mfma_f32_16x16x32_bf16 v[122:125], v[154:157], v[182:185], v[122:125]
	v_mfma_f32_16x16x32_bf16 v[110:113], v[146:149], v[190:193], v[110:113]
	v_mfma_f32_16x16x32_bf16 v[106:109], v[154:157], v[190:193], v[106:109]
	v_mfma_f32_16x16x32_bf16 v[94:97], v[146:149], v[198:201], v[94:97]
	v_mfma_f32_16x16x32_bf16 v[90:93], v[154:157], v[198:201], v[90:93]
	v_mfma_f32_16x16x32_bf16 v[78:81], v[146:149], v[206:209], v[78:81]
	v_mfma_f32_16x16x32_bf16 v[74:77], v[154:157], v[206:209], v[74:77]
	v_mfma_f32_16x16x32_bf16 v[118:121], v[158:161], v[178:181], v[118:121]
	v_mfma_f32_16x16x32_bf16 v[114:117], v[166:169], v[178:181], v[114:117]
	v_mfma_f32_16x16x32_bf16 v[102:105], v[158:161], v[186:189], v[102:105]
	v_mfma_f32_16x16x32_bf16 v[98:101], v[166:169], v[186:189], v[98:101]
	v_mfma_f32_16x16x32_bf16 v[86:89], v[158:161], v[194:197], v[86:89]
	v_mfma_f32_16x16x32_bf16 v[82:85], v[166:169], v[194:197], v[82:85]
	v_mfma_f32_16x16x32_bf16 v[70:73], v[158:161], v[202:205], v[70:73]
	v_mfma_f32_16x16x32_bf16 v[66:69], v[166:169], v[202:205], v[66:69]
	v_mfma_f32_16x16x32_bf16 v[118:121], v[162:165], v[182:185], v[118:121]
	v_mfma_f32_16x16x32_bf16 v[114:117], v[174:177], v[182:185], v[114:117]
	v_mfma_f32_16x16x32_bf16 v[102:105], v[162:165], v[190:193], v[102:105]
	v_mfma_f32_16x16x32_bf16 v[98:101], v[174:177], v[190:193], v[98:101]
	v_mfma_f32_16x16x32_bf16 v[86:89], v[162:165], v[198:201], v[86:89]
	v_mfma_f32_16x16x32_bf16 v[82:85], v[174:177], v[198:201], v[82:85]
	v_mfma_f32_16x16x32_bf16 v[70:73], v[162:165], v[206:209], v[70:73]
	v_mfma_f32_16x16x32_bf16 v[66:69], v[174:177], v[206:209], v[66:69]
	s_setprio 0
	s_barrier
	ds_read_b128 v[178:181], v138 offset:49152
	ds_read_b128 v[182:185], v138 offset:50176
	ds_read_b128 v[186:189], v138 offset:51200
	ds_read_b128 v[190:193], v138 offset:52224
	ds_read_b128 v[194:197], v138 offset:53248
	ds_read_b128 v[198:201], v138 offset:54272
	ds_read_b128 v[202:205], v138 offset:55296
	ds_read_b128 v[206:209], v138 offset:56320
	s_add_u32 s12, s18, 0x80
	s_addc_u32 s13, s19, 0
	s_mov_b32 s20, m0
	s_mov_b32 m0, s34
	s_nop 2
	global_load_lds_dwordx4 v133, s[12:13]
	s_mov_b32 m0, s20
	s_nop 0
	s_mov_b32 s20, m0
	s_mov_b32 m0, s35
	s_nop 2
	global_load_lds_dwordx4 v135, s[12:13]
	s_mov_b32 m0, s20
	s_add_u32 s12, s18, 0x40080
	s_addc_u32 s13, s19, 0
	s_mov_b32 s18, m0
	s_mov_b32 m0, s40
	s_nop 2
	global_load_lds_dwordx4 v133, s[12:13]
	s_mov_b32 m0, s18
	s_nop 0
	s_mov_b32 s18, m0
	s_mov_b32 m0, s41
	s_nop 2
	global_load_lds_dwordx4 v135, s[12:13]
	s_mov_b32 m0, s18
	s_mov_b32 s12, m0
	s_mov_b32 m0, s36
	s_nop 2
	global_load_lds_dwordx4 v132, s[16:17]
	s_mov_b32 m0, s12
	s_nop 0
	s_mov_b32 s12, m0
	s_mov_b32 m0, s37
	s_nop 2
	global_load_lds_dwordx4 v134, s[16:17]
	s_mov_b32 m0, s12
	s_waitcnt vmcnt(8) lgkmcnt(0)
	s_barrier
	s_setprio 1
	v_mfma_f32_16x16x32_bf16 v[62:65], v[142:145], v[178:181], v[62:65]
	v_mfma_f32_16x16x32_bf16 v[58:61], v[150:153], v[178:181], v[58:61]
	v_mfma_f32_16x16x32_bf16 v[46:49], v[142:145], v[186:189], v[46:49]
	v_mfma_f32_16x16x32_bf16 v[42:45], v[150:153], v[186:189], v[42:45]
	v_mfma_f32_16x16x32_bf16 v[30:33], v[142:145], v[194:197], v[30:33]
	v_mfma_f32_16x16x32_bf16 v[26:29], v[150:153], v[194:197], v[26:29]
	v_mfma_f32_16x16x32_bf16 v[14:17], v[142:145], v[202:205], v[14:17]
	v_mfma_f32_16x16x32_bf16 v[10:13], v[150:153], v[202:205], v[10:13]
	v_mfma_f32_16x16x32_bf16 v[62:65], v[146:149], v[182:185], v[62:65]
	v_mfma_f32_16x16x32_bf16 v[58:61], v[154:157], v[182:185], v[58:61]
	v_mfma_f32_16x16x32_bf16 v[46:49], v[146:149], v[190:193], v[46:49]
	v_mfma_f32_16x16x32_bf16 v[42:45], v[154:157], v[190:193], v[42:45]
	v_mfma_f32_16x16x32_bf16 v[30:33], v[146:149], v[198:201], v[30:33]
	v_mfma_f32_16x16x32_bf16 v[26:29], v[154:157], v[198:201], v[26:29]
	v_mfma_f32_16x16x32_bf16 v[14:17], v[146:149], v[206:209], v[14:17]
	v_mfma_f32_16x16x32_bf16 v[10:13], v[154:157], v[206:209], v[10:13]
	v_mfma_f32_16x16x32_bf16 v[54:57], v[158:161], v[178:181], v[54:57]
	v_mfma_f32_16x16x32_bf16 v[50:53], v[166:169], v[178:181], v[50:53]
	v_mfma_f32_16x16x32_bf16 v[38:41], v[158:161], v[186:189], v[38:41]
	v_mfma_f32_16x16x32_bf16 v[34:37], v[166:169], v[186:189], v[34:37]
	v_mfma_f32_16x16x32_bf16 v[22:25], v[158:161], v[194:197], v[22:25]
	v_mfma_f32_16x16x32_bf16 v[18:21], v[166:169], v[194:197], v[18:21]
	v_mfma_f32_16x16x32_bf16 v[6:9], v[158:161], v[202:205], v[6:9]
	v_mfma_f32_16x16x32_bf16 v[2:5], v[166:169], v[202:205], v[2:5]
	v_mfma_f32_16x16x32_bf16 v[54:57], v[162:165], v[182:185], v[54:57]
	v_mfma_f32_16x16x32_bf16 v[50:53], v[174:177], v[182:185], v[50:53]
	v_mfma_f32_16x16x32_bf16 v[38:41], v[162:165], v[190:193], v[38:41]
	v_mfma_f32_16x16x32_bf16 v[34:37], v[174:177], v[190:193], v[34:37]
	v_mfma_f32_16x16x32_bf16 v[22:25], v[162:165], v[198:201], v[22:25]
	v_mfma_f32_16x16x32_bf16 v[18:21], v[174:177], v[198:201], v[18:21]
	v_mfma_f32_16x16x32_bf16 v[6:9], v[162:165], v[206:209], v[6:9]
	v_mfma_f32_16x16x32_bf16 v[2:5], v[174:177], v[206:209], v[2:5]
	s_setprio 0
	s_barrier
	s_add_i32 s56, s56, 2
	s_add_u32 s54, s54, 0x100
	s_addc_u32 s55, s55, 0
	s_cmp_gt_u32 s56, 13
	s_mov_b64 s[12:13], s[14:15]
	s_cbranch_scc0 .LBB0_170
	s_cmpk_lt_u32 s23, 0x100
	s_cbranch_scc0 .LBB0_173
	s_barrier

.LBB0_190:
	ds_read_b128 v[18:21], v174
	ds_read_b128 v[22:25], v174 offset:1024
	ds_read_b128 v[26:29], v174 offset:2048
	ds_read_b128 v[30:33], v174 offset:3072
	ds_read_b128 v[2:5], v175
	ds_read_b128 v[6:9], v175 offset:1024
	ds_read_b128 v[10:13], v175 offset:2048
	ds_read_b128 v[14:17], v175 offset:3072
	s_add_u32 s76, s78, 0x100
	s_addc_u32 s77, s79, 0
	s_cmp_eq_u32 s33, 4
	s_cselect_b32 s84, s59, s76
	s_cselect_b32 s85, s7, s77
	s_cselect_b32 s82, s67, vcc_lo
	s_cselect_b32 s83, s57, vcc_hi
	s_add_u32 s80, s84, 0x80
	s_addc_u32 s81, s85, 0
	ds_read_b128 v[180:183], v176
	ds_read_b128 v[184:187], v176 offset:1024
	ds_read_b128 v[188:191], v176 offset:2048
	ds_read_b128 v[192:195], v176 offset:3072
	ds_read_b128 v[196:199], v176 offset:4096
	ds_read_b128 v[200:203], v176 offset:5120
	ds_read_b128 v[204:207], v176 offset:6144
	ds_read_b128 v[208:211], v176 offset:7168
	s_add_u32 s78, s78, 0x20080
	s_addc_u32 s79, s79, 0
	s_mov_b32 s88, m0
	s_mov_b32 m0, s96
	s_nop 2
	global_load_lds_dwordx4 v166, s[78:79]
	s_mov_b32 m0, s88
	s_nop 0
	s_mov_b32 s88, m0
	s_mov_b32 m0, s92
	s_nop 2
	global_load_lds_dwordx4 v168, s[78:79]
	s_mov_b32 m0, s88
	s_waitcnt vmcnt(8) lgkmcnt(0)
	s_barrier
	s_setprio 1
	v_mfma_f32_16x16x128_f8f6f4 v[158:161], v[18:25], v[180:187], v[158:161]
	v_mfma_f32_16x16x128_f8f6f4 v[154:157], v[26:33], v[180:187], v[154:157]
	v_mfma_f32_16x16x128_f8f6f4 v[146:149], v[18:25], v[188:195], v[146:149]
	v_mfma_f32_16x16x128_f8f6f4 v[138:141], v[26:33], v[188:195], v[138:141]
	v_mfma_f32_16x16x128_f8f6f4 v[130:133], v[18:25], v[196:203], v[130:133]
	v_mfma_f32_16x16x128_f8f6f4 v[122:125], v[26:33], v[196:203], v[122:125]
	v_mfma_f32_16x16x128_f8f6f4 v[114:117], v[18:25], v[204:211], v[114:117]
	v_mfma_f32_16x16x128_f8f6f4 v[106:109], v[26:33], v[204:211], v[106:109]
	v_mfma_f32_16x16x128_f8f6f4 v[150:153], v[2:9], v[180:187], v[150:153]
	v_mfma_f32_16x16x128_f8f6f4 v[142:145], v[10:17], v[180:187], v[142:145]
	v_mfma_f32_16x16x128_f8f6f4 v[134:137], v[2:9], v[188:195], v[134:137]
	v_mfma_f32_16x16x128_f8f6f4 v[126:129], v[10:17], v[188:195], v[126:129]
	v_mfma_f32_16x16x128_f8f6f4 v[118:121], v[2:9], v[196:203], v[118:121]
	v_mfma_f32_16x16x128_f8f6f4 v[110:113], v[10:17], v[196:203], v[110:113]
	v_mfma_f32_16x16x128_f8f6f4 v[102:105], v[2:9], v[204:211], v[102:105]
	v_mfma_f32_16x16x128_f8f6f4 v[98:101], v[10:17], v[204:211], v[98:101]
	s_setprio 0
	s_barrier
	ds_read_b128 v[180:183], v176 offset:16384
	ds_read_b128 v[184:187], v176 offset:17408
	ds_read_b128 v[188:191], v176 offset:18432
	ds_read_b128 v[192:195], v176 offset:19456
	ds_read_b128 v[196:199], v176 offset:20480
	ds_read_b128 v[200:203], v176 offset:21504
	ds_read_b128 v[204:207], v176 offset:22528
	ds_read_b128 v[208:211], v176 offset:23552
	s_mov_b32 s78, m0
	s_mov_b32 m0, s36
	s_nop 2
	global_load_lds_dwordx4 v167, s[82:83]
	s_mov_b32 m0, s78
	s_nop 0
	s_mov_b32 s78, m0
	s_mov_b32 m0, s37
	s_nop 2
	global_load_lds_dwordx4 v169, s[82:83]
	s_mov_b32 m0, s78
	s_add_u32 s78, s82, 0x20000
	s_addc_u32 s79, s83, 0
	s_mov_b32 s88, m0
	s_mov_b32 m0, s55
	s_nop 2
	global_load_lds_dwordx4 v167, s[78:79]
	s_mov_b32 m0, s88
	s_nop 0
	s_mov_b32 s88, m0
	s_mov_b32 m0, s86
	s_nop 2
	global_load_lds_dwordx4 v169, s[78:79]
	s_mov_b32 m0, s88
	s_mov_b32 s78, m0
	s_mov_b32 m0, s35
	s_nop 2
	global_load_lds_dwordx4 v166, s[84:85]
	s_mov_b32 m0, s78
	s_nop 0
	s_mov_b32 s78, m0
	s_mov_b32 m0, s87
	s_nop 2
	global_load_lds_dwordx4 v168, s[84:85]
	s_mov_b32 m0, s78
	s_waitcnt vmcnt(8) lgkmcnt(0)
	s_barrier
	s_setprio 1
	v_mfma_f32_16x16x128_f8f6f4 v[94:97], v[18:25], v[180:187], v[94:97]
	v_mfma_f32_16x16x128_f8f6f4 v[90:93], v[26:33], v[180:187], v[90:93]
	v_mfma_f32_16x16x128_f8f6f4 v[82:85], v[18:25], v[188:195], v[82:85]
	v_mfma_f32_16x16x128_f8f6f4 v[74:77], v[26:33], v[188:195], v[74:77]
	v_mfma_f32_16x16x128_f8f6f4 v[66:69], v[18:25], v[196:203], v[66:69]
	v_mfma_f32_16x16x128_f8f6f4 v[58:61], v[26:33], v[196:203], v[58:61]
	v_mfma_f32_16x16x128_f8f6f4 v[50:53], v[18:25], v[204:211], v[50:53]
	v_mfma_f32_16x16x128_f8f6f4 v[42:45], v[26:33], v[204:211], v[42:45]
	v_mfma_f32_16x16x128_f8f6f4 v[86:89], v[2:9], v[180:187], v[86:89]
	v_mfma_f32_16x16x128_f8f6f4 v[78:81], v[10:17], v[180:187], v[78:81]
	v_mfma_f32_16x16x128_f8f6f4 v[70:73], v[2:9], v[188:195], v[70:73]
	v_mfma_f32_16x16x128_f8f6f4 v[62:65], v[10:17], v[188:195], v[62:65]
	v_mfma_f32_16x16x128_f8f6f4 v[54:57], v[2:9], v[196:203], v[54:57]
	v_mfma_f32_16x16x128_f8f6f4 v[46:49], v[10:17], v[196:203], v[46:49]
	v_mfma_f32_16x16x128_f8f6f4 v[38:41], v[2:9], v[204:211], v[38:41]
	v_mfma_f32_16x16x128_f8f6f4 v[34:37], v[10:17], v[204:211], v[34:37]
	s_setprio 0
	s_barrier
	ds_read_b128 v[2:5], v177
	ds_read_b128 v[6:9], v177 offset:1024
	ds_read_b128 v[10:13], v177 offset:2048
	ds_read_b128 v[14:17], v177 offset:3072
	ds_read_b128 v[18:21], v178
	ds_read_b128 v[22:25], v178 offset:1024
	ds_read_b128 v[26:29], v178 offset:2048
	ds_read_b128 v[30:33], v178 offset:3072
	ds_read_b128 v[180:183], v176 offset:32768
	ds_read_b128 v[184:187], v176 offset:33792
	ds_read_b128 v[188:191], v176 offset:34816
	ds_read_b128 v[192:195], v176 offset:35840
	ds_read_b128 v[196:199], v176 offset:36864
	ds_read_b128 v[200:203], v176 offset:37888
	ds_read_b128 v[204:207], v176 offset:38912
	ds_read_b128 v[208:211], v176 offset:39936
	s_add_u32 s78, s84, 0x20000
	s_addc_u32 s79, s85, 0
	s_mov_b32 s84, m0
	s_mov_b32 m0, s89
	s_nop 2
	global_load_lds_dwordx4 v166, s[78:79]
	s_mov_b32 m0, s84
	s_nop 0
	s_mov_b32 s84, m0
	s_mov_b32 m0, s3
	s_nop 2
	global_load_lds_dwordx4 v168, s[78:79]
	s_mov_b32 m0, s84
	s_waitcnt vmcnt(8) lgkmcnt(0)
	s_barrier
	s_setprio 1
	v_mfma_f32_16x16x128_f8f6f4 v[158:161], v[2:9], v[180:187], v[158:161]
	v_mfma_f32_16x16x128_f8f6f4 v[154:157], v[10:17], v[180:187], v[154:157]
	v_mfma_f32_16x16x128_f8f6f4 v[146:149], v[2:9], v[188:195], v[146:149]
	v_mfma_f32_16x16x128_f8f6f4 v[138:141], v[10:17], v[188:195], v[138:141]
	v_mfma_f32_16x16x128_f8f6f4 v[130:133], v[2:9], v[196:203], v[130:133]
	v_mfma_f32_16x16x128_f8f6f4 v[122:125], v[10:17], v[196:203], v[122:125]
	v_mfma_f32_16x16x128_f8f6f4 v[114:117], v[2:9], v[204:211], v[114:117]
	v_mfma_f32_16x16x128_f8f6f4 v[106:109], v[10:17], v[204:211], v[106:109]
	v_mfma_f32_16x16x128_f8f6f4 v[150:153], v[18:25], v[180:187], v[150:153]
	v_mfma_f32_16x16x128_f8f6f4 v[142:145], v[26:33], v[180:187], v[142:145]
	v_mfma_f32_16x16x128_f8f6f4 v[134:137], v[18:25], v[188:195], v[134:137]
	v_mfma_f32_16x16x128_f8f6f4 v[126:129], v[26:33], v[188:195], v[126:129]
	v_mfma_f32_16x16x128_f8f6f4 v[118:121], v[18:25], v[196:203], v[118:121]
	v_mfma_f32_16x16x128_f8f6f4 v[110:113], v[26:33], v[196:203], v[110:113]
	v_mfma_f32_16x16x128_f8f6f4 v[102:105], v[18:25], v[204:211], v[102:105]
	v_mfma_f32_16x16x128_f8f6f4 v[98:101], v[26:33], v[204:211], v[98:101]
	s_setprio 0
	s_barrier
	ds_read_b128 v[180:183], v176 offset:49152
	ds_read_b128 v[184:187], v176 offset:50176
	ds_read_b128 v[188:191], v176 offset:51200
	ds_read_b128 v[192:195], v176 offset:52224
	ds_read_b128 v[196:199], v176 offset:53248
	ds_read_b128 v[200:203], v176 offset:54272
	ds_read_b128 v[204:207], v176 offset:55296
	ds_read_b128 v[208:211], v176 offset:56320
	s_add_u32 s78, s82, 0x80
	s_addc_u32 s79, s83, 0
	s_mov_b32 s84, m0
	s_mov_b32 m0, s90
	s_nop 2
	global_load_lds_dwordx4 v167, s[78:79]
	s_mov_b32 m0, s84
	s_nop 0
	s_mov_b32 s84, m0
	s_mov_b32 m0, s28
	s_nop 2
	global_load_lds_dwordx4 v169, s[78:79]
	s_mov_b32 m0, s84
	s_add_u32 s78, s82, 0x20080
	s_addc_u32 s79, s83, 0
	s_mov_b32 s82, m0
	s_mov_b32 m0, s94
	s_nop 2
	global_load_lds_dwordx4 v167, s[78:79]
	s_mov_b32 m0, s82
	s_nop 0
	s_mov_b32 s82, m0
	s_mov_b32 m0, s95
	s_nop 2
	global_load_lds_dwordx4 v169, s[78:79]
	s_mov_b32 m0, s82
	s_mov_b32 s78, m0
	s_mov_b32 m0, s93
	s_nop 2
	global_load_lds_dwordx4 v166, s[80:81]
	s_mov_b32 m0, s78
	s_nop 0
	s_mov_b32 s78, m0
	s_mov_b32 m0, s2
	s_nop 2
	global_load_lds_dwordx4 v168, s[80:81]
	s_mov_b32 m0, s78
	s_waitcnt vmcnt(8) lgkmcnt(0)
	s_barrier
	s_setprio 1
	v_mfma_f32_16x16x128_f8f6f4 v[94:97], v[2:9], v[180:187], v[94:97]
	v_mfma_f32_16x16x128_f8f6f4 v[90:93], v[10:17], v[180:187], v[90:93]
	v_mfma_f32_16x16x128_f8f6f4 v[82:85], v[2:9], v[188:195], v[82:85]
	v_mfma_f32_16x16x128_f8f6f4 v[74:77], v[10:17], v[188:195], v[74:77]
	v_mfma_f32_16x16x128_f8f6f4 v[66:69], v[2:9], v[196:203], v[66:69]
	v_mfma_f32_16x16x128_f8f6f4 v[58:61], v[10:17], v[196:203], v[58:61]
	v_mfma_f32_16x16x128_f8f6f4 v[50:53], v[2:9], v[204:211], v[50:53]
	v_mfma_f32_16x16x128_f8f6f4 v[42:45], v[10:17], v[204:211], v[42:45]
	v_mfma_f32_16x16x128_f8f6f4 v[86:89], v[18:25], v[180:187], v[86:89]
	v_mfma_f32_16x16x128_f8f6f4 v[78:81], v[26:33], v[180:187], v[78:81]
	v_mfma_f32_16x16x128_f8f6f4 v[70:73], v[18:25], v[188:195], v[70:73]
	v_mfma_f32_16x16x128_f8f6f4 v[62:65], v[26:33], v[188:195], v[62:65]
	v_mfma_f32_16x16x128_f8f6f4 v[54:57], v[18:25], v[196:203], v[54:57]
	v_mfma_f32_16x16x128_f8f6f4 v[46:49], v[26:33], v[196:203], v[46:49]
	v_mfma_f32_16x16x128_f8f6f4 v[38:41], v[18:25], v[204:211], v[38:41]
	v_mfma_f32_16x16x128_f8f6f4 v[34:37], v[26:33], v[204:211], v[34:37]
	s_setprio 0
	s_barrier
	s_add_i32 s33, s33, 2
	s_add_u32 vcc_lo, vcc_lo, 0x100
	s_addc_u32 vcc_hi, vcc_hi, 0
	s_cmp_gt_u32 s33, 5
	s_mov_b64 s[78:79], s[76:77]
	s_cbranch_scc0 .LBB0_190
	s_and_b64 vcc, exec, s[10:11]
	s_cbranch_vccz .LBB0_193
	s_barrier

.LBB0_217:
	s_cmp_lt_i32 s33, 0
	s_cbranch_scc1 .Lpeel1
	ds_read_b128 v[18:21], v168
	ds_read_b128 v[22:25], v168 offset:1024
	ds_read_b128 v[26:29], v168 offset:2048
	ds_read_b128 v[30:33], v168 offset:3072
	ds_read_b128 v[2:5], v169
	ds_read_b128 v[6:9], v169 offset:1024
	ds_read_b128 v[10:13], v169 offset:2048
	ds_read_b128 v[14:17], v169 offset:3072
	s_add_u32 s78, s80, 0x100
	s_addc_u32 s79, s81, 0
	s_cmp_eq_u32 s33, 4
	s_cselect_b32 s86, s57, s78
	s_cselect_b32 s87, s7, s79
	s_cselect_b32 s84, vcc_lo, vcc_hi
	s_cselect_b32 s85, s59, s89
	s_add_u32 s82, s86, 0x80
	s_addc_u32 s83, s87, 0
	ds_read_b128 v[176:179], v170
	ds_read_b128 v[180:183], v170 offset:1024
	ds_read_b128 v[184:187], v170 offset:2048
	ds_read_b128 v[188:191], v170 offset:3072
	ds_read_b128 v[192:195], v170 offset:4096
	ds_read_b128 v[196:199], v170 offset:5120
	ds_read_b128 v[200:203], v170 offset:6144
	ds_read_b128 v[204:207], v170 offset:7168
	s_add_u32 s80, s80, 0x20080
	s_addc_u32 s81, s81, 0
	s_mov_b32 s29, m0
	s_mov_b32 m0, s91
	s_nop 2
	global_load_lds_dwordx4 v162, s[80:81]
	s_mov_b32 m0, s29
	s_nop 0
	s_mov_b32 s29, m0
	s_mov_b32 m0, s92
	s_nop 2
	global_load_lds_dwordx4 v164, s[80:81]
	s_mov_b32 m0, s29
	s_waitcnt vmcnt(8) lgkmcnt(0)
	s_barrier
	s_setprio 1
	v_mfma_f32_16x16x128_f8f6f4 v[158:161], v[18:25], v[176:183], v[158:161]
	v_mfma_f32_16x16x128_f8f6f4 v[154:157], v[26:33], v[176:183], v[154:157]
	v_mfma_f32_16x16x128_f8f6f4 v[146:149], v[18:25], v[184:191], v[146:149]
	v_mfma_f32_16x16x128_f8f6f4 v[138:141], v[26:33], v[184:191], v[138:141]
	v_mfma_f32_16x16x128_f8f6f4 v[130:133], v[18:25], v[192:199], v[130:133]
	v_mfma_f32_16x16x128_f8f6f4 v[122:125], v[26:33], v[192:199], v[122:125]
	v_mfma_f32_16x16x128_f8f6f4 v[114:117], v[18:25], v[200:207], v[114:117]
	v_mfma_f32_16x16x128_f8f6f4 v[106:109], v[26:33], v[200:207], v[106:109]
	v_mfma_f32_16x16x128_f8f6f4 v[150:153], v[2:9], v[176:183], v[150:153]
	v_mfma_f32_16x16x128_f8f6f4 v[142:145], v[10:17], v[176:183], v[142:145]
	v_mfma_f32_16x16x128_f8f6f4 v[134:137], v[2:9], v[184:191], v[134:137]
	v_mfma_f32_16x16x128_f8f6f4 v[126:129], v[10:17], v[184:191], v[126:129]
	v_mfma_f32_16x16x128_f8f6f4 v[118:121], v[2:9], v[192:199], v[118:121]
	v_mfma_f32_16x16x128_f8f6f4 v[110:113], v[10:17], v[192:199], v[110:113]
	v_mfma_f32_16x16x128_f8f6f4 v[102:105], v[2:9], v[200:207], v[102:105]
	v_mfma_f32_16x16x128_f8f6f4 v[98:101], v[10:17], v[200:207], v[98:101]
	s_setprio 0
	s_barrier
	ds_read_b128 v[176:179], v170 offset:16384
	ds_read_b128 v[180:183], v170 offset:17408
	ds_read_b128 v[184:187], v170 offset:18432
	ds_read_b128 v[188:191], v170 offset:19456
	ds_read_b128 v[192:195], v170 offset:20480
	ds_read_b128 v[196:199], v170 offset:21504
	ds_read_b128 v[200:203], v170 offset:22528
	ds_read_b128 v[204:207], v170 offset:23552
	s_mov_b32 s29, m0
	s_mov_b32 m0, s36
	s_nop 2
	global_load_lds_dwordx4 v163, s[84:85]
	s_mov_b32 m0, s29
	s_add_u32 s80, s84, 0x20000
	s_mov_b32 s29, m0
	s_mov_b32 m0, s37
	s_nop 2
	global_load_lds_dwordx4 v165, s[84:85]
	s_mov_b32 m0, s29
	s_addc_u32 s81, s85, 0
	s_mov_b32 s29, m0
	s_mov_b32 m0, s55
	s_nop 2
	global_load_lds_dwordx4 v163, s[80:81]
	s_mov_b32 m0, s29
	s_nop 0
	s_mov_b32 s29, m0
	s_mov_b32 m0, s77
	s_nop 2
	global_load_lds_dwordx4 v165, s[80:81]
	s_mov_b32 m0, s29
	s_nop 0
	s_mov_b32 s29, m0
	s_mov_b32 m0, s35
	s_nop 2
	global_load_lds_dwordx4 v162, s[86:87]
	s_mov_b32 m0, s29
	s_nop 0
	s_mov_b32 s29, m0
	s_mov_b32 m0, s88
	s_nop 2
	global_load_lds_dwordx4 v164, s[86:87]
	s_mov_b32 m0, s29
	s_waitcnt vmcnt(8) lgkmcnt(0)
	s_barrier
	s_setprio 1
	v_mfma_f32_16x16x128_f8f6f4 v[94:97], v[18:25], v[176:183], v[94:97]
	v_mfma_f32_16x16x128_f8f6f4 v[90:93], v[26:33], v[176:183], v[90:93]
	v_mfma_f32_16x16x128_f8f6f4 v[82:85], v[18:25], v[184:191], v[82:85]
	v_mfma_f32_16x16x128_f8f6f4 v[74:77], v[26:33], v[184:191], v[74:77]
	v_mfma_f32_16x16x128_f8f6f4 v[66:69], v[18:25], v[192:199], v[66:69]
	v_mfma_f32_16x16x128_f8f6f4 v[58:61], v[26:33], v[192:199], v[58:61]
	v_mfma_f32_16x16x128_f8f6f4 v[50:53], v[18:25], v[200:207], v[50:53]
	v_mfma_f32_16x16x128_f8f6f4 v[42:45], v[26:33], v[200:207], v[42:45]
	v_mfma_f32_16x16x128_f8f6f4 v[86:89], v[2:9], v[176:183], v[86:89]
	v_mfma_f32_16x16x128_f8f6f4 v[78:81], v[10:17], v[176:183], v[78:81]
	v_mfma_f32_16x16x128_f8f6f4 v[70:73], v[2:9], v[184:191], v[70:73]
	v_mfma_f32_16x16x128_f8f6f4 v[62:65], v[10:17], v[184:191], v[62:65]
	v_mfma_f32_16x16x128_f8f6f4 v[54:57], v[2:9], v[192:199], v[54:57]
	v_mfma_f32_16x16x128_f8f6f4 v[46:49], v[10:17], v[192:199], v[46:49]
	v_mfma_f32_16x16x128_f8f6f4 v[38:41], v[2:9], v[200:207], v[38:41]
	v_mfma_f32_16x16x128_f8f6f4 v[34:37], v[10:17], v[200:207], v[34:37]
	s_setprio 0
	s_barrier
.Lmid1:
	ds_read_b128 v[2:5], v172
	ds_read_b128 v[6:9], v172 offset:1024
	ds_read_b128 v[10:13], v172 offset:2048
	ds_read_b128 v[14:17], v172 offset:3072
	ds_read_b128 v[18:21], v174
	ds_read_b128 v[22:25], v174 offset:1024
	ds_read_b128 v[26:29], v174 offset:2048
	ds_read_b128 v[30:33], v174 offset:3072
	ds_read_b128 v[176:179], v170 offset:32768
	ds_read_b128 v[180:183], v170 offset:33792
	ds_read_b128 v[184:187], v170 offset:34816
	ds_read_b128 v[188:191], v170 offset:35840
	ds_read_b128 v[192:195], v170 offset:36864
	ds_read_b128 v[196:199], v170 offset:37888
	ds_read_b128 v[200:203], v170 offset:38912
	ds_read_b128 v[204:207], v170 offset:39936
	s_add_u32 s80, s86, 0x20000
	s_addc_u32 s81, s87, 0
	s_mov_b32 s29, m0
	s_mov_b32 m0, s97
	s_nop 2
	global_load_lds_dwordx4 v162, s[80:81]
	s_mov_b32 m0, s29
	s_nop 0
	s_mov_b32 s29, m0
	s_mov_b32 m0, s3
	s_nop 2
	global_load_lds_dwordx4 v164, s[80:81]
	s_mov_b32 m0, s29
	s_waitcnt vmcnt(8) lgkmcnt(0)
	s_barrier
	s_setprio 1
	v_mfma_f32_16x16x128_f8f6f4 v[158:161], v[2:9], v[176:183], v[158:161]
	v_mfma_f32_16x16x128_f8f6f4 v[154:157], v[10:17], v[176:183], v[154:157]
	v_mfma_f32_16x16x128_f8f6f4 v[146:149], v[2:9], v[184:191], v[146:149]
	v_mfma_f32_16x16x128_f8f6f4 v[138:141], v[10:17], v[184:191], v[138:141]
	v_mfma_f32_16x16x128_f8f6f4 v[130:133], v[2:9], v[192:199], v[130:133]
	v_mfma_f32_16x16x128_f8f6f4 v[122:125], v[10:17], v[192:199], v[122:125]
	v_mfma_f32_16x16x128_f8f6f4 v[114:117], v[2:9], v[200:207], v[114:117]
	v_mfma_f32_16x16x128_f8f6f4 v[106:109], v[10:17], v[200:207], v[106:109]
	v_mfma_f32_16x16x128_f8f6f4 v[150:153], v[18:25], v[176:183], v[150:153]
	v_mfma_f32_16x16x128_f8f6f4 v[142:145], v[26:33], v[176:183], v[142:145]
	v_mfma_f32_16x16x128_f8f6f4 v[134:137], v[18:25], v[184:191], v[134:137]
	v_mfma_f32_16x16x128_f8f6f4 v[126:129], v[26:33], v[184:191], v[126:129]
	v_mfma_f32_16x16x128_f8f6f4 v[118:121], v[18:25], v[192:199], v[118:121]
	v_mfma_f32_16x16x128_f8f6f4 v[110:113], v[26:33], v[192:199], v[110:113]
	v_mfma_f32_16x16x128_f8f6f4 v[102:105], v[18:25], v[200:207], v[102:105]
	v_mfma_f32_16x16x128_f8f6f4 v[98:101], v[26:33], v[200:207], v[98:101]
	s_setprio 0
	s_barrier
	ds_read_b128 v[176:179], v170 offset:49152
	ds_read_b128 v[180:183], v170 offset:50176
	ds_read_b128 v[184:187], v170 offset:51200
	ds_read_b128 v[188:191], v170 offset:52224
	ds_read_b128 v[192:195], v170 offset:53248
	ds_read_b128 v[196:199], v170 offset:54272
	ds_read_b128 v[200:203], v170 offset:55296
	ds_read_b128 v[204:207], v170 offset:56320
	s_add_u32 s80, s84, 0x80
	s_addc_u32 s81, s85, 0
	s_mov_b32 s29, m0
	s_mov_b32 m0, s90
	s_nop 2
	global_load_lds_dwordx4 v163, s[80:81]
	s_mov_b32 m0, s29
	s_nop 0
	s_mov_b32 s29, m0
	s_mov_b32 m0, s28
	s_nop 2
	global_load_lds_dwordx4 v165, s[80:81]
	s_mov_b32 m0, s29
	s_add_u32 s80, s84, 0x20080
	s_addc_u32 s81, s85, 0
	s_mov_b32 s29, m0
	s_mov_b32 m0, s94
	s_nop 2
	global_load_lds_dwordx4 v163, s[80:81]
	s_mov_b32 m0, s29
	s_nop 0
	s_mov_b32 s29, m0
	s_mov_b32 m0, s95
	s_nop 2
	global_load_lds_dwordx4 v165, s[80:81]
	s_mov_b32 m0, s29
	s_nop 0
	s_mov_b32 s29, m0
	s_mov_b32 m0, s93
	s_nop 2
	global_load_lds_dwordx4 v162, s[82:83]
	s_mov_b32 m0, s29
	s_nop 0
	s_mov_b32 s29, m0
	s_mov_b32 m0, s2
	s_nop 2
	global_load_lds_dwordx4 v164, s[82:83]
	s_mov_b32 m0, s29
	s_waitcnt vmcnt(8) lgkmcnt(0)
	s_barrier
	s_setprio 1
	v_mfma_f32_16x16x128_f8f6f4 v[94:97], v[2:9], v[176:183], v[94:97]
	v_mfma_f32_16x16x128_f8f6f4 v[90:93], v[10:17], v[176:183], v[90:93]
	v_mfma_f32_16x16x128_f8f6f4 v[82:85], v[2:9], v[184:191], v[82:85]
	v_mfma_f32_16x16x128_f8f6f4 v[74:77], v[10:17], v[184:191], v[74:77]
	v_mfma_f32_16x16x128_f8f6f4 v[66:69], v[2:9], v[192:199], v[66:69]
	v_mfma_f32_16x16x128_f8f6f4 v[58:61], v[10:17], v[192:199], v[58:61]
	v_mfma_f32_16x16x128_f8f6f4 v[50:53], v[2:9], v[200:207], v[50:53]
	v_mfma_f32_16x16x128_f8f6f4 v[42:45], v[10:17], v[200:207], v[42:45]
	v_mfma_f32_16x16x128_f8f6f4 v[86:89], v[18:25], v[176:183], v[86:89]
	v_mfma_f32_16x16x128_f8f6f4 v[78:81], v[26:33], v[176:183], v[78:81]
	v_mfma_f32_16x16x128_f8f6f4 v[70:73], v[18:25], v[184:191], v[70:73]
	v_mfma_f32_16x16x128_f8f6f4 v[62:65], v[26:33], v[184:191], v[62:65]
	v_mfma_f32_16x16x128_f8f6f4 v[54:57], v[18:25], v[192:199], v[54:57]
	v_mfma_f32_16x16x128_f8f6f4 v[46:49], v[26:33], v[192:199], v[46:49]
	v_mfma_f32_16x16x128_f8f6f4 v[38:41], v[18:25], v[200:207], v[38:41]
	v_mfma_f32_16x16x128_f8f6f4 v[34:37], v[26:33], v[200:207], v[34:37]
	s_setprio 0
	s_cmp_lt_i32 s33, 4
	s_cbranch_scc1 .Lkb1_do
	s_cmp_lg_u64 s[10:11], 0
	s_cbranch_scc0 .Lkb1_skip

.Lpeel1:
	ds_read_b128 v[18:21], v168
	ds_read_b128 v[22:25], v168 offset:1024
	ds_read_b128 v[26:29], v168 offset:2048
	ds_read_b128 v[30:33], v168 offset:3072
	ds_read_b128 v[2:5], v169
	ds_read_b128 v[6:9], v169 offset:1024
	ds_read_b128 v[10:13], v169 offset:2048
	ds_read_b128 v[14:17], v169 offset:3072
	s_add_u32 s78, s80, 0x100
	s_addc_u32 s79, s81, 0
	s_cmp_eq_u32 s33, 4
	s_cselect_b32 s86, s57, s78
	s_cselect_b32 s87, s7, s79
	s_cselect_b32 s84, vcc_lo, vcc_hi
	s_cselect_b32 s85, s59, s89
	s_add_u32 s82, s86, 0x80
	s_addc_u32 s83, s87, 0
	ds_read_b128 v[176:179], v170
	ds_read_b128 v[180:183], v170 offset:1024
	ds_read_b128 v[184:187], v170 offset:2048
	ds_read_b128 v[188:191], v170 offset:3072
	ds_read_b128 v[192:195], v170 offset:4096
	ds_read_b128 v[196:199], v170 offset:5120
	ds_read_b128 v[200:203], v170 offset:6144
	ds_read_b128 v[204:207], v170 offset:7168
	s_add_u32 s80, s80, 0x20080
	s_addc_u32 s81, s81, 0
	s_mov_b32 s29, m0
	s_mov_b32 m0, s91
	s_nop 2
	global_load_lds_dwordx4 v162, s[80:81]
	s_mov_b32 m0, s29
	s_nop 0
	s_mov_b32 s29, m0
	s_mov_b32 m0, s92
	s_nop 2
	global_load_lds_dwordx4 v164, s[80:81]
	s_mov_b32 m0, s29
	s_waitcnt vmcnt(8) lgkmcnt(0)
	s_barrier
	s_setprio 1
	v_mfma_f32_16x16x128_f8f6f4 v[158:161], v[18:25], v[176:183], 0
	v_mfma_f32_16x16x128_f8f6f4 v[154:157], v[26:33], v[176:183], 0
	v_mfma_f32_16x16x128_f8f6f4 v[146:149], v[18:25], v[184:191], 0
	v_mfma_f32_16x16x128_f8f6f4 v[138:141], v[26:33], v[184:191], 0
	v_mfma_f32_16x16x128_f8f6f4 v[130:133], v[18:25], v[192:199], 0
	v_mfma_f32_16x16x128_f8f6f4 v[122:125], v[26:33], v[192:199], 0
	v_mfma_f32_16x16x128_f8f6f4 v[114:117], v[18:25], v[200:207], 0
	v_mfma_f32_16x16x128_f8f6f4 v[106:109], v[26:33], v[200:207], 0
	v_mfma_f32_16x16x128_f8f6f4 v[150:153], v[2:9], v[176:183], 0
	v_mfma_f32_16x16x128_f8f6f4 v[142:145], v[10:17], v[176:183], 0
	v_mfma_f32_16x16x128_f8f6f4 v[134:137], v[2:9], v[184:191], 0
	v_mfma_f32_16x16x128_f8f6f4 v[126:129], v[10:17], v[184:191], 0
	v_mfma_f32_16x16x128_f8f6f4 v[118:121], v[2:9], v[192:199], 0
	v_mfma_f32_16x16x128_f8f6f4 v[110:113], v[10:17], v[192:199], 0
	v_mfma_f32_16x16x128_f8f6f4 v[102:105], v[2:9], v[200:207], 0
	v_mfma_f32_16x16x128_f8f6f4 v[98:101], v[10:17], v[200:207], 0
	s_setprio 0
	s_barrier
	ds_read_b128 v[176:179], v170 offset:16384
	ds_read_b128 v[180:183], v170 offset:17408
	ds_read_b128 v[184:187], v170 offset:18432
	ds_read_b128 v[188:191], v170 offset:19456
	ds_read_b128 v[192:195], v170 offset:20480
	ds_read_b128 v[196:199], v170 offset:21504
	ds_read_b128 v[200:203], v170 offset:22528
	ds_read_b128 v[204:207], v170 offset:23552
	s_mov_b32 s29, m0
	s_mov_b32 m0, s36
	s_nop 2
	global_load_lds_dwordx4 v163, s[84:85]
	s_mov_b32 m0, s29
	s_add_u32 s80, s84, 0x20000
	s_mov_b32 s29, m0
	s_mov_b32 m0, s37
	s_nop 2
	global_load_lds_dwordx4 v165, s[84:85]
	s_mov_b32 m0, s29
	s_addc_u32 s81, s85, 0
	s_mov_b32 s29, m0
	s_mov_b32 m0, s55
	s_nop 2
	global_load_lds_dwordx4 v163, s[80:81]
	s_mov_b32 m0, s29
	s_nop 0
	s_mov_b32 s29, m0
	s_mov_b32 m0, s77
	s_nop 2
	global_load_lds_dwordx4 v165, s[80:81]
	s_mov_b32 m0, s29
	s_nop 0
	s_mov_b32 s29, m0
	s_mov_b32 m0, s35
	s_nop 2
	global_load_lds_dwordx4 v162, s[86:87]
	s_mov_b32 m0, s29
	s_nop 0
	s_mov_b32 s29, m0
	s_mov_b32 m0, s88
	s_nop 2
	global_load_lds_dwordx4 v164, s[86:87]
	s_mov_b32 m0, s29
	s_waitcnt vmcnt(8) lgkmcnt(0)
	s_barrier
	s_setprio 1
	v_mfma_f32_16x16x128_f8f6f4 v[94:97], v[18:25], v[176:183], 0
	v_mfma_f32_16x16x128_f8f6f4 v[90:93], v[26:33], v[176:183], 0
	v_mfma_f32_16x16x128_f8f6f4 v[82:85], v[18:25], v[184:191], 0
	v_mfma_f32_16x16x128_f8f6f4 v[74:77], v[26:33], v[184:191], 0
	v_mfma_f32_16x16x128_f8f6f4 v[66:69], v[18:25], v[192:199], 0
	v_mfma_f32_16x16x128_f8f6f4 v[58:61], v[26:33], v[192:199], 0
	v_mfma_f32_16x16x128_f8f6f4 v[50:53], v[18:25], v[200:207], 0
	v_mfma_f32_16x16x128_f8f6f4 v[42:45], v[26:33], v[200:207], 0
	v_mfma_f32_16x16x128_f8f6f4 v[86:89], v[2:9], v[176:183], 0
	v_mfma_f32_16x16x128_f8f6f4 v[78:81], v[10:17], v[176:183], 0
	v_mfma_f32_16x16x128_f8f6f4 v[70:73], v[2:9], v[184:191], 0
	v_mfma_f32_16x16x128_f8f6f4 v[62:65], v[10:17], v[184:191], 0
	v_mfma_f32_16x16x128_f8f6f4 v[54:57], v[2:9], v[192:199], 0
	v_mfma_f32_16x16x128_f8f6f4 v[46:49], v[10:17], v[192:199], 0
	v_mfma_f32_16x16x128_f8f6f4 v[38:41], v[2:9], v[200:207], 0
	v_mfma_f32_16x16x128_f8f6f4 v[34:37], v[10:17], v[200:207], 0
	s_setprio 0
	s_barrier
	s_branch .Lmid1

.Lpeel1046:
	ds_read_b128 v[136:139], v172
	ds_read_b128 v[140:143], v172 offset:1024
	ds_read_b128 v[144:147], v172 offset:2048
	ds_read_b128 v[148:151], v172 offset:3072
	ds_read_b128 v[152:155], v173
	ds_read_b128 v[156:159], v173 offset:1024
	ds_read_b128 v[160:163], v173 offset:2048
	ds_read_b128 v[178:181], v173 offset:3072
	s_add_u32 s25, s64, s56
	s_addc_u32 s33, s65, s57
	s_add_u32 s66, s25, 0x100
	s_addc_u32 s67, s33, 0
	s_add_u32 s23, s62, s56
	s_addc_u32 s24, s63, s57
	s_add_u32 s28, s23, 0x100
	s_addc_u32 s29, s24, 0
	s_add_u32 s58, s25, 0x180
	s_addc_u32 s59, s33, 0
	ds_read_b128 v[182:185], v174
	ds_read_b128 v[186:189], v174 offset:1024
	ds_read_b128 v[190:193], v174 offset:2048
	ds_read_b128 v[194:197], v174 offset:3072
	ds_read_b128 v[198:201], v174 offset:4096
	ds_read_b128 v[202:205], v174 offset:5120
	ds_read_b128 v[206:209], v174 offset:6144
	ds_read_b128 v[210:213], v174 offset:7168
	s_add_u32 s30, s25, 0x40080
	s_addc_u32 s31, s33, 0
	s_mov_b32 s36, m0
	s_mov_b32 m0, s26
	s_nop 2
	global_load_lds_dwordx4 v165, s[30:31]
	s_mov_b32 m0, s36
	s_nop 0
	s_mov_b32 s36, m0
	s_mov_b32 m0, s27
	s_nop 2
	global_load_lds_dwordx4 v167, s[30:31]
	s_mov_b32 m0, s36
	s_waitcnt vmcnt(8) lgkmcnt(0)
	s_barrier
	s_setprio 1
	v_mfma_f32_16x16x32_bf16 v[26:29], v[136:139], v[182:185], 0
	v_mfma_f32_16x16x32_bf16 v[30:33], v[144:147], v[182:185], 0
	v_mfma_f32_16x16x32_bf16 v[50:53], v[136:139], v[190:193], 0
	v_mfma_f32_16x16x32_bf16 v[54:57], v[144:147], v[190:193], 0
	v_mfma_f32_16x16x32_bf16 v[74:77], v[136:139], v[198:201], 0
	v_mfma_f32_16x16x32_bf16 v[78:81], v[144:147], v[198:201], 0
	v_mfma_f32_16x16x32_bf16 v[94:97], v[136:139], v[206:209], 0
	v_mfma_f32_16x16x32_bf16 v[102:105], v[144:147], v[206:209], 0
	v_mfma_f32_16x16x32_bf16 v[26:29], v[140:143], v[186:189], v[26:29]
	v_mfma_f32_16x16x32_bf16 v[30:33], v[148:151], v[186:189], v[30:33]
	v_mfma_f32_16x16x32_bf16 v[50:53], v[140:143], v[194:197], v[50:53]
	v_mfma_f32_16x16x32_bf16 v[54:57], v[148:151], v[194:197], v[54:57]
	v_mfma_f32_16x16x32_bf16 v[74:77], v[140:143], v[202:205], v[74:77]
	v_mfma_f32_16x16x32_bf16 v[78:81], v[148:151], v[202:205], v[78:81]
	v_mfma_f32_16x16x32_bf16 v[94:97], v[140:143], v[210:213], v[94:97]
	v_mfma_f32_16x16x32_bf16 v[102:105], v[148:151], v[210:213], v[102:105]
	v_mfma_f32_16x16x32_bf16 v[38:41], v[152:155], v[182:185], 0
	v_mfma_f32_16x16x32_bf16 v[42:45], v[160:163], v[182:185], 0
	v_mfma_f32_16x16x32_bf16 v[62:65], v[152:155], v[190:193], 0
	v_mfma_f32_16x16x32_bf16 v[66:69], v[160:163], v[190:193], 0
	v_mfma_f32_16x16x32_bf16 v[82:85], v[152:155], v[198:201], 0
	v_mfma_f32_16x16x32_bf16 v[90:93], v[160:163], v[198:201], 0
	v_mfma_f32_16x16x32_bf16 v[106:109], v[152:155], v[206:209], 0
	v_mfma_f32_16x16x32_bf16 v[114:117], v[160:163], v[206:209], 0
	v_mfma_f32_16x16x32_bf16 v[38:41], v[156:159], v[186:189], v[38:41]
	v_mfma_f32_16x16x32_bf16 v[42:45], v[178:181], v[186:189], v[42:45]
	v_mfma_f32_16x16x32_bf16 v[62:65], v[156:159], v[194:197], v[62:65]
	v_mfma_f32_16x16x32_bf16 v[66:69], v[178:181], v[194:197], v[66:69]
	v_mfma_f32_16x16x32_bf16 v[82:85], v[156:159], v[202:205], v[82:85]
	v_mfma_f32_16x16x32_bf16 v[90:93], v[178:181], v[202:205], v[90:93]
	v_mfma_f32_16x16x32_bf16 v[106:109], v[156:159], v[210:213], v[106:109]
	v_mfma_f32_16x16x32_bf16 v[114:117], v[178:181], v[210:213], v[114:117]
	s_setprio 0
	s_barrier
	ds_read_b128 v[182:185], v174 offset:16384
	ds_read_b128 v[186:189], v174 offset:17408
	ds_read_b128 v[190:193], v174 offset:18432
	ds_read_b128 v[194:197], v174 offset:19456
	ds_read_b128 v[198:201], v174 offset:20480
	ds_read_b128 v[202:205], v174 offset:21504
	ds_read_b128 v[206:209], v174 offset:22528
	ds_read_b128 v[210:213], v174 offset:23552
	s_mov_b32 s30, m0
	s_mov_b32 m0, s80
	s_nop 2
	global_load_lds_dwordx4 v166, s[28:29]
	s_mov_b32 m0, s30
	s_nop 0
	s_mov_b32 s30, m0
	s_mov_b32 m0, s81
	s_nop 2
	global_load_lds_dwordx4 v168, s[28:29]
	s_mov_b32 m0, s30
	s_add_u32 s28, s23, 0x40100
	s_addc_u32 s29, s24, 0
	s_mov_b32 s30, m0
	s_mov_b32 m0, s82
	s_nop 2
	global_load_lds_dwordx4 v166, s[28:29]
	s_mov_b32 m0, s30
	s_nop 0
	s_mov_b32 s30, m0
	s_mov_b32 m0, s83
	s_nop 2
	global_load_lds_dwordx4 v168, s[28:29]
	s_mov_b32 m0, s30
	s_mov_b32 s28, m0
	s_mov_b32 m0, s79
	s_nop 2
	global_load_lds_dwordx4 v165, s[66:67]
	s_mov_b32 m0, s28
	s_nop 0
	s_mov_b32 s28, m0
	s_mov_b32 m0, s84
	s_nop 2
	global_load_lds_dwordx4 v167, s[66:67]
	s_mov_b32 m0, s28
	s_waitcnt vmcnt(8) lgkmcnt(0)
	s_barrier
	s_setprio 1
	v_mfma_f32_16x16x32_bf16 v[118:121], v[136:139], v[182:185], 0
	v_mfma_f32_16x16x32_bf16 v[126:129], v[144:147], v[182:185], 0
	v_mfma_f32_16x16x32_bf16 v[98:101], v[136:139], v[190:193], 0
	v_mfma_f32_16x16x32_bf16 v[86:89], v[144:147], v[190:193], 0
	v_mfma_f32_16x16x32_bf16 v[46:49], v[136:139], v[198:201], 0
	v_mfma_f32_16x16x32_bf16 v[34:37], v[144:147], v[198:201], 0
	v_mfma_f32_16x16x32_bf16 v[14:17], v[136:139], v[206:209], 0
	v_mfma_f32_16x16x32_bf16 v[10:13], v[144:147], v[206:209], 0
	v_mfma_f32_16x16x32_bf16 v[118:121], v[140:143], v[186:189], v[118:121]
	v_mfma_f32_16x16x32_bf16 v[126:129], v[148:151], v[186:189], v[126:129]
	v_mfma_f32_16x16x32_bf16 v[98:101], v[140:143], v[194:197], v[98:101]
	v_mfma_f32_16x16x32_bf16 v[86:89], v[148:151], v[194:197], v[86:89]
	v_mfma_f32_16x16x32_bf16 v[46:49], v[140:143], v[202:205], v[46:49]
	v_mfma_f32_16x16x32_bf16 v[34:37], v[148:151], v[202:205], v[34:37]
	v_mfma_f32_16x16x32_bf16 v[14:17], v[140:143], v[210:213], v[14:17]
	v_mfma_f32_16x16x32_bf16 v[10:13], v[148:151], v[210:213], v[10:13]
	v_mfma_f32_16x16x32_bf16 v[122:125], v[152:155], v[182:185], 0
	v_mfma_f32_16x16x32_bf16 v[110:113], v[160:163], v[182:185], 0
	v_mfma_f32_16x16x32_bf16 v[70:73], v[152:155], v[190:193], 0
	v_mfma_f32_16x16x32_bf16 v[58:61], v[160:163], v[190:193], 0
	v_mfma_f32_16x16x32_bf16 v[22:25], v[152:155], v[198:201], 0
	v_mfma_f32_16x16x32_bf16 v[18:21], v[160:163], v[198:201], 0
	v_mfma_f32_16x16x32_bf16 v[6:9], v[152:155], v[206:209], 0
	v_mfma_f32_16x16x32_bf16 v[2:5], v[160:163], v[206:209], 0
	v_mfma_f32_16x16x32_bf16 v[122:125], v[156:159], v[186:189], v[122:125]
	v_mfma_f32_16x16x32_bf16 v[110:113], v[178:181], v[186:189], v[110:113]
	v_mfma_f32_16x16x32_bf16 v[70:73], v[156:159], v[194:197], v[70:73]
	v_mfma_f32_16x16x32_bf16 v[58:61], v[178:181], v[194:197], v[58:61]
	v_mfma_f32_16x16x32_bf16 v[22:25], v[156:159], v[202:205], v[22:25]
	v_mfma_f32_16x16x32_bf16 v[18:21], v[178:181], v[202:205], v[18:21]
	v_mfma_f32_16x16x32_bf16 v[6:9], v[156:159], v[210:213], v[6:9]
	v_mfma_f32_16x16x32_bf16 v[2:5], v[178:181], v[210:213], v[2:5]
	s_setprio 0
	s_barrier
	s_branch .Lmid1046
.LBB0_1046:
	ds_read_b128 v[136:139], v172
	ds_read_b128 v[140:143], v172 offset:1024
	ds_read_b128 v[144:147], v172 offset:2048
	ds_read_b128 v[148:151], v172 offset:3072
	ds_read_b128 v[152:155], v173
	ds_read_b128 v[156:159], v173 offset:1024
	ds_read_b128 v[160:163], v173 offset:2048
	ds_read_b128 v[178:181], v173 offset:3072
	s_add_u32 s25, s64, s56
	s_addc_u32 s33, s65, s57
	s_add_u32 s66, s25, 0x100
	s_addc_u32 s67, s33, 0
	s_add_u32 s23, s62, s56
	s_addc_u32 s24, s63, s57
	s_add_u32 s28, s23, 0x100
	s_addc_u32 s29, s24, 0
	s_add_u32 s58, s25, 0x180
	s_addc_u32 s59, s33, 0
	ds_read_b128 v[182:185], v174
	ds_read_b128 v[186:189], v174 offset:1024
	ds_read_b128 v[190:193], v174 offset:2048
	ds_read_b128 v[194:197], v174 offset:3072
	ds_read_b128 v[198:201], v174 offset:4096
	ds_read_b128 v[202:205], v174 offset:5120
	ds_read_b128 v[206:209], v174 offset:6144
	ds_read_b128 v[210:213], v174 offset:7168
	s_add_u32 s30, s25, 0x40080
	s_addc_u32 s31, s33, 0
	s_mov_b32 s36, m0
	s_mov_b32 m0, s26
	s_nop 2
	global_load_lds_dwordx4 v165, s[30:31]
	s_mov_b32 m0, s36
	s_nop 0
	s_mov_b32 s36, m0
	s_mov_b32 m0, s27
	s_nop 2
	global_load_lds_dwordx4 v167, s[30:31]
	s_mov_b32 m0, s36
	s_waitcnt vmcnt(8) lgkmcnt(0)
	s_barrier
	s_setprio 1
	v_mfma_f32_16x16x32_bf16 v[26:29], v[136:139], v[182:185], v[26:29]
	v_mfma_f32_16x16x32_bf16 v[30:33], v[144:147], v[182:185], v[30:33]
	v_mfma_f32_16x16x32_bf16 v[50:53], v[136:139], v[190:193], v[50:53]
	v_mfma_f32_16x16x32_bf16 v[54:57], v[144:147], v[190:193], v[54:57]
	v_mfma_f32_16x16x32_bf16 v[74:77], v[136:139], v[198:201], v[74:77]
	v_mfma_f32_16x16x32_bf16 v[78:81], v[144:147], v[198:201], v[78:81]
	v_mfma_f32_16x16x32_bf16 v[94:97], v[136:139], v[206:209], v[94:97]
	v_mfma_f32_16x16x32_bf16 v[102:105], v[144:147], v[206:209], v[102:105]
	v_mfma_f32_16x16x32_bf16 v[26:29], v[140:143], v[186:189], v[26:29]
	v_mfma_f32_16x16x32_bf16 v[30:33], v[148:151], v[186:189], v[30:33]
	v_mfma_f32_16x16x32_bf16 v[50:53], v[140:143], v[194:197], v[50:53]
	v_mfma_f32_16x16x32_bf16 v[54:57], v[148:151], v[194:197], v[54:57]
	v_mfma_f32_16x16x32_bf16 v[74:77], v[140:143], v[202:205], v[74:77]
	v_mfma_f32_16x16x32_bf16 v[78:81], v[148:151], v[202:205], v[78:81]
	v_mfma_f32_16x16x32_bf16 v[94:97], v[140:143], v[210:213], v[94:97]
	v_mfma_f32_16x16x32_bf16 v[102:105], v[148:151], v[210:213], v[102:105]
	v_mfma_f32_16x16x32_bf16 v[38:41], v[152:155], v[182:185], v[38:41]
	v_mfma_f32_16x16x32_bf16 v[42:45], v[160:163], v[182:185], v[42:45]
	v_mfma_f32_16x16x32_bf16 v[62:65], v[152:155], v[190:193], v[62:65]
	v_mfma_f32_16x16x32_bf16 v[66:69], v[160:163], v[190:193], v[66:69]
	v_mfma_f32_16x16x32_bf16 v[82:85], v[152:155], v[198:201], v[82:85]
	v_mfma_f32_16x16x32_bf16 v[90:93], v[160:163], v[198:201], v[90:93]
	v_mfma_f32_16x16x32_bf16 v[106:109], v[152:155], v[206:209], v[106:109]
	v_mfma_f32_16x16x32_bf16 v[114:117], v[160:163], v[206:209], v[114:117]
	v_mfma_f32_16x16x32_bf16 v[38:41], v[156:159], v[186:189], v[38:41]
	v_mfma_f32_16x16x32_bf16 v[42:45], v[178:181], v[186:189], v[42:45]
	v_mfma_f32_16x16x32_bf16 v[62:65], v[156:159], v[194:197], v[62:65]
	v_mfma_f32_16x16x32_bf16 v[66:69], v[178:181], v[194:197], v[66:69]
	v_mfma_f32_16x16x32_bf16 v[82:85], v[156:159], v[202:205], v[82:85]
	v_mfma_f32_16x16x32_bf16 v[90:93], v[178:181], v[202:205], v[90:93]
	v_mfma_f32_16x16x32_bf16 v[106:109], v[156:159], v[210:213], v[106:109]
	v_mfma_f32_16x16x32_bf16 v[114:117], v[178:181], v[210:213], v[114:117]
	s_setprio 0
	s_barrier
	ds_read_b128 v[182:185], v174 offset:16384
	ds_read_b128 v[186:189], v174 offset:17408
	ds_read_b128 v[190:193], v174 offset:18432
	ds_read_b128 v[194:197], v174 offset:19456
	ds_read_b128 v[198:201], v174 offset:20480
	ds_read_b128 v[202:205], v174 offset:21504
	ds_read_b128 v[206:209], v174 offset:22528
	ds_read_b128 v[210:213], v174 offset:23552
	s_mov_b32 s30, m0
	s_mov_b32 m0, s80
	s_nop 2
	global_load_lds_dwordx4 v166, s[28:29]
	s_mov_b32 m0, s30
	s_nop 0
	s_mov_b32 s30, m0
	s_mov_b32 m0, s81
	s_nop 2
	global_load_lds_dwordx4 v168, s[28:29]
	s_mov_b32 m0, s30
	s_add_u32 s28, s23, 0x40100
	s_addc_u32 s29, s24, 0
	s_mov_b32 s30, m0
	s_mov_b32 m0, s82
	s_nop 2
	global_load_lds_dwordx4 v166, s[28:29]
	s_mov_b32 m0, s30
	s_nop 0
	s_mov_b32 s30, m0
	s_mov_b32 m0, s83
	s_nop 2
	global_load_lds_dwordx4 v168, s[28:29]
	s_mov_b32 m0, s30
	s_mov_b32 s28, m0
	s_mov_b32 m0, s79
	s_nop 2
	global_load_lds_dwordx4 v165, s[66:67]
	s_mov_b32 m0, s28
	s_nop 0
	s_mov_b32 s28, m0
	s_mov_b32 m0, s84
	s_nop 2
	global_load_lds_dwordx4 v167, s[66:67]
	s_mov_b32 m0, s28
	s_waitcnt vmcnt(8) lgkmcnt(0)
	s_barrier
	s_setprio 1
	v_mfma_f32_16x16x32_bf16 v[118:121], v[136:139], v[182:185], v[118:121]
	v_mfma_f32_16x16x32_bf16 v[126:129], v[144:147], v[182:185], v[126:129]
	v_mfma_f32_16x16x32_bf16 v[98:101], v[136:139], v[190:193], v[98:101]
	v_mfma_f32_16x16x32_bf16 v[86:89], v[144:147], v[190:193], v[86:89]
	v_mfma_f32_16x16x32_bf16 v[46:49], v[136:139], v[198:201], v[46:49]
	v_mfma_f32_16x16x32_bf16 v[34:37], v[144:147], v[198:201], v[34:37]
	v_mfma_f32_16x16x32_bf16 v[14:17], v[136:139], v[206:209], v[14:17]
	v_mfma_f32_16x16x32_bf16 v[10:13], v[144:147], v[206:209], v[10:13]
	v_mfma_f32_16x16x32_bf16 v[118:121], v[140:143], v[186:189], v[118:121]
	v_mfma_f32_16x16x32_bf16 v[126:129], v[148:151], v[186:189], v[126:129]
	v_mfma_f32_16x16x32_bf16 v[98:101], v[140:143], v[194:197], v[98:101]
	v_mfma_f32_16x16x32_bf16 v[86:89], v[148:151], v[194:197], v[86:89]
	v_mfma_f32_16x16x32_bf16 v[46:49], v[140:143], v[202:205], v[46:49]
	v_mfma_f32_16x16x32_bf16 v[34:37], v[148:151], v[202:205], v[34:37]
	v_mfma_f32_16x16x32_bf16 v[14:17], v[140:143], v[210:213], v[14:17]
	v_mfma_f32_16x16x32_bf16 v[10:13], v[148:151], v[210:213], v[10:13]
	v_mfma_f32_16x16x32_bf16 v[122:125], v[152:155], v[182:185], v[122:125]
	v_mfma_f32_16x16x32_bf16 v[110:113], v[160:163], v[182:185], v[110:113]
	v_mfma_f32_16x16x32_bf16 v[70:73], v[152:155], v[190:193], v[70:73]
	v_mfma_f32_16x16x32_bf16 v[58:61], v[160:163], v[190:193], v[58:61]
	v_mfma_f32_16x16x32_bf16 v[22:25], v[152:155], v[198:201], v[22:25]
	v_mfma_f32_16x16x32_bf16 v[18:21], v[160:163], v[198:201], v[18:21]
	v_mfma_f32_16x16x32_bf16 v[6:9], v[152:155], v[206:209], v[6:9]
	v_mfma_f32_16x16x32_bf16 v[2:5], v[160:163], v[206:209], v[2:5]
	v_mfma_f32_16x16x32_bf16 v[122:125], v[156:159], v[186:189], v[122:125]
	v_mfma_f32_16x16x32_bf16 v[110:113], v[178:181], v[186:189], v[110:113]
	v_mfma_f32_16x16x32_bf16 v[70:73], v[156:159], v[194:197], v[70:73]
	v_mfma_f32_16x16x32_bf16 v[58:61], v[178:181], v[194:197], v[58:61]
	v_mfma_f32_16x16x32_bf16 v[22:25], v[156:159], v[202:205], v[22:25]
	v_mfma_f32_16x16x32_bf16 v[18:21], v[178:181], v[202:205], v[18:21]
	v_mfma_f32_16x16x32_bf16 v[6:9], v[156:159], v[210:213], v[6:9]
	v_mfma_f32_16x16x32_bf16 v[2:5], v[178:181], v[210:213], v[2:5]
	s_setprio 0
	s_barrier
.Lmid1046:
	ds_read_b128 v[136:139], v175
	ds_read_b128 v[140:143], v175 offset:1024
	ds_read_b128 v[144:147], v175 offset:2048
	ds_read_b128 v[148:151], v175 offset:3072
	ds_read_b128 v[152:155], v176
	ds_read_b128 v[156:159], v176 offset:1024
	ds_read_b128 v[160:163], v176 offset:2048
	ds_read_b128 v[178:181], v176 offset:3072
	ds_read_b128 v[182:185], v174 offset:32768
	ds_read_b128 v[186:189], v174 offset:33792
	ds_read_b128 v[190:193], v174 offset:34816
	ds_read_b128 v[194:197], v174 offset:35840
	ds_read_b128 v[198:201], v174 offset:36864
	ds_read_b128 v[202:205], v174 offset:37888
	ds_read_b128 v[206:209], v174 offset:38912
	ds_read_b128 v[210:213], v174 offset:39936
	s_add_u32 s28, s25, 0x40100
	s_addc_u32 s29, s33, 0
	s_mov_b32 s25, m0
	s_mov_b32 m0, s85
	s_nop 2
	global_load_lds_dwordx4 v165, s[28:29]
	s_mov_b32 m0, s25
	s_nop 0
	s_mov_b32 s25, m0
	s_mov_b32 m0, s86
	s_nop 2
	global_load_lds_dwordx4 v167, s[28:29]
	s_mov_b32 m0, s25
	s_waitcnt vmcnt(8) lgkmcnt(0)
	s_barrier
	s_setprio 1
	v_mfma_f32_16x16x32_bf16 v[26:29], v[136:139], v[182:185], v[26:29]
	v_mfma_f32_16x16x32_bf16 v[30:33], v[144:147], v[182:185], v[30:33]
	v_mfma_f32_16x16x32_bf16 v[50:53], v[136:139], v[190:193], v[50:53]
	v_mfma_f32_16x16x32_bf16 v[54:57], v[144:147], v[190:193], v[54:57]
	v_mfma_f32_16x16x32_bf16 v[74:77], v[136:139], v[198:201], v[74:77]
	v_mfma_f32_16x16x32_bf16 v[78:81], v[144:147], v[198:201], v[78:81]
	v_mfma_f32_16x16x32_bf16 v[94:97], v[136:139], v[206:209], v[94:97]
	v_mfma_f32_16x16x32_bf16 v[102:105], v[144:147], v[206:209], v[102:105]
	v_mfma_f32_16x16x32_bf16 v[26:29], v[140:143], v[186:189], v[26:29]
	v_mfma_f32_16x16x32_bf16 v[30:33], v[148:151], v[186:189], v[30:33]
	v_mfma_f32_16x16x32_bf16 v[50:53], v[140:143], v[194:197], v[50:53]
	v_mfma_f32_16x16x32_bf16 v[54:57], v[148:151], v[194:197], v[54:57]
	v_mfma_f32_16x16x32_bf16 v[74:77], v[140:143], v[202:205], v[74:77]
	v_mfma_f32_16x16x32_bf16 v[78:81], v[148:151], v[202:205], v[78:81]
	v_mfma_f32_16x16x32_bf16 v[94:97], v[140:143], v[210:213], v[94:97]
	v_mfma_f32_16x16x32_bf16 v[102:105], v[148:151], v[210:213], v[102:105]
	v_mfma_f32_16x16x32_bf16 v[38:41], v[152:155], v[182:185], v[38:41]
	v_mfma_f32_16x16x32_bf16 v[42:45], v[160:163], v[182:185], v[42:45]
	v_mfma_f32_16x16x32_bf16 v[62:65], v[152:155], v[190:193], v[62:65]
	v_mfma_f32_16x16x32_bf16 v[66:69], v[160:163], v[190:193], v[66:69]
	v_mfma_f32_16x16x32_bf16 v[82:85], v[152:155], v[198:201], v[82:85]
	v_mfma_f32_16x16x32_bf16 v[90:93], v[160:163], v[198:201], v[90:93]
	v_mfma_f32_16x16x32_bf16 v[106:109], v[152:155], v[206:209], v[106:109]
	v_mfma_f32_16x16x32_bf16 v[114:117], v[160:163], v[206:209], v[114:117]
	v_mfma_f32_16x16x32_bf16 v[38:41], v[156:159], v[186:189], v[38:41]
	v_mfma_f32_16x16x32_bf16 v[42:45], v[178:181], v[186:189], v[42:45]
	v_mfma_f32_16x16x32_bf16 v[62:65], v[156:159], v[194:197], v[62:65]
	v_mfma_f32_16x16x32_bf16 v[66:69], v[178:181], v[194:197], v[66:69]
	v_mfma_f32_16x16x32_bf16 v[82:85], v[156:159], v[202:205], v[82:85]
	v_mfma_f32_16x16x32_bf16 v[90:93], v[178:181], v[202:205], v[90:93]
	v_mfma_f32_16x16x32_bf16 v[106:109], v[156:159], v[210:213], v[106:109]
	v_mfma_f32_16x16x32_bf16 v[114:117], v[178:181], v[210:213], v[114:117]
	s_setprio 0
	s_barrier
	ds_read_b128 v[182:185], v174 offset:49152
	ds_read_b128 v[186:189], v174 offset:50176
	ds_read_b128 v[190:193], v174 offset:51200
	ds_read_b128 v[194:197], v174 offset:52224
	ds_read_b128 v[198:201], v174 offset:53248
	ds_read_b128 v[202:205], v174 offset:54272
	ds_read_b128 v[206:209], v174 offset:55296
	ds_read_b128 v[210:213], v174 offset:56320
	s_add_u32 s28, s23, 0x180
	s_addc_u32 s29, s24, 0
	s_mov_b32 s25, m0
	s_mov_b32 m0, s92
	s_nop 2
	global_load_lds_dwordx4 v166, s[28:29]
	s_mov_b32 m0, s25
	s_nop 0
	s_mov_b32 s25, m0
	s_mov_b32 m0, s93
	s_nop 2
	global_load_lds_dwordx4 v168, s[28:29]
	s_mov_b32 m0, s25
	s_add_u32 s28, s23, 0x40180
	s_addc_u32 s29, s24, 0
	s_mov_b32 s23, m0
	s_mov_b32 m0, s96
	s_nop 2
	global_load_lds_dwordx4 v166, s[28:29]
	s_mov_b32 m0, s23
	s_nop 0
	s_mov_b32 s23, m0
	s_mov_b32 m0, s97
	s_nop 2
	global_load_lds_dwordx4 v168, s[28:29]
	s_mov_b32 m0, s23
	s_nop 0
	s_mov_b32 s23, m0
	s_mov_b32 m0, s94
	s_nop 2
	global_load_lds_dwordx4 v165, s[58:59]
	s_mov_b32 m0, s23
	s_nop 0
	s_mov_b32 s23, m0
	s_mov_b32 m0, s95
	s_nop 2
	global_load_lds_dwordx4 v167, s[58:59]
	s_mov_b32 m0, s23
	s_waitcnt vmcnt(8) lgkmcnt(0)
	s_barrier
	s_setprio 1
	v_mfma_f32_16x16x32_bf16 v[118:121], v[136:139], v[182:185], v[118:121]
	v_mfma_f32_16x16x32_bf16 v[126:129], v[144:147], v[182:185], v[126:129]
	v_mfma_f32_16x16x32_bf16 v[98:101], v[136:139], v[190:193], v[98:101]
	v_mfma_f32_16x16x32_bf16 v[86:89], v[144:147], v[190:193], v[86:89]
	v_mfma_f32_16x16x32_bf16 v[46:49], v[136:139], v[198:201], v[46:49]
	v_mfma_f32_16x16x32_bf16 v[34:37], v[144:147], v[198:201], v[34:37]
	v_mfma_f32_16x16x32_bf16 v[14:17], v[136:139], v[206:209], v[14:17]
	v_mfma_f32_16x16x32_bf16 v[10:13], v[144:147], v[206:209], v[10:13]
	v_mfma_f32_16x16x32_bf16 v[118:121], v[140:143], v[186:189], v[118:121]
	v_mfma_f32_16x16x32_bf16 v[126:129], v[148:151], v[186:189], v[126:129]
	v_mfma_f32_16x16x32_bf16 v[98:101], v[140:143], v[194:197], v[98:101]
	v_mfma_f32_16x16x32_bf16 v[86:89], v[148:151], v[194:197], v[86:89]
	v_mfma_f32_16x16x32_bf16 v[46:49], v[140:143], v[202:205], v[46:49]
	v_mfma_f32_16x16x32_bf16 v[34:37], v[148:151], v[202:205], v[34:37]
	v_mfma_f32_16x16x32_bf16 v[14:17], v[140:143], v[210:213], v[14:17]
	v_mfma_f32_16x16x32_bf16 v[10:13], v[148:151], v[210:213], v[10:13]
	v_mfma_f32_16x16x32_bf16 v[122:125], v[152:155], v[182:185], v[122:125]
	v_mfma_f32_16x16x32_bf16 v[110:113], v[160:163], v[182:185], v[110:113]
	v_mfma_f32_16x16x32_bf16 v[70:73], v[152:155], v[190:193], v[70:73]
	v_mfma_f32_16x16x32_bf16 v[58:61], v[160:163], v[190:193], v[58:61]
	v_mfma_f32_16x16x32_bf16 v[22:25], v[152:155], v[198:201], v[22:25]
	v_mfma_f32_16x16x32_bf16 v[18:21], v[160:163], v[198:201], v[18:21]
	v_mfma_f32_16x16x32_bf16 v[6:9], v[152:155], v[206:209], v[6:9]
	v_mfma_f32_16x16x32_bf16 v[2:5], v[160:163], v[206:209], v[2:5]
	v_mfma_f32_16x16x32_bf16 v[122:125], v[156:159], v[186:189], v[122:125]
	v_mfma_f32_16x16x32_bf16 v[110:113], v[178:181], v[186:189], v[110:113]
	v_mfma_f32_16x16x32_bf16 v[70:73], v[156:159], v[194:197], v[70:73]
	v_mfma_f32_16x16x32_bf16 v[58:61], v[178:181], v[194:197], v[58:61]
	v_mfma_f32_16x16x32_bf16 v[22:25], v[156:159], v[202:205], v[22:25]
	v_mfma_f32_16x16x32_bf16 v[18:21], v[178:181], v[202:205], v[18:21]
	v_mfma_f32_16x16x32_bf16 v[6:9], v[156:159], v[210:213], v[6:9]
	v_mfma_f32_16x16x32_bf16 v[2:5], v[178:181], v[210:213], v[2:5]
	s_setprio 0
	s_barrier
	s_add_i32 s3, s3, 2
	s_add_u32 s56, s56, 0x100
	s_addc_u32 s57, s57, 0
	s_cmp_gt_u32 s3, 5
	s_cbranch_scc0 .LBB0_1046
	s_ashr_i32 s55, s54, 31
	s_lshl_b64 s[24:25], s[54:55], 19
	s_add_u32 s56, s69, s24
	s_addc_u32 s57, s76, s25
	s_ashr_i32 s23, s22, 31
	s_lshl_b64 s[24:25], s[22:23], 19
	s_add_u32 s58, s77, s24
	s_addc_u32 s59, s78, s25
	s_lshl_b32 s3, s60, 18
	s_lshl_b32 s23, s2, 8
	s_lshl_b32 s32, s2, 16
	s_add_i32 s2, s32, s3
	v_lshrrev_b32_e32 v214, 6, v0
	v_lshlrev_b32_e32 v214, 13, v214
	v_and_b32_e32 v215, 63, v0
	v_lshl_add_u32 v214, v215, 3, v214
	v_add_u32_e32 v134, s2, v214
	s_cmp_lg_u32 s37, 0
	s_cbranch_scc1 .Lmpf_have
	global_load_dwordx2 v[162:163], v134, s[14:15]
	global_load_dwordx2 v[178:179], v134, s[16:17]
	v_or_b32_e32 v136, 0x200, v134
	v_add_u32_e32 v137, 0x400, v134
	v_add_u32_e32 v138, 0x600, v134
	v_add_u32_e32 v139, 0x800, v134
	v_add_u32_e32 v140, 0xa00, v134
	v_add_u32_e32 v141, 0xc00, v134
	v_add_u32_e32 v161, 0xe00, v134
	global_load_dwordx2 v[180:181], v136, s[14:15]
	global_load_dwordx2 v[182:183], v136, s[16:17]
	global_load_dwordx2 v[158:159], v137, s[14:15]
	global_load_dwordx2 v[156:157], v137, s[16:17]
	global_load_dwordx2 v[154:155], v138, s[14:15]
	global_load_dwordx2 v[152:153], v138, s[16:17]
	global_load_dwordx2 v[150:151], v139, s[14:15]
	global_load_dwordx2 v[148:149], v139, s[16:17]
	global_load_dwordx2 v[146:147], v140, s[14:15]
	global_load_dwordx2 v[144:145], v140, s[16:17]
	global_load_dwordx2 v[142:143], v141, s[14:15]
	s_nop 0
	global_load_dwordx2 v[140:141], v141, s[16:17]
	s_nop 0
	global_load_dwordx2 v[138:139], v161, s[14:15]
	global_load_dwordx2 v[136:137], v161, s[16:17]
	s_branch .Lmpf_join

.LBB0_1048:
	ds_read_b128 v[136:139], v172
	ds_read_b128 v[140:143], v172 offset:1024
	ds_read_b128 v[144:147], v172 offset:2048
	ds_read_b128 v[148:151], v172 offset:3072
	ds_read_b128 v[152:155], v173
	ds_read_b128 v[156:159], v173 offset:1024
	ds_read_b128 v[160:163], v173 offset:2048
	ds_read_b128 v[178:181], v173 offset:3072
	s_cmp_eq_u32 s33, 12
	s_cselect_b32 s66, s3, s28
	s_cselect_b32 s67, s2, s29
	s_cselect_b32 s64, s25, s30
	s_cselect_b32 s65, s24, s31
	s_add_u32 s62, s66, 0x80
	s_addc_u32 s63, s67, 0
	ds_read_b128 v[182:185], v174
	ds_read_b128 v[186:189], v174 offset:1024
	ds_read_b128 v[190:193], v174 offset:2048
	ds_read_b128 v[194:197], v174 offset:3072
	ds_read_b128 v[198:201], v174 offset:4096
	ds_read_b128 v[202:205], v174 offset:5120
	ds_read_b128 v[206:209], v174 offset:6144
	ds_read_b128 v[210:213], v174 offset:7168
	s_add_u32 s36, s28, 0x3ff80
	s_addc_u32 s37, s29, 0
	s_mov_b32 s52, m0
	s_mov_b32 m0, s26
	s_nop 2
	global_load_lds_dwordx4 v165, s[36:37]
	s_mov_b32 m0, s52
	s_nop 0
	s_mov_b32 s52, m0
	s_mov_b32 m0, s27
	s_nop 2
	global_load_lds_dwordx4 v167, s[36:37]
	s_mov_b32 m0, s52
	s_waitcnt vmcnt(8) lgkmcnt(0)
	s_barrier
	s_setprio 1
	v_mfma_f32_16x16x32_bf16 v[26:29], v[136:139], v[182:185], v[26:29]
	v_mfma_f32_16x16x32_bf16 v[30:33], v[144:147], v[182:185], v[30:33]
	v_mfma_f32_16x16x32_bf16 v[50:53], v[136:139], v[190:193], v[50:53]
	v_mfma_f32_16x16x32_bf16 v[54:57], v[144:147], v[190:193], v[54:57]
	v_mfma_f32_16x16x32_bf16 v[74:77], v[136:139], v[198:201], v[74:77]
	v_mfma_f32_16x16x32_bf16 v[78:81], v[144:147], v[198:201], v[78:81]
	v_mfma_f32_16x16x32_bf16 v[94:97], v[136:139], v[206:209], v[94:97]
	v_mfma_f32_16x16x32_bf16 v[102:105], v[144:147], v[206:209], v[102:105]
	v_mfma_f32_16x16x32_bf16 v[26:29], v[140:143], v[186:189], v[26:29]
	v_mfma_f32_16x16x32_bf16 v[30:33], v[148:151], v[186:189], v[30:33]
	v_mfma_f32_16x16x32_bf16 v[50:53], v[140:143], v[194:197], v[50:53]
	v_mfma_f32_16x16x32_bf16 v[54:57], v[148:151], v[194:197], v[54:57]
	v_mfma_f32_16x16x32_bf16 v[74:77], v[140:143], v[202:205], v[74:77]
	v_mfma_f32_16x16x32_bf16 v[78:81], v[148:151], v[202:205], v[78:81]
	v_mfma_f32_16x16x32_bf16 v[94:97], v[140:143], v[210:213], v[94:97]
	v_mfma_f32_16x16x32_bf16 v[102:105], v[148:151], v[210:213], v[102:105]
	v_mfma_f32_16x16x32_bf16 v[38:41], v[152:155], v[182:185], v[38:41]
	v_mfma_f32_16x16x32_bf16 v[42:45], v[160:163], v[182:185], v[42:45]
	v_mfma_f32_16x16x32_bf16 v[62:65], v[152:155], v[190:193], v[62:65]
	v_mfma_f32_16x16x32_bf16 v[66:69], v[160:163], v[190:193], v[66:69]
	v_mfma_f32_16x16x32_bf16 v[82:85], v[152:155], v[198:201], v[82:85]
	v_mfma_f32_16x16x32_bf16 v[90:93], v[160:163], v[198:201], v[90:93]
	v_mfma_f32_16x16x32_bf16 v[106:109], v[152:155], v[206:209], v[106:109]
	v_mfma_f32_16x16x32_bf16 v[114:117], v[160:163], v[206:209], v[114:117]
	v_mfma_f32_16x16x32_bf16 v[38:41], v[156:159], v[186:189], v[38:41]
	v_mfma_f32_16x16x32_bf16 v[42:45], v[178:181], v[186:189], v[42:45]
	v_mfma_f32_16x16x32_bf16 v[62:65], v[156:159], v[194:197], v[62:65]
	v_mfma_f32_16x16x32_bf16 v[66:69], v[178:181], v[194:197], v[66:69]
	v_mfma_f32_16x16x32_bf16 v[82:85], v[156:159], v[202:205], v[82:85]
	v_mfma_f32_16x16x32_bf16 v[90:93], v[178:181], v[202:205], v[90:93]
	v_mfma_f32_16x16x32_bf16 v[106:109], v[156:159], v[210:213], v[106:109]
	v_mfma_f32_16x16x32_bf16 v[114:117], v[178:181], v[210:213], v[114:117]
	s_setprio 0
	s_barrier
	ds_read_b128 v[182:185], v174 offset:16384
	ds_read_b128 v[186:189], v174 offset:17408
	ds_read_b128 v[190:193], v174 offset:18432
	ds_read_b128 v[194:197], v174 offset:19456
	ds_read_b128 v[198:201], v174 offset:20480
	ds_read_b128 v[202:205], v174 offset:21504
	ds_read_b128 v[206:209], v174 offset:22528
	ds_read_b128 v[210:213], v174 offset:23552
	s_mov_b32 s36, m0
	s_mov_b32 m0, s80
	s_nop 2
	global_load_lds_dwordx4 v166, s[64:65]
	s_mov_b32 m0, s36
	s_nop 0
	s_mov_b32 s36, m0
	s_mov_b32 m0, s81
	s_nop 2
	global_load_lds_dwordx4 v168, s[64:65]
	s_mov_b32 m0, s36
	s_add_u32 s36, s64, 0x40000
	s_addc_u32 s37, s65, 0
	s_mov_b32 s52, m0
	s_mov_b32 m0, s82
	s_nop 2
	global_load_lds_dwordx4 v166, s[36:37]
	s_mov_b32 m0, s52
	s_nop 0
	s_mov_b32 s52, m0
	s_mov_b32 m0, s83
	s_nop 2
	global_load_lds_dwordx4 v168, s[36:37]
	s_mov_b32 m0, s52
	s_mov_b32 s36, m0
	s_mov_b32 m0, s79
	s_nop 2
	global_load_lds_dwordx4 v165, s[66:67]
	s_mov_b32 m0, s36
	s_nop 0
	s_mov_b32 s36, m0
	s_mov_b32 m0, s84
	s_nop 2
	global_load_lds_dwordx4 v167, s[66:67]
	s_mov_b32 m0, s36
	s_waitcnt vmcnt(8) lgkmcnt(0)
	s_barrier
	s_setprio 1
	v_mfma_f32_16x16x32_bf16 v[118:121], v[136:139], v[182:185], v[118:121]
	v_mfma_f32_16x16x32_bf16 v[126:129], v[144:147], v[182:185], v[126:129]
	v_mfma_f32_16x16x32_bf16 v[98:101], v[136:139], v[190:193], v[98:101]
	v_mfma_f32_16x16x32_bf16 v[86:89], v[144:147], v[190:193], v[86:89]
	v_mfma_f32_16x16x32_bf16 v[46:49], v[136:139], v[198:201], v[46:49]
	v_mfma_f32_16x16x32_bf16 v[34:37], v[144:147], v[198:201], v[34:37]
	v_mfma_f32_16x16x32_bf16 v[14:17], v[136:139], v[206:209], v[14:17]
	v_mfma_f32_16x16x32_bf16 v[10:13], v[144:147], v[206:209], v[10:13]
	v_mfma_f32_16x16x32_bf16 v[118:121], v[140:143], v[186:189], v[118:121]
	v_mfma_f32_16x16x32_bf16 v[126:129], v[148:151], v[186:189], v[126:129]
	v_mfma_f32_16x16x32_bf16 v[98:101], v[140:143], v[194:197], v[98:101]
	v_mfma_f32_16x16x32_bf16 v[86:89], v[148:151], v[194:197], v[86:89]
	v_mfma_f32_16x16x32_bf16 v[46:49], v[140:143], v[202:205], v[46:49]
	v_mfma_f32_16x16x32_bf16 v[34:37], v[148:151], v[202:205], v[34:37]
	v_mfma_f32_16x16x32_bf16 v[14:17], v[140:143], v[210:213], v[14:17]
	v_mfma_f32_16x16x32_bf16 v[10:13], v[148:151], v[210:213], v[10:13]
	v_mfma_f32_16x16x32_bf16 v[122:125], v[152:155], v[182:185], v[122:125]
	v_mfma_f32_16x16x32_bf16 v[110:113], v[160:163], v[182:185], v[110:113]
	v_mfma_f32_16x16x32_bf16 v[70:73], v[152:155], v[190:193], v[70:73]
	v_mfma_f32_16x16x32_bf16 v[58:61], v[160:163], v[190:193], v[58:61]
	v_mfma_f32_16x16x32_bf16 v[22:25], v[152:155], v[198:201], v[22:25]
	v_mfma_f32_16x16x32_bf16 v[18:21], v[160:163], v[198:201], v[18:21]
	v_mfma_f32_16x16x32_bf16 v[6:9], v[152:155], v[206:209], v[6:9]
	v_mfma_f32_16x16x32_bf16 v[2:5], v[160:163], v[206:209], v[2:5]
	v_mfma_f32_16x16x32_bf16 v[122:125], v[156:159], v[186:189], v[122:125]
	v_mfma_f32_16x16x32_bf16 v[110:113], v[178:181], v[186:189], v[110:113]
	v_mfma_f32_16x16x32_bf16 v[70:73], v[156:159], v[194:197], v[70:73]
	v_mfma_f32_16x16x32_bf16 v[58:61], v[178:181], v[194:197], v[58:61]
	v_mfma_f32_16x16x32_bf16 v[22:25], v[156:159], v[202:205], v[22:25]
	v_mfma_f32_16x16x32_bf16 v[18:21], v[178:181], v[202:205], v[18:21]
	v_mfma_f32_16x16x32_bf16 v[6:9], v[156:159], v[210:213], v[6:9]
	v_mfma_f32_16x16x32_bf16 v[2:5], v[178:181], v[210:213], v[2:5]
	s_setprio 0
	s_barrier
	ds_read_b128 v[136:139], v175
	ds_read_b128 v[140:143], v175 offset:1024
	ds_read_b128 v[144:147], v175 offset:2048
	ds_read_b128 v[148:151], v175 offset:3072
	ds_read_b128 v[152:155], v176
	ds_read_b128 v[156:159], v176 offset:1024
	ds_read_b128 v[160:163], v176 offset:2048
	ds_read_b128 v[178:181], v176 offset:3072
	ds_read_b128 v[182:185], v174 offset:32768
	ds_read_b128 v[186:189], v174 offset:33792
	ds_read_b128 v[190:193], v174 offset:34816
	ds_read_b128 v[194:197], v174 offset:35840
	ds_read_b128 v[198:201], v174 offset:36864
	ds_read_b128 v[202:205], v174 offset:37888
	ds_read_b128 v[206:209], v174 offset:38912
	ds_read_b128 v[210:213], v174 offset:39936
	s_add_u32 s36, s66, 0x40000
	s_addc_u32 s37, s67, 0
	s_mov_b32 s52, m0
	s_mov_b32 m0, s85
	s_nop 2
	global_load_lds_dwordx4 v165, s[36:37]
	s_mov_b32 m0, s52
	s_nop 0
	s_mov_b32 s52, m0
	s_mov_b32 m0, s86
	s_nop 2
	global_load_lds_dwordx4 v167, s[36:37]
	s_mov_b32 m0, s52
	s_waitcnt vmcnt(8) lgkmcnt(0)
	s_barrier
	s_setprio 1
	v_mfma_f32_16x16x32_bf16 v[26:29], v[136:139], v[182:185], v[26:29]
	v_mfma_f32_16x16x32_bf16 v[30:33], v[144:147], v[182:185], v[30:33]
	v_mfma_f32_16x16x32_bf16 v[50:53], v[136:139], v[190:193], v[50:53]
	v_mfma_f32_16x16x32_bf16 v[54:57], v[144:147], v[190:193], v[54:57]
	v_mfma_f32_16x16x32_bf16 v[74:77], v[136:139], v[198:201], v[74:77]
	v_mfma_f32_16x16x32_bf16 v[78:81], v[144:147], v[198:201], v[78:81]
	v_mfma_f32_16x16x32_bf16 v[94:97], v[136:139], v[206:209], v[94:97]
	v_mfma_f32_16x16x32_bf16 v[102:105], v[144:147], v[206:209], v[102:105]
	v_mfma_f32_16x16x32_bf16 v[26:29], v[140:143], v[186:189], v[26:29]
	v_mfma_f32_16x16x32_bf16 v[30:33], v[148:151], v[186:189], v[30:33]
	v_mfma_f32_16x16x32_bf16 v[50:53], v[140:143], v[194:197], v[50:53]
	v_mfma_f32_16x16x32_bf16 v[54:57], v[148:151], v[194:197], v[54:57]
	v_mfma_f32_16x16x32_bf16 v[74:77], v[140:143], v[202:205], v[74:77]
	v_mfma_f32_16x16x32_bf16 v[78:81], v[148:151], v[202:205], v[78:81]
	v_mfma_f32_16x16x32_bf16 v[94:97], v[140:143], v[210:213], v[94:97]
	v_mfma_f32_16x16x32_bf16 v[102:105], v[148:151], v[210:213], v[102:105]
	v_mfma_f32_16x16x32_bf16 v[38:41], v[152:155], v[182:185], v[38:41]
	v_mfma_f32_16x16x32_bf16 v[42:45], v[160:163], v[182:185], v[42:45]
	v_mfma_f32_16x16x32_bf16 v[62:65], v[152:155], v[190:193], v[62:65]
	v_mfma_f32_16x16x32_bf16 v[66:69], v[160:163], v[190:193], v[66:69]
	v_mfma_f32_16x16x32_bf16 v[82:85], v[152:155], v[198:201], v[82:85]
	v_mfma_f32_16x16x32_bf16 v[90:93], v[160:163], v[198:201], v[90:93]
	v_mfma_f32_16x16x32_bf16 v[106:109], v[152:155], v[206:209], v[106:109]
	v_mfma_f32_16x16x32_bf16 v[114:117], v[160:163], v[206:209], v[114:117]
	v_mfma_f32_16x16x32_bf16 v[38:41], v[156:159], v[186:189], v[38:41]
	v_mfma_f32_16x16x32_bf16 v[42:45], v[178:181], v[186:189], v[42:45]
	v_mfma_f32_16x16x32_bf16 v[62:65], v[156:159], v[194:197], v[62:65]
	v_mfma_f32_16x16x32_bf16 v[66:69], v[178:181], v[194:197], v[66:69]
	v_mfma_f32_16x16x32_bf16 v[82:85], v[156:159], v[202:205], v[82:85]
	v_mfma_f32_16x16x32_bf16 v[90:93], v[178:181], v[202:205], v[90:93]
	v_mfma_f32_16x16x32_bf16 v[106:109], v[156:159], v[210:213], v[106:109]
	v_mfma_f32_16x16x32_bf16 v[114:117], v[178:181], v[210:213], v[114:117]
	s_setprio 0
	s_barrier
	ds_read_b128 v[182:185], v174 offset:49152
	ds_read_b128 v[186:189], v174 offset:50176
	ds_read_b128 v[190:193], v174 offset:51200
	ds_read_b128 v[194:197], v174 offset:52224
	ds_read_b128 v[198:201], v174 offset:53248
	ds_read_b128 v[202:205], v174 offset:54272
	ds_read_b128 v[206:209], v174 offset:55296
	ds_read_b128 v[210:213], v174 offset:56320
	s_add_u32 s36, s64, 0x80
	s_addc_u32 s37, s65, 0
	s_mov_b32 s52, m0
	s_mov_b32 m0, s92
	s_nop 2
	global_load_lds_dwordx4 v166, s[36:37]
	s_mov_b32 m0, s52
	s_nop 0
	s_mov_b32 s52, m0
	s_mov_b32 m0, s93
	s_nop 2
	global_load_lds_dwordx4 v168, s[36:37]
	s_mov_b32 m0, s52
	s_add_u32 s36, s64, 0x40080
	s_addc_u32 s37, s65, 0
	s_mov_b32 s52, m0
	s_mov_b32 m0, s96
	s_nop 2
	global_load_lds_dwordx4 v166, s[36:37]
	s_mov_b32 m0, s52
	s_nop 0
	s_mov_b32 s52, m0
	s_mov_b32 m0, s97
	s_nop 2
	global_load_lds_dwordx4 v168, s[36:37]
	s_mov_b32 m0, s52
	s_mov_b32 s36, m0
	s_mov_b32 m0, s94
	s_nop 2
	global_load_lds_dwordx4 v165, s[62:63]
	s_mov_b32 m0, s36
	s_nop 0
	s_mov_b32 s36, m0
	s_mov_b32 m0, s95
	s_nop 2
	global_load_lds_dwordx4 v167, s[62:63]
	s_mov_b32 m0, s36
	s_waitcnt vmcnt(8) lgkmcnt(0)
	s_barrier
	s_setprio 1
	v_mfma_f32_16x16x32_bf16 v[118:121], v[136:139], v[182:185], v[118:121]
	v_mfma_f32_16x16x32_bf16 v[126:129], v[144:147], v[182:185], v[126:129]
	v_mfma_f32_16x16x32_bf16 v[98:101], v[136:139], v[190:193], v[98:101]
	v_mfma_f32_16x16x32_bf16 v[86:89], v[144:147], v[190:193], v[86:89]
	v_mfma_f32_16x16x32_bf16 v[46:49], v[136:139], v[198:201], v[46:49]
	v_mfma_f32_16x16x32_bf16 v[34:37], v[144:147], v[198:201], v[34:37]
	v_mfma_f32_16x16x32_bf16 v[14:17], v[136:139], v[206:209], v[14:17]
	v_mfma_f32_16x16x32_bf16 v[10:13], v[144:147], v[206:209], v[10:13]
	v_mfma_f32_16x16x32_bf16 v[118:121], v[140:143], v[186:189], v[118:121]
	v_mfma_f32_16x16x32_bf16 v[126:129], v[148:151], v[186:189], v[126:129]
	v_mfma_f32_16x16x32_bf16 v[98:101], v[140:143], v[194:197], v[98:101]
	v_mfma_f32_16x16x32_bf16 v[86:89], v[148:151], v[194:197], v[86:89]
	v_mfma_f32_16x16x32_bf16 v[46:49], v[140:143], v[202:205], v[46:49]
	v_mfma_f32_16x16x32_bf16 v[34:37], v[148:151], v[202:205], v[34:37]
	v_mfma_f32_16x16x32_bf16 v[14:17], v[140:143], v[210:213], v[14:17]
	v_mfma_f32_16x16x32_bf16 v[10:13], v[148:151], v[210:213], v[10:13]
	v_mfma_f32_16x16x32_bf16 v[122:125], v[152:155], v[182:185], v[122:125]
	v_mfma_f32_16x16x32_bf16 v[110:113], v[160:163], v[182:185], v[110:113]
	v_mfma_f32_16x16x32_bf16 v[70:73], v[152:155], v[190:193], v[70:73]
	v_mfma_f32_16x16x32_bf16 v[58:61], v[160:163], v[190:193], v[58:61]
	v_mfma_f32_16x16x32_bf16 v[22:25], v[152:155], v[198:201], v[22:25]
	v_mfma_f32_16x16x32_bf16 v[18:21], v[160:163], v[198:201], v[18:21]
	v_mfma_f32_16x16x32_bf16 v[6:9], v[152:155], v[206:209], v[6:9]
	v_mfma_f32_16x16x32_bf16 v[2:5], v[160:163], v[206:209], v[2:5]
	v_mfma_f32_16x16x32_bf16 v[122:125], v[156:159], v[186:189], v[122:125]
	v_mfma_f32_16x16x32_bf16 v[110:113], v[178:181], v[186:189], v[110:113]
	v_mfma_f32_16x16x32_bf16 v[70:73], v[156:159], v[194:197], v[70:73]
	v_mfma_f32_16x16x32_bf16 v[58:61], v[178:181], v[194:197], v[58:61]
	v_mfma_f32_16x16x32_bf16 v[22:25], v[156:159], v[202:205], v[22:25]
	v_mfma_f32_16x16x32_bf16 v[18:21], v[178:181], v[202:205], v[18:21]
	v_mfma_f32_16x16x32_bf16 v[6:9], v[156:159], v[210:213], v[6:9]
	v_mfma_f32_16x16x32_bf16 v[2:5], v[178:181], v[210:213], v[2:5]
	s_setprio 0
	s_barrier
	s_add_i32 s33, s33, 2
	s_add_u32 s28, s28, 0x100
	s_addc_u32 s29, s29, 0
	s_add_u32 s30, s30, 0x100
	s_addc_u32 s31, s31, 0
	s_cmp_lt_u32 s33, 14
	s_cbranch_scc1 .LBB0_1048
	s_and_b64 vcc, exec, s[20:21]
	s_cbranch_vccz .LBB0_1051
	s_barrier

.Lpeel1440:
	ds_read_b128 v[130:133], v234
	ds_read_b128 v[134:137], v234 offset:1024
	ds_read_b128 v[138:141], v234 offset:2048
	ds_read_b128 v[142:145], v234 offset:3072
	ds_read_b128 v[146:149], v235
	ds_read_b128 v[150:153], v235 offset:1024
	ds_read_b128 v[154:157], v235 offset:2048
	ds_read_b128 v[158:161], v235 offset:3072
	s_add_u32 s60, s58, 0x100
	s_addc_u32 s61, s59, 0
	s_cmp_eq_u32 s87, 12
	s_cselect_b32 s66, s33, s60
	s_cselect_b32 s67, s21, s61
	s_cselect_b32 s64, s84, s85
	s_cselect_b32 s65, s19, s86
	s_add_u32 s62, s66, 0x80
	s_addc_u32 s63, s67, 0
	ds_read_b128 v[162:165], v236
	ds_read_b128 v[166:169], v236 offset:1024
	ds_read_b128 v[170:173], v236 offset:2048
	ds_read_b128 v[174:177], v236 offset:3072
	ds_read_b128 v[178:181], v236 offset:4096
	ds_read_b128 v[182:185], v236 offset:5120
	ds_read_b128 v[186:189], v236 offset:6144
	ds_read_b128 v[190:193], v236 offset:7168
	s_add_u32 s58, s58, 0x40080
	s_addc_u32 s59, s59, 0
	s_mov_b32 s88, m0
	s_mov_b32 m0, s80
	s_nop 2
	global_load_lds_dwordx4 v228, s[58:59]
	s_mov_b32 m0, s88
	s_nop 0
	s_mov_b32 s88, m0
	s_mov_b32 m0, s81
	s_nop 2
	global_load_lds_dwordx4 v230, s[58:59]
	s_mov_b32 m0, s88
	s_waitcnt vmcnt(8) lgkmcnt(0)
	s_barrier
	s_setprio 1
	v_mfma_f32_16x16x32_bf16 v[126:129], v[130:133], v[162:165], 0
	v_mfma_f32_16x16x32_bf16 v[122:125], v[138:141], v[162:165], 0
	v_mfma_f32_16x16x32_bf16 v[114:117], v[130:133], v[170:173], 0
	v_mfma_f32_16x16x32_bf16 v[106:109], v[138:141], v[170:173], 0
	v_mfma_f32_16x16x32_bf16 v[94:97], v[130:133], v[178:181], 0
	v_mfma_f32_16x16x32_bf16 v[90:93], v[138:141], v[178:181], 0
	v_mfma_f32_16x16x32_bf16 v[86:89], v[130:133], v[186:189], 0
	v_mfma_f32_16x16x32_bf16 v[78:81], v[138:141], v[186:189], 0
	v_mfma_f32_16x16x32_bf16 v[126:129], v[134:137], v[166:169], v[126:129]
	v_mfma_f32_16x16x32_bf16 v[122:125], v[142:145], v[166:169], v[122:125]
	v_mfma_f32_16x16x32_bf16 v[114:117], v[134:137], v[174:177], v[114:117]
	v_mfma_f32_16x16x32_bf16 v[106:109], v[142:145], v[174:177], v[106:109]
	v_mfma_f32_16x16x32_bf16 v[94:97], v[134:137], v[182:185], v[94:97]
	v_mfma_f32_16x16x32_bf16 v[90:93], v[142:145], v[182:185], v[90:93]
	v_mfma_f32_16x16x32_bf16 v[86:89], v[134:137], v[190:193], v[86:89]
	v_mfma_f32_16x16x32_bf16 v[78:81], v[142:145], v[190:193], v[78:81]
	v_mfma_f32_16x16x32_bf16 v[118:121], v[146:149], v[162:165], 0
	v_mfma_f32_16x16x32_bf16 v[110:113], v[154:157], v[162:165], 0
	v_mfma_f32_16x16x32_bf16 v[102:105], v[146:149], v[170:173], 0
	v_mfma_f32_16x16x32_bf16 v[98:101], v[154:157], v[170:173], 0
	v_mfma_f32_16x16x32_bf16 v[82:85], v[146:149], v[178:181], 0
	v_mfma_f32_16x16x32_bf16 v[74:77], v[154:157], v[178:181], 0
	v_mfma_f32_16x16x32_bf16 v[70:73], v[146:149], v[186:189], 0
	v_mfma_f32_16x16x32_bf16 v[66:69], v[154:157], v[186:189], 0
	v_mfma_f32_16x16x32_bf16 v[118:121], v[150:153], v[166:169], v[118:121]
	v_mfma_f32_16x16x32_bf16 v[110:113], v[158:161], v[166:169], v[110:113]
	v_mfma_f32_16x16x32_bf16 v[102:105], v[150:153], v[174:177], v[102:105]
	v_mfma_f32_16x16x32_bf16 v[98:101], v[158:161], v[174:177], v[98:101]
	v_mfma_f32_16x16x32_bf16 v[82:85], v[150:153], v[182:185], v[82:85]
	v_mfma_f32_16x16x32_bf16 v[74:77], v[158:161], v[182:185], v[74:77]
	v_mfma_f32_16x16x32_bf16 v[70:73], v[150:153], v[190:193], v[70:73]
	v_mfma_f32_16x16x32_bf16 v[66:69], v[158:161], v[190:193], v[66:69]
	s_setprio 0
	s_barrier
	ds_read_b128 v[162:165], v236 offset:16384
	ds_read_b128 v[166:169], v236 offset:17408
	ds_read_b128 v[170:173], v236 offset:18432
	ds_read_b128 v[174:177], v236 offset:19456
	ds_read_b128 v[178:181], v236 offset:20480
	ds_read_b128 v[182:185], v236 offset:21504
	ds_read_b128 v[186:189], v236 offset:22528
	ds_read_b128 v[190:193], v236 offset:23552
	s_mov_b32 s58, m0
	s_mov_b32 m0, s30
	s_nop 2
	global_load_lds_dwordx4 v229, s[64:65]
	s_mov_b32 m0, s58
	s_nop 0
	s_mov_b32 s58, m0
	s_mov_b32 m0, s31
	s_nop 2
	global_load_lds_dwordx4 v231, s[64:65]
	s_mov_b32 m0, s58
	s_add_u32 s58, s64, 0x40000
	s_addc_u32 s59, s65, 0
	s_mov_b32 s88, m0
	s_mov_b32 m0, s34
	s_nop 2
	global_load_lds_dwordx4 v229, s[58:59]
	s_mov_b32 m0, s88
	s_nop 0
	s_mov_b32 s88, m0
	s_mov_b32 m0, s35
	s_nop 2
	global_load_lds_dwordx4 v231, s[58:59]
	s_mov_b32 m0, s88
	s_mov_b32 s58, m0
	s_mov_b32 m0, s28
	s_nop 2
	global_load_lds_dwordx4 v228, s[66:67]
	s_mov_b32 m0, s58
	s_nop 0
	s_mov_b32 s58, m0
	s_mov_b32 m0, s36
	s_nop 2
	global_load_lds_dwordx4 v230, s[66:67]
	s_mov_b32 m0, s58
	s_waitcnt vmcnt(8) lgkmcnt(0)
	s_barrier
	s_setprio 1
	v_mfma_f32_16x16x32_bf16 v[62:65], v[130:133], v[162:165], 0
	v_mfma_f32_16x16x32_bf16 v[58:61], v[138:141], v[162:165], 0
	v_mfma_f32_16x16x32_bf16 v[54:57], v[130:133], v[170:173], 0
	v_mfma_f32_16x16x32_bf16 v[46:49], v[138:141], v[170:173], 0
	v_mfma_f32_16x16x32_bf16 v[38:41], v[130:133], v[178:181], 0
	v_mfma_f32_16x16x32_bf16 v[30:33], v[138:141], v[178:181], 0
	v_mfma_f32_16x16x32_bf16 v[22:25], v[130:133], v[186:189], 0
	v_mfma_f32_16x16x32_bf16 v[14:17], v[138:141], v[186:189], 0
	v_mfma_f32_16x16x32_bf16 v[62:65], v[134:137], v[166:169], v[62:65]
	v_mfma_f32_16x16x32_bf16 v[58:61], v[142:145], v[166:169], v[58:61]
	v_mfma_f32_16x16x32_bf16 v[54:57], v[134:137], v[174:177], v[54:57]
	v_mfma_f32_16x16x32_bf16 v[46:49], v[142:145], v[174:177], v[46:49]
	v_mfma_f32_16x16x32_bf16 v[38:41], v[134:137], v[182:185], v[38:41]
	v_mfma_f32_16x16x32_bf16 v[30:33], v[142:145], v[182:185], v[30:33]
	v_mfma_f32_16x16x32_bf16 v[22:25], v[134:137], v[190:193], v[22:25]
	v_mfma_f32_16x16x32_bf16 v[14:17], v[142:145], v[190:193], v[14:17]
	v_mfma_f32_16x16x32_bf16 v[50:53], v[146:149], v[162:165], 0
	v_mfma_f32_16x16x32_bf16 v[42:45], v[154:157], v[162:165], 0
	v_mfma_f32_16x16x32_bf16 v[34:37], v[146:149], v[170:173], 0
	v_mfma_f32_16x16x32_bf16 v[26:29], v[154:157], v[170:173], 0
	v_mfma_f32_16x16x32_bf16 v[18:21], v[146:149], v[178:181], 0
	v_mfma_f32_16x16x32_bf16 v[10:13], v[154:157], v[178:181], 0
	v_mfma_f32_16x16x32_bf16 v[6:9], v[146:149], v[186:189], 0
	v_mfma_f32_16x16x32_bf16 v[2:5], v[154:157], v[186:189], 0
	v_mfma_f32_16x16x32_bf16 v[50:53], v[150:153], v[166:169], v[50:53]
	v_mfma_f32_16x16x32_bf16 v[42:45], v[158:161], v[166:169], v[42:45]
	v_mfma_f32_16x16x32_bf16 v[34:37], v[150:153], v[174:177], v[34:37]
	v_mfma_f32_16x16x32_bf16 v[26:29], v[158:161], v[174:177], v[26:29]
	v_mfma_f32_16x16x32_bf16 v[18:21], v[150:153], v[182:185], v[18:21]
	v_mfma_f32_16x16x32_bf16 v[10:13], v[158:161], v[182:185], v[10:13]
	v_mfma_f32_16x16x32_bf16 v[6:9], v[150:153], v[190:193], v[6:9]
	v_mfma_f32_16x16x32_bf16 v[2:5], v[158:161], v[190:193], v[2:5]
	s_setprio 0
	s_barrier
	s_branch .Lmid1440
.LBB0_1440:
	ds_read_b128 v[130:133], v234
	ds_read_b128 v[134:137], v234 offset:1024
	ds_read_b128 v[138:141], v234 offset:2048
	ds_read_b128 v[142:145], v234 offset:3072
	ds_read_b128 v[146:149], v235
	ds_read_b128 v[150:153], v235 offset:1024
	ds_read_b128 v[154:157], v235 offset:2048
	ds_read_b128 v[158:161], v235 offset:3072
	s_add_u32 s60, s58, 0x100
	s_addc_u32 s61, s59, 0
	s_cmp_eq_u32 s87, 12
	s_cselect_b32 s66, s33, s60
	s_cselect_b32 s67, s21, s61
	s_cselect_b32 s64, s84, s85
	s_cselect_b32 s65, s19, s86
	s_add_u32 s62, s66, 0x80
	s_addc_u32 s63, s67, 0
	ds_read_b128 v[162:165], v236
	ds_read_b128 v[166:169], v236 offset:1024
	ds_read_b128 v[170:173], v236 offset:2048
	ds_read_b128 v[174:177], v236 offset:3072
	ds_read_b128 v[178:181], v236 offset:4096
	ds_read_b128 v[182:185], v236 offset:5120
	ds_read_b128 v[186:189], v236 offset:6144
	ds_read_b128 v[190:193], v236 offset:7168
	s_add_u32 s58, s58, 0x40080
	s_addc_u32 s59, s59, 0
	s_mov_b32 s88, m0
	s_mov_b32 m0, s80
	s_nop 2
	global_load_lds_dwordx4 v228, s[58:59]
	s_mov_b32 m0, s88
	s_nop 0
	s_mov_b32 s88, m0
	s_mov_b32 m0, s81
	s_nop 2
	global_load_lds_dwordx4 v230, s[58:59]
	s_mov_b32 m0, s88
	s_waitcnt vmcnt(8) lgkmcnt(0)
	s_barrier
	s_setprio 1
	v_mfma_f32_16x16x32_bf16 v[126:129], v[130:133], v[162:165], v[126:129]
	v_mfma_f32_16x16x32_bf16 v[122:125], v[138:141], v[162:165], v[122:125]
	v_mfma_f32_16x16x32_bf16 v[114:117], v[130:133], v[170:173], v[114:117]
	v_mfma_f32_16x16x32_bf16 v[106:109], v[138:141], v[170:173], v[106:109]
	v_mfma_f32_16x16x32_bf16 v[94:97], v[130:133], v[178:181], v[94:97]
	v_mfma_f32_16x16x32_bf16 v[90:93], v[138:141], v[178:181], v[90:93]
	v_mfma_f32_16x16x32_bf16 v[86:89], v[130:133], v[186:189], v[86:89]
	v_mfma_f32_16x16x32_bf16 v[78:81], v[138:141], v[186:189], v[78:81]
	v_mfma_f32_16x16x32_bf16 v[126:129], v[134:137], v[166:169], v[126:129]
	v_mfma_f32_16x16x32_bf16 v[122:125], v[142:145], v[166:169], v[122:125]
	v_mfma_f32_16x16x32_bf16 v[114:117], v[134:137], v[174:177], v[114:117]
	v_mfma_f32_16x16x32_bf16 v[106:109], v[142:145], v[174:177], v[106:109]
	v_mfma_f32_16x16x32_bf16 v[94:97], v[134:137], v[182:185], v[94:97]
	v_mfma_f32_16x16x32_bf16 v[90:93], v[142:145], v[182:185], v[90:93]
	v_mfma_f32_16x16x32_bf16 v[86:89], v[134:137], v[190:193], v[86:89]
	v_mfma_f32_16x16x32_bf16 v[78:81], v[142:145], v[190:193], v[78:81]
	v_mfma_f32_16x16x32_bf16 v[118:121], v[146:149], v[162:165], v[118:121]
	v_mfma_f32_16x16x32_bf16 v[110:113], v[154:157], v[162:165], v[110:113]
	v_mfma_f32_16x16x32_bf16 v[102:105], v[146:149], v[170:173], v[102:105]
	v_mfma_f32_16x16x32_bf16 v[98:101], v[154:157], v[170:173], v[98:101]
	v_mfma_f32_16x16x32_bf16 v[82:85], v[146:149], v[178:181], v[82:85]
	v_mfma_f32_16x16x32_bf16 v[74:77], v[154:157], v[178:181], v[74:77]
	v_mfma_f32_16x16x32_bf16 v[70:73], v[146:149], v[186:189], v[70:73]
	v_mfma_f32_16x16x32_bf16 v[66:69], v[154:157], v[186:189], v[66:69]
	v_mfma_f32_16x16x32_bf16 v[118:121], v[150:153], v[166:169], v[118:121]
	v_mfma_f32_16x16x32_bf16 v[110:113], v[158:161], v[166:169], v[110:113]
	v_mfma_f32_16x16x32_bf16 v[102:105], v[150:153], v[174:177], v[102:105]
	v_mfma_f32_16x16x32_bf16 v[98:101], v[158:161], v[174:177], v[98:101]
	v_mfma_f32_16x16x32_bf16 v[82:85], v[150:153], v[182:185], v[82:85]
	v_mfma_f32_16x16x32_bf16 v[74:77], v[158:161], v[182:185], v[74:77]
	v_mfma_f32_16x16x32_bf16 v[70:73], v[150:153], v[190:193], v[70:73]
	v_mfma_f32_16x16x32_bf16 v[66:69], v[158:161], v[190:193], v[66:69]
	s_setprio 0
	s_barrier
	ds_read_b128 v[162:165], v236 offset:16384
	ds_read_b128 v[166:169], v236 offset:17408
	ds_read_b128 v[170:173], v236 offset:18432
	ds_read_b128 v[174:177], v236 offset:19456
	ds_read_b128 v[178:181], v236 offset:20480
	ds_read_b128 v[182:185], v236 offset:21504
	ds_read_b128 v[186:189], v236 offset:22528
	ds_read_b128 v[190:193], v236 offset:23552
	s_mov_b32 s58, m0
	s_mov_b32 m0, s30
	s_nop 2
	global_load_lds_dwordx4 v229, s[64:65]
	s_mov_b32 m0, s58
	s_nop 0
	s_mov_b32 s58, m0
	s_mov_b32 m0, s31
	s_nop 2
	global_load_lds_dwordx4 v231, s[64:65]
	s_mov_b32 m0, s58
	s_add_u32 s58, s64, 0x40000
	s_addc_u32 s59, s65, 0
	s_mov_b32 s88, m0
	s_mov_b32 m0, s34
	s_nop 2
	global_load_lds_dwordx4 v229, s[58:59]
	s_mov_b32 m0, s88
	s_nop 0
	s_mov_b32 s88, m0
	s_mov_b32 m0, s35
	s_nop 2
	global_load_lds_dwordx4 v231, s[58:59]
	s_mov_b32 m0, s88
	s_mov_b32 s58, m0
	s_mov_b32 m0, s28
	s_nop 2
	global_load_lds_dwordx4 v228, s[66:67]
	s_mov_b32 m0, s58
	s_nop 0
	s_mov_b32 s58, m0
	s_mov_b32 m0, s36
	s_nop 2
	global_load_lds_dwordx4 v230, s[66:67]
	s_mov_b32 m0, s58
	s_waitcnt vmcnt(8) lgkmcnt(0)
	s_barrier
	s_setprio 1
	v_mfma_f32_16x16x32_bf16 v[62:65], v[130:133], v[162:165], v[62:65]
	v_mfma_f32_16x16x32_bf16 v[58:61], v[138:141], v[162:165], v[58:61]
	v_mfma_f32_16x16x32_bf16 v[54:57], v[130:133], v[170:173], v[54:57]
	v_mfma_f32_16x16x32_bf16 v[46:49], v[138:141], v[170:173], v[46:49]
	v_mfma_f32_16x16x32_bf16 v[38:41], v[130:133], v[178:181], v[38:41]
	v_mfma_f32_16x16x32_bf16 v[30:33], v[138:141], v[178:181], v[30:33]
	v_mfma_f32_16x16x32_bf16 v[22:25], v[130:133], v[186:189], v[22:25]
	v_mfma_f32_16x16x32_bf16 v[14:17], v[138:141], v[186:189], v[14:17]
	v_mfma_f32_16x16x32_bf16 v[62:65], v[134:137], v[166:169], v[62:65]
	v_mfma_f32_16x16x32_bf16 v[58:61], v[142:145], v[166:169], v[58:61]
	v_mfma_f32_16x16x32_bf16 v[54:57], v[134:137], v[174:177], v[54:57]
	v_mfma_f32_16x16x32_bf16 v[46:49], v[142:145], v[174:177], v[46:49]
	v_mfma_f32_16x16x32_bf16 v[38:41], v[134:137], v[182:185], v[38:41]
	v_mfma_f32_16x16x32_bf16 v[30:33], v[142:145], v[182:185], v[30:33]
	v_mfma_f32_16x16x32_bf16 v[22:25], v[134:137], v[190:193], v[22:25]
	v_mfma_f32_16x16x32_bf16 v[14:17], v[142:145], v[190:193], v[14:17]
	v_mfma_f32_16x16x32_bf16 v[50:53], v[146:149], v[162:165], v[50:53]
	v_mfma_f32_16x16x32_bf16 v[42:45], v[154:157], v[162:165], v[42:45]
	v_mfma_f32_16x16x32_bf16 v[34:37], v[146:149], v[170:173], v[34:37]
	v_mfma_f32_16x16x32_bf16 v[26:29], v[154:157], v[170:173], v[26:29]
	v_mfma_f32_16x16x32_bf16 v[18:21], v[146:149], v[178:181], v[18:21]
	v_mfma_f32_16x16x32_bf16 v[10:13], v[154:157], v[178:181], v[10:13]
	v_mfma_f32_16x16x32_bf16 v[6:9], v[146:149], v[186:189], v[6:9]
	v_mfma_f32_16x16x32_bf16 v[2:5], v[154:157], v[186:189], v[2:5]
	v_mfma_f32_16x16x32_bf16 v[50:53], v[150:153], v[166:169], v[50:53]
	v_mfma_f32_16x16x32_bf16 v[42:45], v[158:161], v[166:169], v[42:45]
	v_mfma_f32_16x16x32_bf16 v[34:37], v[150:153], v[174:177], v[34:37]
	v_mfma_f32_16x16x32_bf16 v[26:29], v[158:161], v[174:177], v[26:29]
	v_mfma_f32_16x16x32_bf16 v[18:21], v[150:153], v[182:185], v[18:21]
	v_mfma_f32_16x16x32_bf16 v[10:13], v[158:161], v[182:185], v[10:13]
	v_mfma_f32_16x16x32_bf16 v[6:9], v[150:153], v[190:193], v[6:9]
	v_mfma_f32_16x16x32_bf16 v[2:5], v[158:161], v[190:193], v[2:5]
	s_setprio 0
	s_barrier
.Lmid1440:
	ds_read_b128 v[130:133], v237
	ds_read_b128 v[134:137], v237 offset:1024
	ds_read_b128 v[138:141], v237 offset:2048
	ds_read_b128 v[142:145], v237 offset:3072
	ds_read_b128 v[146:149], v238
	ds_read_b128 v[150:153], v238 offset:1024
	ds_read_b128 v[154:157], v238 offset:2048
	ds_read_b128 v[158:161], v238 offset:3072
	ds_read_b128 v[162:165], v236 offset:32768
	ds_read_b128 v[166:169], v236 offset:33792
	ds_read_b128 v[170:173], v236 offset:34816
	ds_read_b128 v[174:177], v236 offset:35840
	ds_read_b128 v[178:181], v236 offset:36864
	ds_read_b128 v[182:185], v236 offset:37888
	ds_read_b128 v[186:189], v236 offset:38912
	ds_read_b128 v[190:193], v236 offset:39936
	s_add_u32 s58, s66, 0x40000
	s_addc_u32 s59, s67, 0
	s_mov_b32 s66, m0
	s_mov_b32 m0, s37
	s_nop 2
	global_load_lds_dwordx4 v228, s[58:59]
	s_mov_b32 m0, s66
	s_nop 0
	s_mov_b32 s66, m0
	s_mov_b32 m0, s52
	s_nop 2
	global_load_lds_dwordx4 v230, s[58:59]
	s_mov_b32 m0, s66
	s_waitcnt vmcnt(8) lgkmcnt(0)
	s_barrier
	s_setprio 1
	v_mfma_f32_16x16x32_bf16 v[126:129], v[130:133], v[162:165], v[126:129]
	v_mfma_f32_16x16x32_bf16 v[122:125], v[138:141], v[162:165], v[122:125]
	v_mfma_f32_16x16x32_bf16 v[114:117], v[130:133], v[170:173], v[114:117]
	v_mfma_f32_16x16x32_bf16 v[106:109], v[138:141], v[170:173], v[106:109]
	v_mfma_f32_16x16x32_bf16 v[94:97], v[130:133], v[178:181], v[94:97]
	v_mfma_f32_16x16x32_bf16 v[90:93], v[138:141], v[178:181], v[90:93]
	v_mfma_f32_16x16x32_bf16 v[86:89], v[130:133], v[186:189], v[86:89]
	v_mfma_f32_16x16x32_bf16 v[78:81], v[138:141], v[186:189], v[78:81]
	v_mfma_f32_16x16x32_bf16 v[126:129], v[134:137], v[166:169], v[126:129]
	v_mfma_f32_16x16x32_bf16 v[122:125], v[142:145], v[166:169], v[122:125]
	v_mfma_f32_16x16x32_bf16 v[114:117], v[134:137], v[174:177], v[114:117]
	v_mfma_f32_16x16x32_bf16 v[106:109], v[142:145], v[174:177], v[106:109]
	v_mfma_f32_16x16x32_bf16 v[94:97], v[134:137], v[182:185], v[94:97]
	v_mfma_f32_16x16x32_bf16 v[90:93], v[142:145], v[182:185], v[90:93]
	v_mfma_f32_16x16x32_bf16 v[86:89], v[134:137], v[190:193], v[86:89]
	v_mfma_f32_16x16x32_bf16 v[78:81], v[142:145], v[190:193], v[78:81]
	v_mfma_f32_16x16x32_bf16 v[118:121], v[146:149], v[162:165], v[118:121]
	v_mfma_f32_16x16x32_bf16 v[110:113], v[154:157], v[162:165], v[110:113]
	v_mfma_f32_16x16x32_bf16 v[102:105], v[146:149], v[170:173], v[102:105]
	v_mfma_f32_16x16x32_bf16 v[98:101], v[154:157], v[170:173], v[98:101]
	v_mfma_f32_16x16x32_bf16 v[82:85], v[146:149], v[178:181], v[82:85]
	v_mfma_f32_16x16x32_bf16 v[74:77], v[154:157], v[178:181], v[74:77]
	v_mfma_f32_16x16x32_bf16 v[70:73], v[146:149], v[186:189], v[70:73]
	v_mfma_f32_16x16x32_bf16 v[66:69], v[154:157], v[186:189], v[66:69]
	v_mfma_f32_16x16x32_bf16 v[118:121], v[150:153], v[166:169], v[118:121]
	v_mfma_f32_16x16x32_bf16 v[110:113], v[158:161], v[166:169], v[110:113]
	v_mfma_f32_16x16x32_bf16 v[102:105], v[150:153], v[174:177], v[102:105]
	v_mfma_f32_16x16x32_bf16 v[98:101], v[158:161], v[174:177], v[98:101]
	v_mfma_f32_16x16x32_bf16 v[82:85], v[150:153], v[182:185], v[82:85]
	v_mfma_f32_16x16x32_bf16 v[74:77], v[158:161], v[182:185], v[74:77]
	v_mfma_f32_16x16x32_bf16 v[70:73], v[150:153], v[190:193], v[70:73]
	v_mfma_f32_16x16x32_bf16 v[66:69], v[158:161], v[190:193], v[66:69]
	s_setprio 0
	s_barrier
	ds_read_b128 v[162:165], v236 offset:49152
	ds_read_b128 v[166:169], v236 offset:50176
	ds_read_b128 v[170:173], v236 offset:51200
	ds_read_b128 v[174:177], v236 offset:52224
	ds_read_b128 v[178:181], v236 offset:53248
	ds_read_b128 v[182:185], v236 offset:54272
	ds_read_b128 v[186:189], v236 offset:55296
	ds_read_b128 v[190:193], v236 offset:56320
	s_add_u32 s58, s64, 0x80
	s_addc_u32 s59, s65, 0
	s_mov_b32 s66, m0
	s_mov_b32 m0, s68
	s_nop 2
	global_load_lds_dwordx4 v229, s[58:59]
	s_mov_b32 m0, s66
	s_nop 0
	s_mov_b32 s66, m0
	s_mov_b32 m0, s69
	s_nop 2
	global_load_lds_dwordx4 v231, s[58:59]
	s_mov_b32 m0, s66
	s_add_u32 s58, s64, 0x40080
	s_addc_u32 s59, s65, 0
	s_mov_b32 s64, m0
	s_mov_b32 m0, s78
	s_nop 2
	global_load_lds_dwordx4 v229, s[58:59]
	s_mov_b32 m0, s64
	s_nop 0
	s_mov_b32 s64, m0
	s_mov_b32 m0, s79
	s_nop 2
	global_load_lds_dwordx4 v231, s[58:59]
	s_mov_b32 m0, s64
	s_mov_b32 s58, m0
	s_mov_b32 m0, s76
	s_nop 2
	global_load_lds_dwordx4 v228, s[62:63]
	s_mov_b32 m0, s58
	s_nop 0
	s_mov_b32 s58, m0
	s_mov_b32 m0, s77
	s_nop 2
	global_load_lds_dwordx4 v230, s[62:63]
	s_mov_b32 m0, s58
	s_waitcnt vmcnt(8) lgkmcnt(0)
	s_barrier
	s_setprio 1
	v_mfma_f32_16x16x32_bf16 v[62:65], v[130:133], v[162:165], v[62:65]
	v_mfma_f32_16x16x32_bf16 v[58:61], v[138:141], v[162:165], v[58:61]
	v_mfma_f32_16x16x32_bf16 v[54:57], v[130:133], v[170:173], v[54:57]
	v_mfma_f32_16x16x32_bf16 v[46:49], v[138:141], v[170:173], v[46:49]
	v_mfma_f32_16x16x32_bf16 v[38:41], v[130:133], v[178:181], v[38:41]
	v_mfma_f32_16x16x32_bf16 v[30:33], v[138:141], v[178:181], v[30:33]
	v_mfma_f32_16x16x32_bf16 v[22:25], v[130:133], v[186:189], v[22:25]
	v_mfma_f32_16x16x32_bf16 v[14:17], v[138:141], v[186:189], v[14:17]
	v_mfma_f32_16x16x32_bf16 v[62:65], v[134:137], v[166:169], v[62:65]
	v_mfma_f32_16x16x32_bf16 v[58:61], v[142:145], v[166:169], v[58:61]
	v_mfma_f32_16x16x32_bf16 v[54:57], v[134:137], v[174:177], v[54:57]
	v_mfma_f32_16x16x32_bf16 v[46:49], v[142:145], v[174:177], v[46:49]
	v_mfma_f32_16x16x32_bf16 v[38:41], v[134:137], v[182:185], v[38:41]
	v_mfma_f32_16x16x32_bf16 v[30:33], v[142:145], v[182:185], v[30:33]
	v_mfma_f32_16x16x32_bf16 v[22:25], v[134:137], v[190:193], v[22:25]
	v_mfma_f32_16x16x32_bf16 v[14:17], v[142:145], v[190:193], v[14:17]
	v_mfma_f32_16x16x32_bf16 v[50:53], v[146:149], v[162:165], v[50:53]
	v_mfma_f32_16x16x32_bf16 v[42:45], v[154:157], v[162:165], v[42:45]
	v_mfma_f32_16x16x32_bf16 v[34:37], v[146:149], v[170:173], v[34:37]
	v_mfma_f32_16x16x32_bf16 v[26:29], v[154:157], v[170:173], v[26:29]
	v_mfma_f32_16x16x32_bf16 v[18:21], v[146:149], v[178:181], v[18:21]
	v_mfma_f32_16x16x32_bf16 v[10:13], v[154:157], v[178:181], v[10:13]
	v_mfma_f32_16x16x32_bf16 v[6:9], v[146:149], v[186:189], v[6:9]
	v_mfma_f32_16x16x32_bf16 v[2:5], v[154:157], v[186:189], v[2:5]
	v_mfma_f32_16x16x32_bf16 v[50:53], v[150:153], v[166:169], v[50:53]
	v_mfma_f32_16x16x32_bf16 v[42:45], v[158:161], v[166:169], v[42:45]
	v_mfma_f32_16x16x32_bf16 v[34:37], v[150:153], v[174:177], v[34:37]
	v_mfma_f32_16x16x32_bf16 v[26:29], v[158:161], v[174:177], v[26:29]
	v_mfma_f32_16x16x32_bf16 v[18:21], v[150:153], v[182:185], v[18:21]
	v_mfma_f32_16x16x32_bf16 v[10:13], v[158:161], v[182:185], v[10:13]
	v_mfma_f32_16x16x32_bf16 v[6:9], v[150:153], v[190:193], v[6:9]
	v_mfma_f32_16x16x32_bf16 v[2:5], v[158:161], v[190:193], v[2:5]
	s_setprio 0
	s_barrier
	s_add_i32 s87, s87, 2
	s_add_u32 s85, s85, 0x100
	s_addc_u32 s86, s86, 0
	s_cmp_gt_u32 s87, 13
	s_mov_b64 s[58:59], s[60:61]
	s_cbranch_scc0 .LBB0_1440
	s_and_b64 vcc, exec, s[16:17]
	s_cbranch_vccz .LBB0_1443
	s_barrier

.LBB0_1717:
	s_mov_b32 s0, m0
	s_mov_b32 m0, s3
	s_nop 2
	global_load_lds_dwordx4 v178, s[12:13]
	s_mov_b32 m0, s0
	s_and_b64 vcc, exec, s[8:9]
	s_mov_b32 s0, m0
	s_mov_b32 m0, s26
	s_nop 2
	global_load_lds_dwordx4 v179, s[12:13]
	s_mov_b32 m0, s0
	s_nop 0
	s_mov_b32 s0, m0
	s_mov_b32 m0, s27
	s_nop 2
	global_load_lds_dwordx4 v180, s[12:13]
	s_mov_b32 m0, s0
	s_nop 0
	s_mov_b32 s0, m0
	s_mov_b32 m0, s34
	s_nop 2
	global_load_lds_dwordx4 v181, s[12:13]
	s_mov_b32 m0, s0
	s_nop 0
	s_mov_b32 s0, m0
	s_mov_b32 m0, s35
	s_nop 2
	global_load_lds_dwordx4 v182, s[12:13]
	s_mov_b32 m0, s0
	s_nop 0
	s_mov_b32 s0, m0
	s_mov_b32 m0, s56
	s_nop 2
	global_load_lds_dwordx4 v183, s[12:13]
	s_mov_b32 m0, s0
	s_nop 0
	s_mov_b32 s0, m0
	s_mov_b32 m0, s57
	s_nop 2
	global_load_lds_dwordx4 v184, s[12:13]
	s_mov_b32 m0, s0
	s_nop 0
	s_mov_b32 s0, m0
	s_mov_b32 m0, s58
	s_nop 2
	global_load_lds_dwordx4 v185, s[12:13]
	s_mov_b32 m0, s0
	s_nop 0
	s_mov_b32 s0, m0
	s_mov_b32 m0, s59
	s_nop 2
	global_load_lds_dwordx4 v186, s[12:13]
	s_mov_b32 m0, s0
	s_nop 0
	s_mov_b32 s0, m0
	s_mov_b32 m0, s60
	s_nop 2
	global_load_lds_dwordx4 v187, s[12:13]
	s_mov_b32 m0, s0
	s_nop 0
	s_mov_b32 s0, m0
	s_mov_b32 m0, s61
	s_nop 2
	global_load_lds_dwordx4 v188, s[12:13]
	s_mov_b32 m0, s0
	s_nop 0
	s_mov_b32 s0, m0
	s_mov_b32 m0, s62
	s_nop 2
	global_load_lds_dwordx4 v189, s[12:13]
	s_mov_b32 m0, s0
	s_nop 0
	s_mov_b32 s0, m0
	s_mov_b32 m0, s63
	s_nop 2
	global_load_lds_dwordx4 v190, s[12:13]
	s_mov_b32 m0, s0
	s_nop 0
	s_mov_b32 s0, m0
	s_mov_b32 m0, s64
	s_nop 2
	global_load_lds_dwordx4 v191, s[12:13]
	s_mov_b32 m0, s0
	s_nop 0
	s_mov_b32 s0, m0
	s_mov_b32 m0, s65
	s_nop 2
	global_load_lds_dwordx4 v192, s[12:13]
	s_mov_b32 m0, s0
	s_nop 0
	s_mov_b32 s0, m0
	s_mov_b32 m0, s66
	s_nop 2
	global_load_lds_dwordx4 v193, s[12:13]
	s_mov_b32 m0, s0
	s_waitcnt vmcnt(0) lgkmcnt(0)
	s_barrier
	s_cbranch_vccnz .LBB0_1721
	v_add_u32_e32 v136, v175, v194
	ds_read_b128 v[132:135], v136
	ds_read_b128 v[136:139], v136 offset:32768
	v_add_u32_e32 v140, v176, v194
	ds_read_b128 v[140:143], v140
	v_add_u32_e32 v144, v177, v194
	s_waitcnt vmcnt(31) lgkmcnt(2)
	v_mfma_f32_16x16x32_bf16 v[132:135], v[126:129], v[132:135], 0
	ds_read_b128 v[144:147], v144
	v_and_b32_e32 v149, 0xffff0000, v127
	v_med3_f32 v150, v149, s78, v240
	s_waitcnt lgkmcnt(2)
	v_mfma_f32_16x16x32_bf16 v[136:139], v[126:129], v[136:139], 0
	v_lshlrev_b32_e32 v151, 16, v128
	v_and_b32_e32 v153, 0xffff0000, v128
	v_med3_f32 v152, v151, s78, v240
	s_waitcnt lgkmcnt(1)
	v_mfma_f32_16x16x32_bf16 v[132:135], v[126:129], v[140:143], v[132:135]
	v_lshlrev_b32_e32 v141, 16, v126
	v_and_b32_e32 v143, 0xffff0000, v126
	v_med3_f32 v154, v153, s78, v240
	s_waitcnt lgkmcnt(0)
	v_mfma_f32_16x16x32_bf16 v[136:139], v[126:129], v[144:147], v[136:139]
	v_med3_f32 v145, v141, s78, v240
	v_med3_f32 v146, v143, s78, v240
	v_mov_b32_e32 v144, 0
	v_cvt_pk_fp8_f32 v144, v145, v146
	v_lshlrev_b32_e32 v147, 16, v127
	v_med3_f32 v145, v147, s78, v240
	v_lshlrev_b32_e32 v155, 16, v129
	v_cvt_pk_fp8_f32 v144, v145, v150 op_sel:[0,0,1]
	v_mov_b32_e32 v145, 0
	v_cvt_pk_fp8_f32 v145, v152, v154
	v_and_b32_e32 v157, 0xffff0000, v129
	v_med3_f32 v152, v155, s78, v240
	v_med3_f32 v154, v157, s78, v240
	v_cvt_pk_fp8_f32 v145, v152, v154 op_sel:[0,0,1]
	v_lshlrev_b64 v[130:131], 10, v[130:131]
	v_lshl_add_u64 v[130:131], v[164:165], 0, v[130:131]
	s_waitcnt vmcnt(30)
	v_and_b32_e32 v142, 0xffff0000, v122
	v_lshlrev_b32_e32 v140, 16, v122
	v_and_b32_e32 v148, 0xffff0000, v123
	global_store_dwordx2 v[130:131], v[144:145], off
	v_pk_mul_f32 v[144:145], v[142:143], v[142:143]
	v_lshlrev_b32_e32 v146, 16, v123
	v_pk_fma_f32 v[144:145], v[140:141], v[140:141], v[144:145]
	v_pk_mul_f32 v[158:159], v[148:149], v[148:149]
	v_med3_f32 v140, v140, s78, v240
	v_med3_f32 v141, v142, s78, v240
	v_mov_b32_e32 v160, 0
	v_and_b32_e32 v152, 0xffff0000, v124
	v_pk_fma_f32 v[158:159], v[146:147], v[146:147], v[158:159]
	v_cvt_pk_fp8_f32 v160, v140, v141
	v_lshlrev_b32_e32 v150, 16, v124
	v_pk_add_f32 v[144:145], v[144:145], v[158:159]
	v_pk_mul_f32 v[158:159], v[152:153], v[152:153]
	v_and_b32_e32 v156, 0xffff0000, v125
	v_pk_fma_f32 v[158:159], v[150:151], v[150:151], v[158:159]
	v_lshlrev_b32_e32 v154, 16, v125
	v_pk_add_f32 v[158:159], v[158:159], v[144:145]
	v_pk_mul_f32 v[144:145], v[156:157], v[156:157]
	v_med3_f32 v140, v146, s78, v240
	v_med3_f32 v141, v148, s78, v240
	v_add_u32_e32 v146, v175, v195
	v_pk_fma_f32 v[244:245], v[154:155], v[154:155], v[144:145]
	v_cvt_pk_fp8_f32 v160, v140, v141 op_sel:[0,0,1]
	v_med3_f32 v144, v150, s78, v240
	v_med3_f32 v145, v152, s78, v240
	ds_read_b128 v[140:143], v146
	v_mov_b32_e32 v161, 0
	v_cvt_pk_fp8_f32 v161, v144, v145
	ds_read_b128 v[144:147], v146 offset:32768
	s_waitcnt lgkmcnt(1)
	v_mfma_f32_16x16x32_bf16 v[132:135], v[122:125], v[140:143], v[132:135]
	v_add_u32_e32 v140, v176, v195
	ds_read_b128 v[140:143], v140
	v_med3_f32 v148, v154, s78, v240
	s_waitcnt lgkmcnt(1)
	v_mfma_f32_16x16x32_bf16 v[136:139], v[122:125], v[144:147], v[136:139]
	v_add_u32_e32 v144, v177, v195
	ds_read_b128 v[144:147], v144
	v_med3_f32 v149, v156, s78, v240
	s_waitcnt lgkmcnt(1)
	v_mfma_f32_16x16x32_bf16 v[132:135], v[122:125], v[140:143], v[132:135]
	v_add_f32_e64 v140, v244, v158
	v_add_f32_e64 v141, v245, v159
	s_waitcnt vmcnt(30)
	v_and_b32_e32 v143, 0xffff0000, v119
	v_and_b32_e32 v142, 0xffff0000, v118
	v_cvt_pk_fp8_f32 v161, v148, v149 op_sel:[0,0,1]
	v_pk_add_f32 v[148:149], v[140:141], v[140:141] op_sel_hi:[0,1]
	s_waitcnt lgkmcnt(0)
	v_mfma_f32_16x16x32_bf16 v[136:139], v[122:125], v[144:147], v[136:139]
	v_lshlrev_b32_e32 v141, 16, v119
	v_lshlrev_b32_e32 v140, 16, v118
	v_pk_mul_f32 v[144:145], v[142:143], v[142:143]
	v_med3_f32 v142, v142, s78, v240
	v_pk_fma_f32 v[144:145], v[140:141], v[140:141], v[144:145]
	v_med3_f32 v140, v140, s78, v240
	v_mov_b32_e32 v154, 0
	v_cvt_pk_fp8_f32 v154, v140, v142
	v_and_b32_e32 v151, 0xffff0000, v121
	v_and_b32_e32 v150, 0xffff0000, v120
	v_lshlrev_b32_e32 v147, 16, v121
	v_lshlrev_b32_e32 v146, 16, v120
	v_pk_mul_f32 v[152:153], v[150:151], v[150:151]
	v_add_f32_e32 v148, v144, v145
	v_pk_fma_f32 v[152:153], v[146:147], v[146:147], v[152:153]
	v_med3_f32 v140, v141, s78, v240
	v_med3_f32 v141, v143, s78, v240
	v_med3_f32 v144, v146, s78, v240
	v_med3_f32 v145, v150, s78, v240
	v_add_u32_e32 v146, v175, v196
	v_mov_b32_e32 v155, 0
	v_cvt_pk_fp8_f32 v154, v140, v141 op_sel:[0,0,1]
	ds_read_b128 v[140:143], v146
	v_cvt_pk_fp8_f32 v155, v144, v145
	v_med3_f32 v150, v147, s78, v240
	ds_read_b128 v[144:147], v146 offset:32768
	s_waitcnt lgkmcnt(1)
	v_mfma_f32_16x16x32_bf16 v[132:135], v[118:121], v[140:143], v[132:135]
	v_add_u32_e32 v140, v176, v196
	ds_read_b128 v[140:143], v140
	v_med3_f32 v151, v151, s78, v240
	s_waitcnt lgkmcnt(1)
	v_mfma_f32_16x16x32_bf16 v[136:139], v[118:121], v[144:147], v[136:139]
	v_add_u32_e32 v144, v177, v196
	ds_read_b128 v[144:147], v144
	v_cvt_pk_fp8_f32 v155, v150, v151 op_sel:[0,0,1]
	s_waitcnt lgkmcnt(1)
	v_mfma_f32_16x16x32_bf16 v[132:135], v[118:121], v[140:143], v[132:135]
	v_add_f32_e32 v140, v152, v148
	v_pk_add_f32 v[150:151], v[152:153], v[140:141] op_sel_hi:[1,0]
	global_store_dwordx2 v[130:131], v[154:155], off offset:64
	s_waitcnt lgkmcnt(0)
	v_mfma_f32_16x16x32_bf16 v[136:139], v[118:121], v[144:147], v[136:139]
	s_waitcnt vmcnt(30)
	v_lshlrev_b32_e32 v144, 16, v114
	v_and_b32_e32 v145, 0xffff0000, v114
	v_mul_f32_e32 v140, v144, v144
	v_add_u32_e32 v147, v175, v197
	v_pk_fma_f32 v[152:153], v[144:145], v[144:145], v[140:141] op_sel_hi:[1,1,0]
	v_lshlrev_b32_e32 v154, 16, v115
	ds_read_b128 v[140:143], v147
	v_and_b32_e32 v155, 0xffff0000, v115
	v_mul_f32_e32 v146, v154, v154
	v_pk_fma_f32 v[156:157], v[154:155], v[154:155], v[146:147] op_sel_hi:[1,1,0]
	v_med3_f32 v148, v144, s78, v240
	v_med3_f32 v150, v145, s78, v240
	ds_read_b128 v[144:147], v147 offset:32768
	s_waitcnt lgkmcnt(1)
	v_mfma_f32_16x16x32_bf16 v[132:135], v[114:117], v[140:143], v[132:135]
	v_add_u32_e32 v140, v176, v197
	ds_read_b128 v[140:143], v140
	v_mov_b32_e32 v158, 0
	s_waitcnt lgkmcnt(1)
	v_mfma_f32_16x16x32_bf16 v[136:139], v[114:117], v[144:147], v[136:139]
	v_add_u32_e32 v144, v177, v197
	v_cvt_pk_fp8_f32 v158, v148, v150
	ds_read_b128 v[144:147], v144
	s_waitcnt lgkmcnt(1)
	v_mfma_f32_16x16x32_bf16 v[132:135], v[114:117], v[140:143], v[132:135]
	v_med3_f32 v140, v154, s78, v240
	v_med3_f32 v141, v155, s78, v240
	v_cvt_pk_fp8_f32 v158, v140, v141 op_sel:[0,0,1]
	v_lshlrev_b32_e32 v141, 16, v116
	v_and_b32_e32 v143, 0xffff0000, v116
	s_waitcnt lgkmcnt(0)
	v_mfma_f32_16x16x32_bf16 v[136:139], v[114:117], v[144:147], v[136:139]
	v_med3_f32 v142, v141, s78, v240
	v_med3_f32 v144, v143, s78, v240
	v_mov_b32_e32 v159, 0
	v_cvt_pk_fp8_f32 v159, v142, v144
	v_lshlrev_b32_e32 v145, 16, v117
	v_and_b32_e32 v147, 0xffff0000, v117
	v_med3_f32 v142, v145, s78, v240
	v_med3_f32 v144, v147, s78, v240
	global_store_dwordx2 v[130:131], v[160:161], off offset:32
	s_waitcnt vmcnt(30)
	v_lshlrev_b32_e32 v160, 16, v111
	v_and_b32_e32 v161, 0xffff0000, v111
	v_cvt_pk_fp8_f32 v159, v142, v144 op_sel:[0,0,1]
	v_and_b32_e32 v142, 0xffff0000, v110
	v_mul_f32_e32 v152, v160, v160
	v_mul_f32_e32 v156, v161, v161
	v_lshlrev_b32_e32 v140, 16, v110
	v_pk_mul_f32 v[154:155], v[142:143], v[142:143]
	v_and_b32_e32 v146, 0xffff0000, v112
	v_pk_fma_f32 v[154:155], v[140:141], v[140:141], v[154:155]
	v_pk_add_f32 v[152:153], v[152:153], v[156:157]
	v_lshlrev_b32_e32 v144, 16, v112
	v_pk_add_f32 v[152:153], v[154:155], v[152:153]
	v_pk_mul_f32 v[154:155], v[146:147], v[146:147]
	v_med3_f32 v140, v140, s78, v240
	v_pk_fma_f32 v[154:155], v[144:145], v[144:145], v[154:155]
	v_med3_f32 v141, v142, s78, v240
	v_pk_add_f32 v[152:153], v[154:155], v[152:153]
	v_mov_b32_e32 v154, 0
	v_cvt_pk_fp8_f32 v154, v140, v141
	v_med3_f32 v140, v160, s78, v240
	v_med3_f32 v141, v161, s78, v240
	v_med3_f32 v145, v146, s78, v240
	v_add_u32_e32 v146, v175, v198
	v_cvt_pk_fp8_f32 v154, v140, v141 op_sel:[0,0,1]
	v_med3_f32 v144, v144, s78, v240
	ds_read_b128 v[140:143], v146
	v_mov_b32_e32 v155, 0
	v_cvt_pk_fp8_f32 v155, v144, v145
	ds_read_b128 v[144:147], v146 offset:32768
	s_waitcnt lgkmcnt(1)
	v_mfma_f32_16x16x32_bf16 v[132:135], v[110:113], v[140:143], v[132:135]
	v_add_u32_e32 v140, v176, v198
	v_lshlrev_b32_e32 v173, 16, v113
	v_and_b32_e32 v243, 0xffff0000, v113
	ds_read_b128 v[140:143], v140
	s_waitcnt lgkmcnt(1)
	v_mfma_f32_16x16x32_bf16 v[136:139], v[110:113], v[144:147], v[136:139]
	v_add_u32_e32 v144, v177, v198
	v_mul_f32_e32 v150, v173, v173
	v_mul_f32_e32 v148, v243, v243
	ds_read_b128 v[144:147], v144
	v_pk_add_f32 v[148:149], v[150:151], v[148:149]
	v_med3_f32 v150, v173, s78, v240
	v_med3_f32 v151, v243, s78, v240
	v_cvt_pk_fp8_f32 v155, v150, v151 op_sel:[0,0,1]
	s_waitcnt lgkmcnt(1)
	v_mfma_f32_16x16x32_bf16 v[132:135], v[110:113], v[140:143], v[132:135]
	v_add_f32_e64 v140, v152, v148
	v_add_f32_e64 v141, v153, v149
	s_waitcnt vmcnt(29)
	v_and_b32_e32 v143, 0xffff0000, v107
	v_and_b32_e32 v142, 0xffff0000, v106
	v_pk_add_f32 v[148:149], v[140:141], v[140:141] op_sel_hi:[0,1]
	s_waitcnt lgkmcnt(0)
	v_mfma_f32_16x16x32_bf16 v[136:139], v[110:113], v[144:147], v[136:139]
	v_lshlrev_b32_e32 v141, 16, v107
	v_lshlrev_b32_e32 v140, 16, v106
	v_pk_mul_f32 v[144:145], v[142:143], v[142:143]
	global_store_dwordx2 v[130:131], v[154:155], off offset:128
	v_pk_fma_f32 v[144:145], v[140:141], v[140:141], v[144:145]
	v_med3_f32 v140, v140, s78, v240
	v_med3_f32 v142, v142, s78, v240
	v_mov_b32_e32 v154, 0
	v_cvt_pk_fp8_f32 v154, v140, v142
	v_and_b32_e32 v151, 0xffff0000, v109
	v_and_b32_e32 v150, 0xffff0000, v108
	v_lshlrev_b32_e32 v147, 16, v109
	v_lshlrev_b32_e32 v146, 16, v108
	v_pk_mul_f32 v[152:153], v[150:151], v[150:151]
	v_add_f32_e32 v148, v144, v145
	v_pk_fma_f32 v[152:153], v[146:147], v[146:147], v[152:153]
	v_med3_f32 v140, v141, s78, v240
	v_med3_f32 v141, v143, s78, v240
	v_med3_f32 v144, v146, s78, v240
	v_med3_f32 v145, v150, s78, v240
	v_add_u32_e32 v146, v175, v199
	v_mov_b32_e32 v155, 0
	v_cvt_pk_fp8_f32 v154, v140, v141 op_sel:[0,0,1]
	ds_read_b128 v[140:143], v146
	v_cvt_pk_fp8_f32 v155, v144, v145
	v_med3_f32 v150, v147, s78, v240
	ds_read_b128 v[144:147], v146 offset:32768
	s_waitcnt lgkmcnt(1)
	v_mfma_f32_16x16x32_bf16 v[132:135], v[106:109], v[140:143], v[132:135]
	v_add_u32_e32 v140, v176, v199
	ds_read_b128 v[140:143], v140
	v_med3_f32 v151, v151, s78, v240
	s_waitcnt lgkmcnt(1)
	v_mfma_f32_16x16x32_bf16 v[136:139], v[106:109], v[144:147], v[136:139]
	v_add_u32_e32 v144, v177, v199
	ds_read_b128 v[144:147], v144
	v_cvt_pk_fp8_f32 v155, v150, v151 op_sel:[0,0,1]
	s_waitcnt lgkmcnt(1)
	v_mfma_f32_16x16x32_bf16 v[132:135], v[106:109], v[140:143], v[132:135]
	v_add_f32_e32 v140, v152, v148
	v_pk_add_f32 v[150:151], v[152:153], v[140:141] op_sel_hi:[1,0]
	global_store_dwordx2 v[130:131], v[154:155], off offset:160
	s_waitcnt lgkmcnt(0)
	v_mfma_f32_16x16x32_bf16 v[136:139], v[106:109], v[144:147], v[136:139]
	s_waitcnt vmcnt(30)
	v_lshlrev_b32_e32 v144, 16, v102
	v_and_b32_e32 v145, 0xffff0000, v102
	v_mul_f32_e32 v140, v144, v144
	v_add_u32_e32 v147, v175, v200
	v_pk_fma_f32 v[152:153], v[144:145], v[144:145], v[140:141] op_sel_hi:[1,1,0]
	v_lshlrev_b32_e32 v154, 16, v103
	ds_read_b128 v[140:143], v147
	v_and_b32_e32 v155, 0xffff0000, v103
	v_mul_f32_e32 v146, v154, v154
	v_pk_fma_f32 v[156:157], v[154:155], v[154:155], v[146:147] op_sel_hi:[1,1,0]
	v_med3_f32 v148, v144, s78, v240
	v_med3_f32 v150, v145, s78, v240
	ds_read_b128 v[144:147], v147 offset:32768
	s_waitcnt lgkmcnt(1)
	v_mfma_f32_16x16x32_bf16 v[132:135], v[102:105], v[140:143], v[132:135]
	v_add_u32_e32 v140, v176, v200
	ds_read_b128 v[140:143], v140
	global_store_dwordx2 v[130:131], v[158:159], off offset:96
	v_mov_b32_e32 v158, 0
	s_waitcnt lgkmcnt(1)
	v_mfma_f32_16x16x32_bf16 v[136:139], v[102:105], v[144:147], v[136:139]
	v_add_u32_e32 v144, v177, v200
	v_cvt_pk_fp8_f32 v158, v148, v150
	ds_read_b128 v[144:147], v144
	s_waitcnt lgkmcnt(1)
	v_mfma_f32_16x16x32_bf16 v[132:135], v[102:105], v[140:143], v[132:135]
	v_med3_f32 v140, v154, s78, v240
	v_med3_f32 v141, v155, s78, v240
	v_cvt_pk_fp8_f32 v158, v140, v141 op_sel:[0,0,1]
	v_lshlrev_b32_e32 v141, 16, v104
	v_and_b32_e32 v143, 0xffff0000, v104
	s_waitcnt lgkmcnt(0)
	v_mfma_f32_16x16x32_bf16 v[136:139], v[102:105], v[144:147], v[136:139]
	v_med3_f32 v142, v141, s78, v240
	v_med3_f32 v144, v143, s78, v240
	v_mov_b32_e32 v159, 0
	v_cvt_pk_fp8_f32 v159, v142, v144
	v_lshlrev_b32_e32 v145, 16, v105
	v_and_b32_e32 v147, 0xffff0000, v105
	v_med3_f32 v142, v145, s78, v240
	v_med3_f32 v144, v147, s78, v240
	s_waitcnt vmcnt(30)
	v_lshlrev_b32_e32 v160, 16, v99
	v_and_b32_e32 v161, 0xffff0000, v99
	v_cvt_pk_fp8_f32 v159, v142, v144 op_sel:[0,0,1]
	v_and_b32_e32 v142, 0xffff0000, v98
	v_mul_f32_e32 v152, v160, v160
	v_mul_f32_e32 v156, v161, v161
	v_lshlrev_b32_e32 v140, 16, v98
	v_pk_mul_f32 v[154:155], v[142:143], v[142:143]
	v_and_b32_e32 v146, 0xffff0000, v100
	v_pk_fma_f32 v[154:155], v[140:141], v[140:141], v[154:155]
	v_pk_add_f32 v[152:153], v[152:153], v[156:157]
	v_lshlrev_b32_e32 v144, 16, v100
	v_pk_add_f32 v[152:153], v[154:155], v[152:153]
	v_pk_mul_f32 v[154:155], v[146:147], v[146:147]
	v_med3_f32 v140, v140, s78, v240
	v_pk_fma_f32 v[154:155], v[144:145], v[144:145], v[154:155]
	v_med3_f32 v141, v142, s78, v240
	v_pk_add_f32 v[152:153], v[154:155], v[152:153]
	v_mov_b32_e32 v154, 0
	v_cvt_pk_fp8_f32 v154, v140, v141
	v_med3_f32 v140, v160, s78, v240
	v_med3_f32 v141, v161, s78, v240
	v_med3_f32 v145, v146, s78, v240
	v_add_u32_e32 v146, v175, v201
	v_cvt_pk_fp8_f32 v154, v140, v141 op_sel:[0,0,1]
	v_med3_f32 v144, v144, s78, v240
	ds_read_b128 v[140:143], v146
	v_mov_b32_e32 v155, 0
	v_cvt_pk_fp8_f32 v155, v144, v145
	ds_read_b128 v[144:147], v146 offset:32768
	s_waitcnt lgkmcnt(1)
	v_mfma_f32_16x16x32_bf16 v[132:135], v[98:101], v[140:143], v[132:135]
	v_add_u32_e32 v140, v176, v201
	v_lshlrev_b32_e32 v173, 16, v101
	v_and_b32_e32 v243, 0xffff0000, v101
	ds_read_b128 v[140:143], v140
	s_waitcnt lgkmcnt(1)
	v_mfma_f32_16x16x32_bf16 v[136:139], v[98:101], v[144:147], v[136:139]
	v_add_u32_e32 v144, v177, v201
	v_mul_f32_e32 v150, v173, v173
	v_mul_f32_e32 v148, v243, v243
	ds_read_b128 v[144:147], v144
	v_pk_add_f32 v[148:149], v[150:151], v[148:149]
	v_med3_f32 v150, v173, s78, v240
	v_med3_f32 v151, v243, s78, v240
	v_cvt_pk_fp8_f32 v155, v150, v151 op_sel:[0,0,1]
	s_waitcnt lgkmcnt(1)
	v_mfma_f32_16x16x32_bf16 v[132:135], v[98:101], v[140:143], v[132:135]
	v_add_f32_e64 v140, v152, v148
	v_add_f32_e64 v141, v153, v149
	s_waitcnt vmcnt(29)
	v_and_b32_e32 v143, 0xffff0000, v95
	v_and_b32_e32 v142, 0xffff0000, v94
	v_pk_add_f32 v[148:149], v[140:141], v[140:141] op_sel_hi:[0,1]
	s_waitcnt lgkmcnt(0)
	v_mfma_f32_16x16x32_bf16 v[136:139], v[98:101], v[144:147], v[136:139]
	v_lshlrev_b32_e32 v141, 16, v95
	v_lshlrev_b32_e32 v140, 16, v94
	v_pk_mul_f32 v[144:145], v[142:143], v[142:143]
	global_store_dwordx2 v[130:131], v[154:155], off offset:224
	v_pk_fma_f32 v[144:145], v[140:141], v[140:141], v[144:145]
	v_med3_f32 v140, v140, s78, v240
	v_med3_f32 v142, v142, s78, v240
	v_mov_b32_e32 v154, 0
	v_cvt_pk_fp8_f32 v154, v140, v142
	v_and_b32_e32 v151, 0xffff0000, v97
	v_and_b32_e32 v150, 0xffff0000, v96
	v_lshlrev_b32_e32 v147, 16, v97
	v_lshlrev_b32_e32 v146, 16, v96
	v_pk_mul_f32 v[152:153], v[150:151], v[150:151]
	v_add_f32_e32 v148, v144, v145
	v_pk_fma_f32 v[152:153], v[146:147], v[146:147], v[152:153]
	v_med3_f32 v140, v141, s78, v240
	v_med3_f32 v141, v143, s78, v240
	v_med3_f32 v144, v146, s78, v240
	v_med3_f32 v145, v150, s78, v240
	v_add_u32_e32 v146, v175, v202
	v_mov_b32_e32 v155, 0
	v_cvt_pk_fp8_f32 v154, v140, v141 op_sel:[0,0,1]
	ds_read_b128 v[140:143], v146
	v_cvt_pk_fp8_f32 v155, v144, v145
	v_med3_f32 v150, v147, s78, v240
	ds_read_b128 v[144:147], v146 offset:32768
	s_waitcnt lgkmcnt(1)
	v_mfma_f32_16x16x32_bf16 v[132:135], v[94:97], v[140:143], v[132:135]
	v_add_u32_e32 v140, v176, v202
	ds_read_b128 v[140:143], v140
	v_med3_f32 v151, v151, s78, v240
	s_waitcnt lgkmcnt(1)
	v_mfma_f32_16x16x32_bf16 v[136:139], v[94:97], v[144:147], v[136:139]
	v_add_u32_e32 v144, v177, v202
	ds_read_b128 v[144:147], v144
	v_cvt_pk_fp8_f32 v155, v150, v151 op_sel:[0,0,1]
	s_waitcnt lgkmcnt(1)
	v_mfma_f32_16x16x32_bf16 v[132:135], v[94:97], v[140:143], v[132:135]
	v_add_f32_e32 v140, v152, v148
	v_pk_add_f32 v[150:151], v[152:153], v[140:141] op_sel_hi:[1,0]
	global_store_dwordx2 v[130:131], v[154:155], off offset:256
	s_waitcnt lgkmcnt(0)
	v_mfma_f32_16x16x32_bf16 v[136:139], v[94:97], v[144:147], v[136:139]
	s_waitcnt vmcnt(30)
	v_lshlrev_b32_e32 v144, 16, v90
	v_and_b32_e32 v145, 0xffff0000, v90
	v_mul_f32_e32 v140, v144, v144
	v_add_u32_e32 v147, v175, v203
	v_pk_fma_f32 v[152:153], v[144:145], v[144:145], v[140:141] op_sel_hi:[1,1,0]
	v_lshlrev_b32_e32 v154, 16, v91
	ds_read_b128 v[140:143], v147
	v_and_b32_e32 v155, 0xffff0000, v91
	v_mul_f32_e32 v146, v154, v154
	v_pk_fma_f32 v[156:157], v[154:155], v[154:155], v[146:147] op_sel_hi:[1,1,0]
	v_med3_f32 v148, v144, s78, v240
	v_med3_f32 v150, v145, s78, v240
	ds_read_b128 v[144:147], v147 offset:32768
	s_waitcnt lgkmcnt(1)
	v_mfma_f32_16x16x32_bf16 v[132:135], v[90:93], v[140:143], v[132:135]
	v_add_u32_e32 v140, v176, v203
	ds_read_b128 v[140:143], v140
	global_store_dwordx2 v[130:131], v[158:159], off offset:192
	v_mov_b32_e32 v158, 0
	s_waitcnt lgkmcnt(1)
	v_mfma_f32_16x16x32_bf16 v[136:139], v[90:93], v[144:147], v[136:139]
	v_add_u32_e32 v144, v177, v203
	v_cvt_pk_fp8_f32 v158, v148, v150
	ds_read_b128 v[144:147], v144
	s_waitcnt lgkmcnt(1)
	v_mfma_f32_16x16x32_bf16 v[132:135], v[90:93], v[140:143], v[132:135]
	v_med3_f32 v140, v154, s78, v240
	v_med3_f32 v141, v155, s78, v240
	v_cvt_pk_fp8_f32 v158, v140, v141 op_sel:[0,0,1]
	v_lshlrev_b32_e32 v141, 16, v92
	v_and_b32_e32 v143, 0xffff0000, v92
	s_waitcnt lgkmcnt(0)
	v_mfma_f32_16x16x32_bf16 v[136:139], v[90:93], v[144:147], v[136:139]
	v_med3_f32 v142, v141, s78, v240
	v_med3_f32 v144, v143, s78, v240
	v_mov_b32_e32 v159, 0
	v_cvt_pk_fp8_f32 v159, v142, v144
	v_lshlrev_b32_e32 v145, 16, v93
	v_and_b32_e32 v147, 0xffff0000, v93
	v_med3_f32 v142, v145, s78, v240
	v_med3_f32 v144, v147, s78, v240
	s_waitcnt vmcnt(30)
	v_lshlrev_b32_e32 v160, 16, v87
	v_and_b32_e32 v161, 0xffff0000, v87
	v_cvt_pk_fp8_f32 v159, v142, v144 op_sel:[0,0,1]
	v_and_b32_e32 v142, 0xffff0000, v86
	v_mul_f32_e32 v152, v160, v160
	v_mul_f32_e32 v156, v161, v161
	v_lshlrev_b32_e32 v140, 16, v86
	v_pk_mul_f32 v[154:155], v[142:143], v[142:143]
	v_and_b32_e32 v146, 0xffff0000, v88
	v_pk_fma_f32 v[154:155], v[140:141], v[140:141], v[154:155]
	v_pk_add_f32 v[152:153], v[152:153], v[156:157]
	v_lshlrev_b32_e32 v144, 16, v88
	v_pk_add_f32 v[152:153], v[154:155], v[152:153]
	v_pk_mul_f32 v[154:155], v[146:147], v[146:147]
	v_med3_f32 v140, v140, s78, v240
	v_pk_fma_f32 v[154:155], v[144:145], v[144:145], v[154:155]
	v_med3_f32 v141, v142, s78, v240
	v_pk_add_f32 v[152:153], v[154:155], v[152:153]
	v_mov_b32_e32 v154, 0
	v_cvt_pk_fp8_f32 v154, v140, v141
	v_med3_f32 v140, v160, s78, v240
	v_med3_f32 v141, v161, s78, v240
	v_med3_f32 v145, v146, s78, v240
	v_add_u32_e32 v146, v175, v204
	v_cvt_pk_fp8_f32 v154, v140, v141 op_sel:[0,0,1]
	v_med3_f32 v144, v144, s78, v240
	ds_read_b128 v[140:143], v146
	v_mov_b32_e32 v155, 0
	v_cvt_pk_fp8_f32 v155, v144, v145
	ds_read_b128 v[144:147], v146 offset:32768
	s_waitcnt lgkmcnt(1)
	v_mfma_f32_16x16x32_bf16 v[132:135], v[86:89], v[140:143], v[132:135]
	v_add_u32_e32 v140, v176, v204
	v_lshlrev_b32_e32 v173, 16, v89
	v_and_b32_e32 v243, 0xffff0000, v89
	ds_read_b128 v[140:143], v140
	s_waitcnt lgkmcnt(1)
	v_mfma_f32_16x16x32_bf16 v[136:139], v[86:89], v[144:147], v[136:139]
	v_add_u32_e32 v144, v177, v204
	v_mul_f32_e32 v150, v173, v173
	v_mul_f32_e32 v148, v243, v243
	ds_read_b128 v[144:147], v144
	v_pk_add_f32 v[148:149], v[150:151], v[148:149]
	v_med3_f32 v150, v173, s78, v240
	v_med3_f32 v151, v243, s78, v240
	v_cvt_pk_fp8_f32 v155, v150, v151 op_sel:[0,0,1]
	s_waitcnt lgkmcnt(1)
	v_mfma_f32_16x16x32_bf16 v[132:135], v[86:89], v[140:143], v[132:135]
	v_add_f32_e64 v140, v152, v148
	v_add_f32_e64 v141, v153, v149
	s_waitcnt vmcnt(29)
	v_and_b32_e32 v143, 0xffff0000, v83
	v_and_b32_e32 v142, 0xffff0000, v82
	v_pk_add_f32 v[148:149], v[140:141], v[140:141] op_sel_hi:[0,1]
	s_waitcnt lgkmcnt(0)
	v_mfma_f32_16x16x32_bf16 v[136:139], v[86:89], v[144:147], v[136:139]
	v_lshlrev_b32_e32 v141, 16, v83
	v_lshlrev_b32_e32 v140, 16, v82
	v_pk_mul_f32 v[144:145], v[142:143], v[142:143]
	global_store_dwordx2 v[130:131], v[154:155], off offset:320
	v_pk_fma_f32 v[144:145], v[140:141], v[140:141], v[144:145]
	v_med3_f32 v140, v140, s78, v240
	v_med3_f32 v142, v142, s78, v240
	v_mov_b32_e32 v154, 0
	v_cvt_pk_fp8_f32 v154, v140, v142
	v_and_b32_e32 v151, 0xffff0000, v85
	v_and_b32_e32 v150, 0xffff0000, v84
	v_lshlrev_b32_e32 v147, 16, v85
	v_lshlrev_b32_e32 v146, 16, v84
	v_pk_mul_f32 v[152:153], v[150:151], v[150:151]
	v_add_f32_e32 v148, v144, v145
	v_pk_fma_f32 v[152:153], v[146:147], v[146:147], v[152:153]
	v_med3_f32 v140, v141, s78, v240
	v_med3_f32 v141, v143, s78, v240
	v_med3_f32 v144, v146, s78, v240
	v_med3_f32 v145, v150, s78, v240
	v_add_u32_e32 v146, v175, v205
	v_mov_b32_e32 v155, 0
	v_cvt_pk_fp8_f32 v154, v140, v141 op_sel:[0,0,1]
	ds_read_b128 v[140:143], v146
	v_cvt_pk_fp8_f32 v155, v144, v145
	v_med3_f32 v150, v147, s78, v240
	ds_read_b128 v[144:147], v146 offset:32768
	s_waitcnt lgkmcnt(1)
	v_mfma_f32_16x16x32_bf16 v[132:135], v[82:85], v[140:143], v[132:135]
	v_add_u32_e32 v140, v176, v205
	ds_read_b128 v[140:143], v140
	v_med3_f32 v151, v151, s78, v240
	s_waitcnt lgkmcnt(1)
	v_mfma_f32_16x16x32_bf16 v[136:139], v[82:85], v[144:147], v[136:139]
	v_add_u32_e32 v144, v177, v205
	ds_read_b128 v[144:147], v144
	v_cvt_pk_fp8_f32 v155, v150, v151 op_sel:[0,0,1]
	s_waitcnt lgkmcnt(1)
	v_mfma_f32_16x16x32_bf16 v[132:135], v[82:85], v[140:143], v[132:135]
	v_add_f32_e32 v140, v152, v148
	v_pk_add_f32 v[150:151], v[152:153], v[140:141] op_sel_hi:[1,0]
	global_store_dwordx2 v[130:131], v[154:155], off offset:352
	s_waitcnt lgkmcnt(0)
	v_mfma_f32_16x16x32_bf16 v[136:139], v[82:85], v[144:147], v[136:139]
	s_waitcnt vmcnt(30)
	v_lshlrev_b32_e32 v144, 16, v78
	v_and_b32_e32 v145, 0xffff0000, v78
	v_mul_f32_e32 v140, v144, v144
	v_add_u32_e32 v147, v175, v206
	v_pk_fma_f32 v[152:153], v[144:145], v[144:145], v[140:141] op_sel_hi:[1,1,0]
	v_lshlrev_b32_e32 v154, 16, v79
	ds_read_b128 v[140:143], v147
	v_and_b32_e32 v155, 0xffff0000, v79
	v_mul_f32_e32 v146, v154, v154
	v_pk_fma_f32 v[156:157], v[154:155], v[154:155], v[146:147] op_sel_hi:[1,1,0]
	v_med3_f32 v148, v144, s78, v240
	v_med3_f32 v150, v145, s78, v240
	ds_read_b128 v[144:147], v147 offset:32768
	s_waitcnt lgkmcnt(1)
	v_mfma_f32_16x16x32_bf16 v[132:135], v[78:81], v[140:143], v[132:135]
	v_add_u32_e32 v140, v176, v206
	ds_read_b128 v[140:143], v140
	global_store_dwordx2 v[130:131], v[158:159], off offset:288
	v_mov_b32_e32 v158, 0
	s_waitcnt lgkmcnt(1)
	v_mfma_f32_16x16x32_bf16 v[136:139], v[78:81], v[144:147], v[136:139]
	v_add_u32_e32 v144, v177, v206
	v_cvt_pk_fp8_f32 v158, v148, v150
	ds_read_b128 v[144:147], v144
	s_waitcnt lgkmcnt(1)
	v_mfma_f32_16x16x32_bf16 v[132:135], v[78:81], v[140:143], v[132:135]
	v_med3_f32 v140, v154, s78, v240
	v_med3_f32 v141, v155, s78, v240
	v_cvt_pk_fp8_f32 v158, v140, v141 op_sel:[0,0,1]
	v_lshlrev_b32_e32 v141, 16, v80
	v_and_b32_e32 v143, 0xffff0000, v80
	s_waitcnt lgkmcnt(0)
	v_mfma_f32_16x16x32_bf16 v[136:139], v[78:81], v[144:147], v[136:139]
	v_med3_f32 v142, v141, s78, v240
	v_med3_f32 v144, v143, s78, v240
	v_mov_b32_e32 v159, 0
	v_cvt_pk_fp8_f32 v159, v142, v144
	v_lshlrev_b32_e32 v145, 16, v81
	v_and_b32_e32 v147, 0xffff0000, v81
	v_med3_f32 v142, v145, s78, v240
	v_med3_f32 v144, v147, s78, v240
	s_waitcnt vmcnt(30)
	v_lshlrev_b32_e32 v160, 16, v75
	v_and_b32_e32 v161, 0xffff0000, v75
	v_cvt_pk_fp8_f32 v159, v142, v144 op_sel:[0,0,1]
	v_and_b32_e32 v142, 0xffff0000, v74
	v_mul_f32_e32 v152, v160, v160
	v_mul_f32_e32 v156, v161, v161
	v_lshlrev_b32_e32 v140, 16, v74
	v_pk_mul_f32 v[154:155], v[142:143], v[142:143]
	v_and_b32_e32 v146, 0xffff0000, v76
	v_pk_fma_f32 v[154:155], v[140:141], v[140:141], v[154:155]
	v_pk_add_f32 v[152:153], v[152:153], v[156:157]
	v_lshlrev_b32_e32 v144, 16, v76
	v_pk_add_f32 v[152:153], v[154:155], v[152:153]
	v_pk_mul_f32 v[154:155], v[146:147], v[146:147]
	v_med3_f32 v140, v140, s78, v240
	v_pk_fma_f32 v[154:155], v[144:145], v[144:145], v[154:155]
	v_med3_f32 v141, v142, s78, v240
	v_pk_add_f32 v[152:153], v[154:155], v[152:153]
	v_mov_b32_e32 v154, 0
	v_cvt_pk_fp8_f32 v154, v140, v141
	v_med3_f32 v140, v160, s78, v240
	v_med3_f32 v141, v161, s78, v240
	v_med3_f32 v145, v146, s78, v240
	v_add_u32_e32 v146, v175, v207
	v_cvt_pk_fp8_f32 v154, v140, v141 op_sel:[0,0,1]
	v_med3_f32 v144, v144, s78, v240
	ds_read_b128 v[140:143], v146
	v_mov_b32_e32 v155, 0
	v_cvt_pk_fp8_f32 v155, v144, v145
	ds_read_b128 v[144:147], v146 offset:32768
	s_waitcnt lgkmcnt(1)
	v_mfma_f32_16x16x32_bf16 v[132:135], v[74:77], v[140:143], v[132:135]
	v_add_u32_e32 v140, v176, v207
	v_lshlrev_b32_e32 v173, 16, v77
	v_and_b32_e32 v243, 0xffff0000, v77
	ds_read_b128 v[140:143], v140
	s_waitcnt lgkmcnt(1)
	v_mfma_f32_16x16x32_bf16 v[136:139], v[74:77], v[144:147], v[136:139]
	v_add_u32_e32 v144, v177, v207
	v_mul_f32_e32 v150, v173, v173
	v_mul_f32_e32 v148, v243, v243
	ds_read_b128 v[144:147], v144
	v_pk_add_f32 v[148:149], v[150:151], v[148:149]
	v_med3_f32 v150, v173, s78, v240
	v_med3_f32 v151, v243, s78, v240
	v_cvt_pk_fp8_f32 v155, v150, v151 op_sel:[0,0,1]
	s_waitcnt lgkmcnt(1)
	v_mfma_f32_16x16x32_bf16 v[132:135], v[74:77], v[140:143], v[132:135]
	v_add_f32_e64 v140, v152, v148
	v_add_f32_e64 v141, v153, v149
	s_waitcnt vmcnt(29)
	v_and_b32_e32 v143, 0xffff0000, v71
	v_and_b32_e32 v142, 0xffff0000, v70
	v_pk_add_f32 v[148:149], v[140:141], v[140:141] op_sel_hi:[0,1]
	s_waitcnt lgkmcnt(0)
	v_mfma_f32_16x16x32_bf16 v[136:139], v[74:77], v[144:147], v[136:139]
	v_lshlrev_b32_e32 v141, 16, v71
	v_lshlrev_b32_e32 v140, 16, v70
	v_pk_mul_f32 v[144:145], v[142:143], v[142:143]
	global_store_dwordx2 v[130:131], v[154:155], off offset:416
	v_pk_fma_f32 v[144:145], v[140:141], v[140:141], v[144:145]
	v_med3_f32 v140, v140, s78, v240
	v_med3_f32 v142, v142, s78, v240
	v_mov_b32_e32 v154, 0
	v_cvt_pk_fp8_f32 v154, v140, v142
	v_and_b32_e32 v151, 0xffff0000, v73
	v_and_b32_e32 v150, 0xffff0000, v72
	v_lshlrev_b32_e32 v147, 16, v73
	v_lshlrev_b32_e32 v146, 16, v72
	v_pk_mul_f32 v[152:153], v[150:151], v[150:151]
	v_add_f32_e32 v148, v144, v145
	v_pk_fma_f32 v[152:153], v[146:147], v[146:147], v[152:153]
	v_med3_f32 v140, v141, s78, v240
	v_med3_f32 v141, v143, s78, v240
	v_med3_f32 v144, v146, s78, v240
	v_med3_f32 v145, v150, s78, v240
	v_add_u32_e32 v146, v175, v208
	v_mov_b32_e32 v155, 0
	v_cvt_pk_fp8_f32 v154, v140, v141 op_sel:[0,0,1]
	ds_read_b128 v[140:143], v146
	v_cvt_pk_fp8_f32 v155, v144, v145
	v_med3_f32 v150, v147, s78, v240
	ds_read_b128 v[144:147], v146 offset:32768
	s_waitcnt lgkmcnt(1)
	v_mfma_f32_16x16x32_bf16 v[132:135], v[70:73], v[140:143], v[132:135]
	v_add_u32_e32 v140, v176, v208
	ds_read_b128 v[140:143], v140
	v_med3_f32 v151, v151, s78, v240
	s_waitcnt lgkmcnt(1)
	v_mfma_f32_16x16x32_bf16 v[136:139], v[70:73], v[144:147], v[136:139]
	v_add_u32_e32 v144, v177, v208
	ds_read_b128 v[144:147], v144
	v_cvt_pk_fp8_f32 v155, v150, v151 op_sel:[0,0,1]
	s_waitcnt lgkmcnt(1)
	v_mfma_f32_16x16x32_bf16 v[132:135], v[70:73], v[140:143], v[132:135]
	v_add_f32_e32 v140, v152, v148
	v_pk_add_f32 v[150:151], v[152:153], v[140:141] op_sel_hi:[1,0]
	global_store_dwordx2 v[130:131], v[154:155], off offset:448
	s_waitcnt lgkmcnt(0)
	v_mfma_f32_16x16x32_bf16 v[136:139], v[70:73], v[144:147], v[136:139]
	s_waitcnt vmcnt(30)
	v_lshlrev_b32_e32 v144, 16, v66
	v_and_b32_e32 v145, 0xffff0000, v66
	v_mul_f32_e32 v140, v144, v144
	v_add_u32_e32 v147, v175, v209
	v_pk_fma_f32 v[152:153], v[144:145], v[144:145], v[140:141] op_sel_hi:[1,1,0]
	v_lshlrev_b32_e32 v154, 16, v67
	ds_read_b128 v[140:143], v147
	v_and_b32_e32 v155, 0xffff0000, v67
	v_mul_f32_e32 v146, v154, v154
	v_pk_fma_f32 v[156:157], v[154:155], v[154:155], v[146:147] op_sel_hi:[1,1,0]
	v_med3_f32 v148, v144, s78, v240
	v_med3_f32 v150, v145, s78, v240
	ds_read_b128 v[144:147], v147 offset:32768
	s_waitcnt lgkmcnt(1)
	v_mfma_f32_16x16x32_bf16 v[132:135], v[66:69], v[140:143], v[132:135]
	v_add_u32_e32 v140, v176, v209
	ds_read_b128 v[140:143], v140
	global_store_dwordx2 v[130:131], v[158:159], off offset:384
	v_mov_b32_e32 v158, 0
	s_waitcnt lgkmcnt(1)
	v_mfma_f32_16x16x32_bf16 v[136:139], v[66:69], v[144:147], v[136:139]
	v_add_u32_e32 v144, v177, v209
	v_cvt_pk_fp8_f32 v158, v148, v150
	ds_read_b128 v[144:147], v144
	s_waitcnt lgkmcnt(1)
	v_mfma_f32_16x16x32_bf16 v[132:135], v[66:69], v[140:143], v[132:135]
	v_med3_f32 v140, v154, s78, v240
	v_med3_f32 v141, v155, s78, v240
	v_cvt_pk_fp8_f32 v158, v140, v141 op_sel:[0,0,1]
	v_lshlrev_b32_e32 v141, 16, v68
	v_and_b32_e32 v143, 0xffff0000, v68
	s_waitcnt lgkmcnt(0)
	v_mfma_f32_16x16x32_bf16 v[136:139], v[66:69], v[144:147], v[136:139]
	v_med3_f32 v142, v141, s78, v240
	v_med3_f32 v144, v143, s78, v240
	v_mov_b32_e32 v159, 0
	v_cvt_pk_fp8_f32 v159, v142, v144
	v_lshlrev_b32_e32 v145, 16, v69
	v_and_b32_e32 v147, 0xffff0000, v69
	v_med3_f32 v142, v145, s78, v240
	v_med3_f32 v144, v147, s78, v240
	s_waitcnt vmcnt(16)
	v_lshlrev_b32_e32 v160, 16, v63
	v_and_b32_e32 v161, 0xffff0000, v63
	v_cvt_pk_fp8_f32 v159, v142, v144 op_sel:[0,0,1]
	v_and_b32_e32 v142, 0xffff0000, v62
	v_mul_f32_e32 v152, v160, v160
	v_mul_f32_e32 v156, v161, v161
	v_lshlrev_b32_e32 v140, 16, v62
	v_pk_mul_f32 v[154:155], v[142:143], v[142:143]
	v_and_b32_e32 v146, 0xffff0000, v64
	v_pk_fma_f32 v[154:155], v[140:141], v[140:141], v[154:155]
	v_pk_add_f32 v[152:153], v[152:153], v[156:157]
	v_lshlrev_b32_e32 v144, 16, v64
	v_pk_add_f32 v[152:153], v[154:155], v[152:153]
	v_pk_mul_f32 v[154:155], v[146:147], v[146:147]
	v_med3_f32 v140, v140, s78, v240
	v_pk_fma_f32 v[154:155], v[144:145], v[144:145], v[154:155]
	v_med3_f32 v141, v142, s78, v240
	v_pk_add_f32 v[152:153], v[154:155], v[152:153]
	v_mov_b32_e32 v154, 0
	v_cvt_pk_fp8_f32 v154, v140, v141
	v_med3_f32 v140, v160, s78, v240
	v_med3_f32 v141, v161, s78, v240
	v_med3_f32 v145, v146, s78, v240
	v_add_u32_e32 v146, v175, v210
	v_cvt_pk_fp8_f32 v154, v140, v141 op_sel:[0,0,1]
	v_med3_f32 v144, v144, s78, v240
	ds_read_b128 v[140:143], v146
	v_mov_b32_e32 v155, 0
	v_cvt_pk_fp8_f32 v155, v144, v145
	ds_read_b128 v[144:147], v146 offset:32768
	s_waitcnt lgkmcnt(1)
	v_mfma_f32_16x16x32_bf16 v[132:135], v[62:65], v[140:143], v[132:135]
	v_add_u32_e32 v140, v176, v210
	v_lshlrev_b32_e32 v173, 16, v65
	v_and_b32_e32 v243, 0xffff0000, v65
	ds_read_b128 v[140:143], v140
	s_waitcnt lgkmcnt(1)
	v_mfma_f32_16x16x32_bf16 v[136:139], v[62:65], v[144:147], v[136:139]
	v_add_u32_e32 v144, v177, v210
	v_mul_f32_e32 v150, v173, v173
	v_mul_f32_e32 v148, v243, v243
	ds_read_b128 v[144:147], v144
	v_pk_add_f32 v[148:149], v[150:151], v[148:149]
	v_med3_f32 v150, v173, s78, v240
	v_med3_f32 v151, v243, s78, v240
	v_cvt_pk_fp8_f32 v155, v150, v151 op_sel:[0,0,1]
	s_waitcnt lgkmcnt(1)
	v_mfma_f32_16x16x32_bf16 v[132:135], v[62:65], v[140:143], v[132:135]
	v_add_f32_e64 v140, v152, v148
	v_add_f32_e64 v141, v153, v149
	s_waitcnt vmcnt(15)
	v_and_b32_e32 v143, 0xffff0000, v59
	v_and_b32_e32 v142, 0xffff0000, v58
	v_pk_add_f32 v[148:149], v[140:141], v[140:141] op_sel_hi:[0,1]
	s_waitcnt lgkmcnt(0)
	v_mfma_f32_16x16x32_bf16 v[136:139], v[62:65], v[144:147], v[136:139]
	v_lshlrev_b32_e32 v141, 16, v59
	v_lshlrev_b32_e32 v140, 16, v58
	v_pk_mul_f32 v[144:145], v[142:143], v[142:143]
	global_store_dwordx2 v[130:131], v[154:155], off offset:512
	v_pk_fma_f32 v[144:145], v[140:141], v[140:141], v[144:145]
	v_med3_f32 v140, v140, s78, v240
	v_med3_f32 v142, v142, s78, v240
	v_mov_b32_e32 v154, 0
	v_cvt_pk_fp8_f32 v154, v140, v142
	v_and_b32_e32 v151, 0xffff0000, v61
	v_and_b32_e32 v150, 0xffff0000, v60
	v_lshlrev_b32_e32 v147, 16, v61
	v_lshlrev_b32_e32 v146, 16, v60
	v_pk_mul_f32 v[152:153], v[150:151], v[150:151]
	v_add_f32_e32 v148, v144, v145
	v_pk_fma_f32 v[152:153], v[146:147], v[146:147], v[152:153]
	v_med3_f32 v140, v141, s78, v240
	v_med3_f32 v141, v143, s78, v240
	v_med3_f32 v144, v146, s78, v240
	v_med3_f32 v145, v150, s78, v240
	v_add_u32_e32 v146, v175, v211
	v_mov_b32_e32 v155, 0
	v_cvt_pk_fp8_f32 v154, v140, v141 op_sel:[0,0,1]
	ds_read_b128 v[140:143], v146
	v_cvt_pk_fp8_f32 v155, v144, v145
	v_med3_f32 v150, v147, s78, v240
	ds_read_b128 v[144:147], v146 offset:32768
	s_waitcnt lgkmcnt(1)
	v_mfma_f32_16x16x32_bf16 v[132:135], v[58:61], v[140:143], v[132:135]
	v_add_u32_e32 v140, v176, v211
	ds_read_b128 v[140:143], v140
	v_med3_f32 v151, v151, s78, v240
	s_waitcnt lgkmcnt(1)
	v_mfma_f32_16x16x32_bf16 v[136:139], v[58:61], v[144:147], v[136:139]
	v_add_u32_e32 v144, v177, v211
	ds_read_b128 v[144:147], v144
	v_cvt_pk_fp8_f32 v155, v150, v151 op_sel:[0,0,1]
	s_waitcnt lgkmcnt(1)
	v_mfma_f32_16x16x32_bf16 v[132:135], v[58:61], v[140:143], v[132:135]
	v_add_f32_e32 v140, v152, v148
	v_pk_add_f32 v[150:151], v[152:153], v[140:141] op_sel_hi:[1,0]
	global_store_dwordx2 v[130:131], v[154:155], off offset:544
	s_waitcnt lgkmcnt(0)
	v_mfma_f32_16x16x32_bf16 v[136:139], v[58:61], v[144:147], v[136:139]
	v_lshlrev_b32_e32 v144, 16, v54
	v_and_b32_e32 v145, 0xffff0000, v54
	v_mul_f32_e32 v140, v144, v144
	v_add_u32_e32 v147, v175, v212
	v_pk_fma_f32 v[152:153], v[144:145], v[144:145], v[140:141] op_sel_hi:[1,1,0]
	v_lshlrev_b32_e32 v154, 16, v55
	ds_read_b128 v[140:143], v147
	v_and_b32_e32 v155, 0xffff0000, v55
	v_mul_f32_e32 v146, v154, v154
	v_pk_fma_f32 v[156:157], v[154:155], v[154:155], v[146:147] op_sel_hi:[1,1,0]
	v_med3_f32 v148, v144, s78, v240
	v_med3_f32 v150, v145, s78, v240
	ds_read_b128 v[144:147], v147 offset:32768
	s_waitcnt lgkmcnt(1)
	v_mfma_f32_16x16x32_bf16 v[132:135], v[54:57], v[140:143], v[132:135]
	v_add_u32_e32 v140, v176, v212
	ds_read_b128 v[140:143], v140
	global_store_dwordx2 v[130:131], v[158:159], off offset:480
	v_mov_b32_e32 v158, 0
	s_waitcnt lgkmcnt(1)
	v_mfma_f32_16x16x32_bf16 v[136:139], v[54:57], v[144:147], v[136:139]
	v_add_u32_e32 v144, v177, v212
	v_cvt_pk_fp8_f32 v158, v148, v150
	ds_read_b128 v[144:147], v144
	s_waitcnt lgkmcnt(1)
	v_mfma_f32_16x16x32_bf16 v[132:135], v[54:57], v[140:143], v[132:135]
	v_med3_f32 v140, v154, s78, v240
	v_med3_f32 v141, v155, s78, v240
	v_cvt_pk_fp8_f32 v158, v140, v141 op_sel:[0,0,1]
	v_lshlrev_b32_e32 v141, 16, v56
	v_and_b32_e32 v143, 0xffff0000, v56
	s_waitcnt lgkmcnt(0)
	v_mfma_f32_16x16x32_bf16 v[136:139], v[54:57], v[144:147], v[136:139]
	v_med3_f32 v142, v141, s78, v240
	v_med3_f32 v144, v143, s78, v240
	v_mov_b32_e32 v159, 0
	v_cvt_pk_fp8_f32 v159, v142, v144
	v_lshlrev_b32_e32 v145, 16, v57
	v_and_b32_e32 v147, 0xffff0000, v57
	v_med3_f32 v142, v145, s78, v240
	v_med3_f32 v144, v147, s78, v240
	v_lshlrev_b32_e32 v160, 16, v51
	v_and_b32_e32 v161, 0xffff0000, v51
	v_cvt_pk_fp8_f32 v159, v142, v144 op_sel:[0,0,1]
	v_and_b32_e32 v142, 0xffff0000, v50
	v_mul_f32_e32 v152, v160, v160
	v_mul_f32_e32 v156, v161, v161
	v_lshlrev_b32_e32 v140, 16, v50
	v_pk_mul_f32 v[154:155], v[142:143], v[142:143]
	v_and_b32_e32 v146, 0xffff0000, v52
	v_pk_fma_f32 v[154:155], v[140:141], v[140:141], v[154:155]
	v_pk_add_f32 v[152:153], v[152:153], v[156:157]
	v_lshlrev_b32_e32 v144, 16, v52
	v_pk_add_f32 v[152:153], v[154:155], v[152:153]
	v_pk_mul_f32 v[154:155], v[146:147], v[146:147]
	v_med3_f32 v140, v140, s78, v240
	v_pk_fma_f32 v[154:155], v[144:145], v[144:145], v[154:155]
	v_med3_f32 v141, v142, s78, v240
	v_pk_add_f32 v[152:153], v[154:155], v[152:153]
	v_mov_b32_e32 v154, 0
	v_cvt_pk_fp8_f32 v154, v140, v141
	v_med3_f32 v140, v160, s78, v240
	v_med3_f32 v141, v161, s78, v240
	v_med3_f32 v145, v146, s78, v240
	v_add_u32_e32 v146, v175, v213
	v_cvt_pk_fp8_f32 v154, v140, v141 op_sel:[0,0,1]
	v_med3_f32 v144, v144, s78, v240
	ds_read_b128 v[140:143], v146
	v_mov_b32_e32 v155, 0
	v_cvt_pk_fp8_f32 v155, v144, v145
	ds_read_b128 v[144:147], v146 offset:32768
	s_waitcnt lgkmcnt(1)
	v_mfma_f32_16x16x32_bf16 v[132:135], v[50:53], v[140:143], v[132:135]
	v_add_u32_e32 v140, v176, v213
	v_lshlrev_b32_e32 v173, 16, v53
	v_and_b32_e32 v243, 0xffff0000, v53
	ds_read_b128 v[140:143], v140
	s_waitcnt lgkmcnt(1)
	v_mfma_f32_16x16x32_bf16 v[136:139], v[50:53], v[144:147], v[136:139]
	v_add_u32_e32 v144, v177, v213
	v_mul_f32_e32 v150, v173, v173
	v_mul_f32_e32 v148, v243, v243
	ds_read_b128 v[144:147], v144
	v_pk_add_f32 v[148:149], v[150:151], v[148:149]
	v_med3_f32 v150, v173, s78, v240
	v_med3_f32 v151, v243, s78, v240
	v_cvt_pk_fp8_f32 v155, v150, v151 op_sel:[0,0,1]
	s_waitcnt lgkmcnt(1)
	v_mfma_f32_16x16x32_bf16 v[132:135], v[50:53], v[140:143], v[132:135]
	v_add_f32_e64 v140, v152, v148
	v_add_f32_e64 v141, v153, v149
	v_and_b32_e32 v143, 0xffff0000, v47
	v_and_b32_e32 v142, 0xffff0000, v46
	v_pk_add_f32 v[148:149], v[140:141], v[140:141] op_sel_hi:[0,1]
	s_waitcnt lgkmcnt(0)
	v_mfma_f32_16x16x32_bf16 v[136:139], v[50:53], v[144:147], v[136:139]
	v_lshlrev_b32_e32 v141, 16, v47
	v_lshlrev_b32_e32 v140, 16, v46
	v_pk_mul_f32 v[144:145], v[142:143], v[142:143]
	global_store_dwordx2 v[130:131], v[154:155], off offset:608
	v_pk_fma_f32 v[144:145], v[140:141], v[140:141], v[144:145]
	v_med3_f32 v140, v140, s78, v240
	v_med3_f32 v142, v142, s78, v240
	v_mov_b32_e32 v154, 0
	v_cvt_pk_fp8_f32 v154, v140, v142
	v_and_b32_e32 v151, 0xffff0000, v49
	v_and_b32_e32 v150, 0xffff0000, v48
	v_lshlrev_b32_e32 v147, 16, v49
	v_lshlrev_b32_e32 v146, 16, v48
	v_pk_mul_f32 v[152:153], v[150:151], v[150:151]
	v_add_f32_e32 v148, v144, v145
	v_pk_fma_f32 v[152:153], v[146:147], v[146:147], v[152:153]
	v_med3_f32 v140, v141, s78, v240
	v_med3_f32 v141, v143, s78, v240
	v_med3_f32 v144, v146, s78, v240
	v_med3_f32 v145, v150, s78, v240
	v_add_u32_e32 v146, v175, v214
	v_mov_b32_e32 v155, 0
	v_cvt_pk_fp8_f32 v154, v140, v141 op_sel:[0,0,1]
	ds_read_b128 v[140:143], v146
	v_cvt_pk_fp8_f32 v155, v144, v145
	v_med3_f32 v150, v147, s78, v240
	ds_read_b128 v[144:147], v146 offset:32768
	s_waitcnt lgkmcnt(1)
	v_mfma_f32_16x16x32_bf16 v[132:135], v[46:49], v[140:143], v[132:135]
	v_add_u32_e32 v140, v176, v214
	ds_read_b128 v[140:143], v140
	v_med3_f32 v151, v151, s78, v240
	s_waitcnt lgkmcnt(1)
	v_mfma_f32_16x16x32_bf16 v[136:139], v[46:49], v[144:147], v[136:139]
	v_add_u32_e32 v144, v177, v214
	ds_read_b128 v[144:147], v144
	v_cvt_pk_fp8_f32 v155, v150, v151 op_sel:[0,0,1]
	s_waitcnt lgkmcnt(1)
	v_mfma_f32_16x16x32_bf16 v[132:135], v[46:49], v[140:143], v[132:135]
	v_add_f32_e32 v140, v152, v148
	v_pk_add_f32 v[150:151], v[152:153], v[140:141] op_sel_hi:[1,0]
	global_store_dwordx2 v[130:131], v[154:155], off offset:640
	s_waitcnt lgkmcnt(0)
	v_mfma_f32_16x16x32_bf16 v[136:139], v[46:49], v[144:147], v[136:139]
	v_lshlrev_b32_e32 v144, 16, v42
	v_and_b32_e32 v145, 0xffff0000, v42
	v_mul_f32_e32 v140, v144, v144
	v_add_u32_e32 v147, v175, v215
	v_pk_fma_f32 v[152:153], v[144:145], v[144:145], v[140:141] op_sel_hi:[1,1,0]
	v_lshlrev_b32_e32 v154, 16, v43
	ds_read_b128 v[140:143], v147
	v_and_b32_e32 v155, 0xffff0000, v43
	v_mul_f32_e32 v146, v154, v154
	v_pk_fma_f32 v[156:157], v[154:155], v[154:155], v[146:147] op_sel_hi:[1,1,0]
	v_med3_f32 v148, v144, s78, v240
	v_med3_f32 v150, v145, s78, v240
	ds_read_b128 v[144:147], v147 offset:32768
	s_waitcnt lgkmcnt(1)
	v_mfma_f32_16x16x32_bf16 v[132:135], v[42:45], v[140:143], v[132:135]
	v_add_u32_e32 v140, v176, v215
	ds_read_b128 v[140:143], v140
	global_store_dwordx2 v[130:131], v[158:159], off offset:576
	v_mov_b32_e32 v158, 0
	s_waitcnt lgkmcnt(1)
	v_mfma_f32_16x16x32_bf16 v[136:139], v[42:45], v[144:147], v[136:139]
	v_add_u32_e32 v144, v177, v215
	v_cvt_pk_fp8_f32 v158, v148, v150
	ds_read_b128 v[144:147], v144
	s_waitcnt lgkmcnt(1)
	v_mfma_f32_16x16x32_bf16 v[132:135], v[42:45], v[140:143], v[132:135]
	v_med3_f32 v140, v154, s78, v240
	v_med3_f32 v141, v155, s78, v240
	v_cvt_pk_fp8_f32 v158, v140, v141 op_sel:[0,0,1]
	v_lshlrev_b32_e32 v141, 16, v44
	v_and_b32_e32 v143, 0xffff0000, v44
	s_waitcnt lgkmcnt(0)
	v_mfma_f32_16x16x32_bf16 v[136:139], v[42:45], v[144:147], v[136:139]
	v_med3_f32 v142, v141, s78, v240
	v_med3_f32 v144, v143, s78, v240
	v_mov_b32_e32 v159, 0
	v_cvt_pk_fp8_f32 v159, v142, v144
	v_lshlrev_b32_e32 v145, 16, v45
	v_and_b32_e32 v147, 0xffff0000, v45
	v_med3_f32 v142, v145, s78, v240
	v_med3_f32 v144, v147, s78, v240
	v_lshlrev_b32_e32 v160, 16, v39
	v_and_b32_e32 v161, 0xffff0000, v39
	v_cvt_pk_fp8_f32 v159, v142, v144 op_sel:[0,0,1]
	v_and_b32_e32 v142, 0xffff0000, v38
	v_mul_f32_e32 v152, v160, v160
	v_mul_f32_e32 v156, v161, v161
	v_lshlrev_b32_e32 v140, 16, v38
	v_pk_mul_f32 v[154:155], v[142:143], v[142:143]
	v_and_b32_e32 v146, 0xffff0000, v40
	v_pk_fma_f32 v[154:155], v[140:141], v[140:141], v[154:155]
	v_pk_add_f32 v[152:153], v[152:153], v[156:157]
	v_lshlrev_b32_e32 v144, 16, v40
	v_pk_add_f32 v[152:153], v[154:155], v[152:153]
	v_pk_mul_f32 v[154:155], v[146:147], v[146:147]
	v_med3_f32 v140, v140, s78, v240
	v_pk_fma_f32 v[154:155], v[144:145], v[144:145], v[154:155]
	v_med3_f32 v141, v142, s78, v240
	v_pk_add_f32 v[152:153], v[154:155], v[152:153]
	v_mov_b32_e32 v154, 0
	v_cvt_pk_fp8_f32 v154, v140, v141
	v_med3_f32 v140, v160, s78, v240
	v_med3_f32 v141, v161, s78, v240
	v_med3_f32 v145, v146, s78, v240
	v_add_u32_e32 v146, v175, v216
	v_cvt_pk_fp8_f32 v154, v140, v141 op_sel:[0,0,1]
	v_med3_f32 v144, v144, s78, v240
	ds_read_b128 v[140:143], v146
	v_mov_b32_e32 v155, 0
	v_cvt_pk_fp8_f32 v155, v144, v145
	ds_read_b128 v[144:147], v146 offset:32768
	s_waitcnt lgkmcnt(1)
	v_mfma_f32_16x16x32_bf16 v[132:135], v[38:41], v[140:143], v[132:135]
	v_add_u32_e32 v140, v176, v216
	v_lshlrev_b32_e32 v173, 16, v41
	v_and_b32_e32 v243, 0xffff0000, v41
	ds_read_b128 v[140:143], v140
	s_waitcnt lgkmcnt(1)
	v_mfma_f32_16x16x32_bf16 v[136:139], v[38:41], v[144:147], v[136:139]
	v_add_u32_e32 v144, v177, v216
	v_mul_f32_e32 v150, v173, v173
	v_mul_f32_e32 v148, v243, v243
	ds_read_b128 v[144:147], v144
	v_pk_add_f32 v[148:149], v[150:151], v[148:149]
	v_med3_f32 v150, v173, s78, v240
	v_med3_f32 v151, v243, s78, v240
	v_cvt_pk_fp8_f32 v155, v150, v151 op_sel:[0,0,1]
	s_waitcnt lgkmcnt(1)
	v_mfma_f32_16x16x32_bf16 v[132:135], v[38:41], v[140:143], v[132:135]
	v_add_f32_e64 v140, v152, v148
	v_add_f32_e64 v141, v153, v149
	v_and_b32_e32 v143, 0xffff0000, v35
	v_and_b32_e32 v142, 0xffff0000, v34
	v_pk_add_f32 v[148:149], v[140:141], v[140:141] op_sel_hi:[0,1]
	s_waitcnt lgkmcnt(0)
	v_mfma_f32_16x16x32_bf16 v[136:139], v[38:41], v[144:147], v[136:139]
	v_lshlrev_b32_e32 v141, 16, v35
	v_lshlrev_b32_e32 v140, 16, v34
	v_pk_mul_f32 v[144:145], v[142:143], v[142:143]
	global_store_dwordx2 v[130:131], v[154:155], off offset:704
	v_pk_fma_f32 v[144:145], v[140:141], v[140:141], v[144:145]
	v_med3_f32 v140, v140, s78, v240
	v_med3_f32 v142, v142, s78, v240
	v_mov_b32_e32 v154, 0
	v_cvt_pk_fp8_f32 v154, v140, v142
	v_and_b32_e32 v151, 0xffff0000, v37
	v_and_b32_e32 v150, 0xffff0000, v36
	v_lshlrev_b32_e32 v147, 16, v37
	v_lshlrev_b32_e32 v146, 16, v36
	v_pk_mul_f32 v[152:153], v[150:151], v[150:151]
	v_add_f32_e32 v148, v144, v145
	v_pk_fma_f32 v[152:153], v[146:147], v[146:147], v[152:153]
	v_med3_f32 v140, v141, s78, v240
	v_med3_f32 v141, v143, s78, v240
	v_med3_f32 v144, v146, s78, v240
	v_med3_f32 v145, v150, s78, v240
	v_add_u32_e32 v146, v175, v217
	v_mov_b32_e32 v155, 0
	v_cvt_pk_fp8_f32 v154, v140, v141 op_sel:[0,0,1]
	ds_read_b128 v[140:143], v146
	v_cvt_pk_fp8_f32 v155, v144, v145
	v_med3_f32 v150, v147, s78, v240
	ds_read_b128 v[144:147], v146 offset:32768
	s_waitcnt lgkmcnt(1)
	v_mfma_f32_16x16x32_bf16 v[132:135], v[34:37], v[140:143], v[132:135]
	v_add_u32_e32 v140, v176, v217
	ds_read_b128 v[140:143], v140
	v_med3_f32 v151, v151, s78, v240
	s_waitcnt lgkmcnt(1)
	v_mfma_f32_16x16x32_bf16 v[136:139], v[34:37], v[144:147], v[136:139]
	v_add_u32_e32 v144, v177, v217
	ds_read_b128 v[144:147], v144
	v_cvt_pk_fp8_f32 v155, v150, v151 op_sel:[0,0,1]
	s_waitcnt lgkmcnt(1)
	v_mfma_f32_16x16x32_bf16 v[132:135], v[34:37], v[140:143], v[132:135]
	v_add_f32_e32 v140, v152, v148
	v_pk_add_f32 v[150:151], v[152:153], v[140:141] op_sel_hi:[1,0]
	global_store_dwordx2 v[130:131], v[154:155], off offset:736
	s_waitcnt lgkmcnt(0)
	v_mfma_f32_16x16x32_bf16 v[136:139], v[34:37], v[144:147], v[136:139]
	v_lshlrev_b32_e32 v144, 16, v30
	v_and_b32_e32 v145, 0xffff0000, v30
	v_mul_f32_e32 v140, v144, v144
	v_add_u32_e32 v147, v175, v219
	v_pk_fma_f32 v[152:153], v[144:145], v[144:145], v[140:141] op_sel_hi:[1,1,0]
	v_lshlrev_b32_e32 v154, 16, v31
	ds_read_b128 v[140:143], v147
	v_and_b32_e32 v155, 0xffff0000, v31
	v_mul_f32_e32 v146, v154, v154
	v_pk_fma_f32 v[156:157], v[154:155], v[154:155], v[146:147] op_sel_hi:[1,1,0]
	v_med3_f32 v148, v144, s78, v240
	v_med3_f32 v150, v145, s78, v240
	ds_read_b128 v[144:147], v147 offset:32768
	s_waitcnt lgkmcnt(1)
	v_mfma_f32_16x16x32_bf16 v[132:135], v[30:33], v[140:143], v[132:135]
	v_add_u32_e32 v140, v176, v219
	ds_read_b128 v[140:143], v140
	global_store_dwordx2 v[130:131], v[158:159], off offset:672
	v_mov_b32_e32 v158, 0
	s_waitcnt lgkmcnt(1)
	v_mfma_f32_16x16x32_bf16 v[136:139], v[30:33], v[144:147], v[136:139]
	v_add_u32_e32 v144, v177, v219
	v_cvt_pk_fp8_f32 v158, v148, v150
	ds_read_b128 v[144:147], v144
	s_waitcnt lgkmcnt(1)
	v_mfma_f32_16x16x32_bf16 v[132:135], v[30:33], v[140:143], v[132:135]
	v_med3_f32 v140, v154, s78, v240
	v_med3_f32 v141, v155, s78, v240
	v_cvt_pk_fp8_f32 v158, v140, v141 op_sel:[0,0,1]
	v_lshlrev_b32_e32 v141, 16, v32
	v_and_b32_e32 v143, 0xffff0000, v32
	s_waitcnt lgkmcnt(0)
	v_mfma_f32_16x16x32_bf16 v[136:139], v[30:33], v[144:147], v[136:139]
	v_med3_f32 v142, v141, s78, v240
	v_med3_f32 v144, v143, s78, v240
	v_mov_b32_e32 v159, 0
	v_cvt_pk_fp8_f32 v159, v142, v144
	v_lshlrev_b32_e32 v145, 16, v33
	v_and_b32_e32 v147, 0xffff0000, v33
	v_med3_f32 v142, v145, s78, v240
	v_med3_f32 v144, v147, s78, v240
	v_lshlrev_b32_e32 v160, 16, v27
	v_and_b32_e32 v161, 0xffff0000, v27
	v_cvt_pk_fp8_f32 v159, v142, v144 op_sel:[0,0,1]
	v_and_b32_e32 v142, 0xffff0000, v26
	v_mul_f32_e32 v152, v160, v160
	v_mul_f32_e32 v156, v161, v161
	v_lshlrev_b32_e32 v140, 16, v26
	v_pk_mul_f32 v[154:155], v[142:143], v[142:143]
	v_and_b32_e32 v146, 0xffff0000, v28
	v_pk_fma_f32 v[154:155], v[140:141], v[140:141], v[154:155]
	v_pk_add_f32 v[152:153], v[152:153], v[156:157]
	v_lshlrev_b32_e32 v144, 16, v28
	v_pk_add_f32 v[152:153], v[154:155], v[152:153]
	v_pk_mul_f32 v[154:155], v[146:147], v[146:147]
	v_med3_f32 v140, v140, s78, v240
	v_pk_fma_f32 v[154:155], v[144:145], v[144:145], v[154:155]
	v_med3_f32 v141, v142, s78, v240
	v_pk_add_f32 v[152:153], v[154:155], v[152:153]
	v_mov_b32_e32 v154, 0
	v_cvt_pk_fp8_f32 v154, v140, v141
	v_med3_f32 v140, v160, s78, v240
	v_med3_f32 v141, v161, s78, v240
	v_med3_f32 v145, v146, s78, v240
	v_add_u32_e32 v146, v175, v220
	v_cvt_pk_fp8_f32 v154, v140, v141 op_sel:[0,0,1]
	v_med3_f32 v144, v144, s78, v240
	ds_read_b128 v[140:143], v146
	v_mov_b32_e32 v155, 0
	v_cvt_pk_fp8_f32 v155, v144, v145
	ds_read_b128 v[144:147], v146 offset:32768
	s_waitcnt lgkmcnt(1)
	v_mfma_f32_16x16x32_bf16 v[132:135], v[26:29], v[140:143], v[132:135]
	v_add_u32_e32 v140, v176, v220
	v_lshlrev_b32_e32 v173, 16, v29
	v_and_b32_e32 v243, 0xffff0000, v29
	ds_read_b128 v[140:143], v140
	s_waitcnt lgkmcnt(1)
	v_mfma_f32_16x16x32_bf16 v[136:139], v[26:29], v[144:147], v[136:139]
	v_add_u32_e32 v144, v177, v220
	v_mul_f32_e32 v150, v173, v173
	v_mul_f32_e32 v148, v243, v243
	ds_read_b128 v[144:147], v144
	v_pk_add_f32 v[148:149], v[150:151], v[148:149]
	v_med3_f32 v150, v173, s78, v240
	v_med3_f32 v151, v243, s78, v240
	v_cvt_pk_fp8_f32 v155, v150, v151 op_sel:[0,0,1]
	s_waitcnt lgkmcnt(1)
	v_mfma_f32_16x16x32_bf16 v[132:135], v[26:29], v[140:143], v[132:135]
	v_add_f32_e64 v140, v152, v148
	v_add_f32_e64 v141, v153, v149
	v_and_b32_e32 v143, 0xffff0000, v23
	v_and_b32_e32 v142, 0xffff0000, v22
	v_pk_add_f32 v[148:149], v[140:141], v[140:141] op_sel_hi:[0,1]
	s_waitcnt lgkmcnt(0)
	v_mfma_f32_16x16x32_bf16 v[136:139], v[26:29], v[144:147], v[136:139]
	v_lshlrev_b32_e32 v141, 16, v23
	v_lshlrev_b32_e32 v140, 16, v22
	v_pk_mul_f32 v[144:145], v[142:143], v[142:143]
	global_store_dwordx2 v[130:131], v[154:155], off offset:800
	v_pk_fma_f32 v[144:145], v[140:141], v[140:141], v[144:145]
	v_med3_f32 v140, v140, s78, v240
	v_med3_f32 v142, v142, s78, v240
	v_mov_b32_e32 v154, 0
	v_cvt_pk_fp8_f32 v154, v140, v142
	v_and_b32_e32 v151, 0xffff0000, v25
	v_and_b32_e32 v150, 0xffff0000, v24
	v_lshlrev_b32_e32 v147, 16, v25
	v_lshlrev_b32_e32 v146, 16, v24
	v_pk_mul_f32 v[152:153], v[150:151], v[150:151]
	v_add_f32_e32 v148, v144, v145
	v_pk_fma_f32 v[152:153], v[146:147], v[146:147], v[152:153]
	v_med3_f32 v140, v141, s78, v240
	v_med3_f32 v141, v143, s78, v240
	v_med3_f32 v144, v146, s78, v240
	v_med3_f32 v145, v150, s78, v240
	v_add_u32_e32 v146, v175, v221
	v_mov_b32_e32 v155, 0
	v_cvt_pk_fp8_f32 v154, v140, v141 op_sel:[0,0,1]
	ds_read_b128 v[140:143], v146
	v_cvt_pk_fp8_f32 v155, v144, v145
	v_med3_f32 v150, v147, s78, v240
	ds_read_b128 v[144:147], v146 offset:32768
	s_waitcnt lgkmcnt(1)
	v_mfma_f32_16x16x32_bf16 v[132:135], v[22:25], v[140:143], v[132:135]
	v_add_u32_e32 v140, v176, v221
	ds_read_b128 v[140:143], v140
	v_med3_f32 v151, v151, s78, v240
	s_waitcnt lgkmcnt(1)
	v_mfma_f32_16x16x32_bf16 v[136:139], v[22:25], v[144:147], v[136:139]
	v_add_u32_e32 v144, v177, v221
	ds_read_b128 v[144:147], v144
	v_cvt_pk_fp8_f32 v155, v150, v151 op_sel:[0,0,1]
	s_waitcnt lgkmcnt(1)
	v_mfma_f32_16x16x32_bf16 v[132:135], v[22:25], v[140:143], v[132:135]
	v_add_f32_e32 v140, v152, v148
	v_pk_add_f32 v[150:151], v[152:153], v[140:141] op_sel_hi:[1,0]
	global_store_dwordx2 v[130:131], v[154:155], off offset:832
	s_waitcnt lgkmcnt(0)
	v_mfma_f32_16x16x32_bf16 v[136:139], v[22:25], v[144:147], v[136:139]
	v_lshlrev_b32_e32 v144, 16, v18
	v_and_b32_e32 v145, 0xffff0000, v18
	v_mul_f32_e32 v140, v144, v144
	v_add_u32_e32 v147, v175, v222
	v_pk_fma_f32 v[152:153], v[144:145], v[144:145], v[140:141] op_sel_hi:[1,1,0]
	v_lshlrev_b32_e32 v154, 16, v19
	ds_read_b128 v[140:143], v147
	v_and_b32_e32 v155, 0xffff0000, v19
	v_mul_f32_e32 v146, v154, v154
	v_pk_fma_f32 v[156:157], v[154:155], v[154:155], v[146:147] op_sel_hi:[1,1,0]
	v_med3_f32 v148, v144, s78, v240
	v_med3_f32 v150, v145, s78, v240
	ds_read_b128 v[144:147], v147 offset:32768
	s_waitcnt lgkmcnt(1)
	v_mfma_f32_16x16x32_bf16 v[132:135], v[18:21], v[140:143], v[132:135]
	v_add_u32_e32 v140, v176, v222
	ds_read_b128 v[140:143], v140
	global_store_dwordx2 v[130:131], v[158:159], off offset:768
	v_mov_b32_e32 v158, 0
	s_waitcnt lgkmcnt(1)
	v_mfma_f32_16x16x32_bf16 v[136:139], v[18:21], v[144:147], v[136:139]
	v_add_u32_e32 v144, v177, v222
	v_cvt_pk_fp8_f32 v158, v148, v150
	ds_read_b128 v[144:147], v144
	s_waitcnt lgkmcnt(1)
	v_mfma_f32_16x16x32_bf16 v[132:135], v[18:21], v[140:143], v[132:135]
	v_med3_f32 v140, v154, s78, v240
	v_med3_f32 v141, v155, s78, v240
	v_cvt_pk_fp8_f32 v158, v140, v141 op_sel:[0,0,1]
	v_lshlrev_b32_e32 v141, 16, v20
	v_and_b32_e32 v143, 0xffff0000, v20
	s_waitcnt lgkmcnt(0)
	v_mfma_f32_16x16x32_bf16 v[136:139], v[18:21], v[144:147], v[136:139]
	v_med3_f32 v142, v141, s78, v240
	v_med3_f32 v144, v143, s78, v240
	v_mov_b32_e32 v159, 0
	v_cvt_pk_fp8_f32 v159, v142, v144
	v_lshlrev_b32_e32 v145, 16, v21
	v_and_b32_e32 v147, 0xffff0000, v21
	v_med3_f32 v142, v145, s78, v240
	v_med3_f32 v144, v147, s78, v240
	v_lshlrev_b32_e32 v160, 16, v15
	v_and_b32_e32 v161, 0xffff0000, v15
	v_cvt_pk_fp8_f32 v159, v142, v144 op_sel:[0,0,1]
	v_and_b32_e32 v142, 0xffff0000, v14
	v_mul_f32_e32 v152, v160, v160
	v_mul_f32_e32 v156, v161, v161
	v_lshlrev_b32_e32 v140, 16, v14
	v_pk_mul_f32 v[154:155], v[142:143], v[142:143]
	v_and_b32_e32 v146, 0xffff0000, v16
	v_pk_fma_f32 v[154:155], v[140:141], v[140:141], v[154:155]
	v_pk_add_f32 v[152:153], v[152:153], v[156:157]
	v_lshlrev_b32_e32 v144, 16, v16
	v_pk_add_f32 v[152:153], v[154:155], v[152:153]
	v_pk_mul_f32 v[154:155], v[146:147], v[146:147]
	v_med3_f32 v140, v140, s78, v240
	v_pk_fma_f32 v[154:155], v[144:145], v[144:145], v[154:155]
	v_med3_f32 v141, v142, s78, v240
	v_pk_add_f32 v[152:153], v[154:155], v[152:153]
	v_mov_b32_e32 v154, 0
	v_cvt_pk_fp8_f32 v154, v140, v141
	v_med3_f32 v140, v160, s78, v240
	v_med3_f32 v141, v161, s78, v240
	v_med3_f32 v145, v146, s78, v240
	v_add_u32_e32 v146, v175, v223
	v_cvt_pk_fp8_f32 v154, v140, v141 op_sel:[0,0,1]
	v_med3_f32 v144, v144, s78, v240
	ds_read_b128 v[140:143], v146
	v_mov_b32_e32 v155, 0
	v_cvt_pk_fp8_f32 v155, v144, v145
	ds_read_b128 v[144:147], v146 offset:32768
	s_waitcnt lgkmcnt(1)
	v_mfma_f32_16x16x32_bf16 v[132:135], v[14:17], v[140:143], v[132:135]
	v_add_u32_e32 v140, v176, v223
	v_lshlrev_b32_e32 v173, 16, v17
	v_and_b32_e32 v243, 0xffff0000, v17
	ds_read_b128 v[140:143], v140
	s_waitcnt lgkmcnt(1)
	v_mfma_f32_16x16x32_bf16 v[136:139], v[14:17], v[144:147], v[136:139]
	v_add_u32_e32 v144, v177, v223
	v_mul_f32_e32 v150, v173, v173
	v_mul_f32_e32 v148, v243, v243
	ds_read_b128 v[144:147], v144
	v_pk_add_f32 v[148:149], v[150:151], v[148:149]
	v_med3_f32 v150, v173, s78, v240
	v_med3_f32 v151, v243, s78, v240
	v_cvt_pk_fp8_f32 v155, v150, v151 op_sel:[0,0,1]
	s_waitcnt lgkmcnt(1)
	v_mfma_f32_16x16x32_bf16 v[132:135], v[14:17], v[140:143], v[132:135]
	v_add_f32_e64 v140, v152, v148
	v_add_f32_e64 v141, v153, v149
	v_and_b32_e32 v143, 0xffff0000, v11
	v_and_b32_e32 v142, 0xffff0000, v10
	v_pk_add_f32 v[148:149], v[140:141], v[140:141] op_sel_hi:[0,1]
	s_waitcnt lgkmcnt(0)
	v_mfma_f32_16x16x32_bf16 v[136:139], v[14:17], v[144:147], v[136:139]
	v_lshlrev_b32_e32 v141, 16, v11
	v_lshlrev_b32_e32 v140, 16, v10
	v_pk_mul_f32 v[144:145], v[142:143], v[142:143]
	global_store_dwordx2 v[130:131], v[154:155], off offset:896
	v_pk_fma_f32 v[144:145], v[140:141], v[140:141], v[144:145]
	v_med3_f32 v140, v140, s78, v240
	v_med3_f32 v142, v142, s78, v240
	v_mov_b32_e32 v154, 0
	v_cvt_pk_fp8_f32 v154, v140, v142
	v_and_b32_e32 v151, 0xffff0000, v13
	v_and_b32_e32 v150, 0xffff0000, v12
	v_lshlrev_b32_e32 v147, 16, v13
	v_lshlrev_b32_e32 v146, 16, v12
	v_pk_mul_f32 v[152:153], v[150:151], v[150:151]
	v_add_f32_e32 v148, v144, v145
	v_pk_fma_f32 v[152:153], v[146:147], v[146:147], v[152:153]
	v_med3_f32 v140, v141, s78, v240
	v_med3_f32 v141, v143, s78, v240
	v_med3_f32 v144, v146, s78, v240
	v_add_u32_e32 v146, v175, v224
	v_cvt_pk_fp8_f32 v154, v140, v141 op_sel:[0,0,1]
	ds_read_b128 v[140:143], v146
	v_med3_f32 v145, v150, s78, v240
	v_mov_b32_e32 v155, 0
	v_cvt_pk_fp8_f32 v155, v144, v145
	v_med3_f32 v150, v147, s78, v240
	ds_read_b128 v[144:147], v146 offset:32768
	s_waitcnt lgkmcnt(1)
	v_mfma_f32_16x16x32_bf16 v[132:135], v[10:13], v[140:143], v[132:135]
	v_add_u32_e32 v140, v176, v224
	ds_read_b128 v[140:143], v140
	v_med3_f32 v151, v151, s78, v240
	s_waitcnt lgkmcnt(1)
	v_mfma_f32_16x16x32_bf16 v[136:139], v[10:13], v[144:147], v[136:139]
	v_add_u32_e32 v144, v177, v224
	v_cvt_pk_fp8_f32 v155, v150, v151 op_sel:[0,0,1]
	ds_read_b128 v[144:147], v144
	s_waitcnt lgkmcnt(1)
	v_mfma_f32_16x16x32_bf16 v[132:135], v[10:13], v[140:143], v[132:135]
	v_add_f32_e32 v140, v152, v148
	v_pk_add_f32 v[150:151], v[152:153], v[140:141] op_sel_hi:[1,0]
	v_lshlrev_b32_e32 v140, 16, v6
	global_store_dwordx2 v[130:131], v[154:155], off offset:928
	v_and_b32_e32 v141, 0xffff0000, v6
	v_mul_f32_e32 v142, v140, v140
	v_lshlrev_b32_e32 v154, 16, v7
	s_waitcnt lgkmcnt(0)
	v_mfma_f32_16x16x32_bf16 v[136:139], v[10:13], v[144:147], v[136:139]
	v_fma_f32 v152, v140, v140, v142
	v_fma_f32 v153, v141, v141, v142
	v_and_b32_e32 v155, 0xffff0000, v7
	v_mul_f32_e32 v142, v154, v154
	v_add_u32_e32 v146, v175, v225
	v_pk_fma_f32 v[156:157], v[154:155], v[154:155], v[142:143] op_sel_hi:[1,1,0]
	v_med3_f32 v144, v140, s78, v240
	v_med3_f32 v145, v141, s78, v240
	ds_read_b128 v[140:143], v146
	global_store_dwordx2 v[130:131], v[158:159], off offset:864
	v_mov_b32_e32 v158, 0
	v_cvt_pk_fp8_f32 v158, v144, v145
	ds_read_b128 v[144:147], v146 offset:32768
	s_waitcnt lgkmcnt(1)
	v_mfma_f32_16x16x32_bf16 v[132:135], v[6:9], v[140:143], v[132:135]
	v_add_u32_e32 v140, v176, v225
	ds_read_b128 v[140:143], v140
	v_med3_f32 v148, v154, s78, v240
	s_waitcnt lgkmcnt(1)
	v_mfma_f32_16x16x32_bf16 v[136:139], v[6:9], v[144:147], v[136:139]
	v_add_u32_e32 v144, v177, v225
	ds_read_b128 v[144:147], v144
	v_med3_f32 v150, v155, s78, v240
	s_waitcnt lgkmcnt(1)
	v_mfma_f32_16x16x32_bf16 v[132:135], v[6:9], v[140:143], v[132:135]
	v_lshlrev_b32_e32 v141, 16, v8
	v_and_b32_e32 v143, 0xffff0000, v8
	v_med3_f32 v154, v141, s78, v240
	v_med3_f32 v155, v143, s78, v240
	v_mov_b32_e32 v159, 0
	v_cvt_pk_fp8_f32 v159, v154, v155
	v_lshlrev_b32_e32 v155, 16, v9
	v_and_b32_e32 v161, 0xffff0000, v9
	v_lshlrev_b32_e32 v140, 16, v2
	v_and_b32_e32 v142, 0xffff0000, v2
	v_med3_f32 v244, v155, s78, v240
	v_med3_f32 v245, v161, s78, v240
	v_lshlrev_b32_e32 v154, 16, v4
	v_and_b32_e32 v160, 0xffff0000, v4
	v_cvt_pk_fp8_f32 v159, v244, v245 op_sel:[0,0,1]
	v_med3_f32 v245, v140, s78, v240
	v_med3_f32 v246, v142, s78, v240
	v_mov_b32_e32 v244, 0
	v_cvt_pk_fp8_f32 v244, v245, v246
	v_med3_f32 v246, v154, s78, v240
	v_med3_f32 v247, v160, s78, v240
	v_mov_b32_e32 v245, 0
	v_cvt_pk_fp8_f32 v245, v246, v247
	v_cvt_pk_fp8_f32 v158, v148, v150 op_sel:[0,0,1]
	v_lshlrev_b32_e32 v148, 16, v3
	v_and_b32_e32 v150, 0xffff0000, v3
	v_lshlrev_b32_e32 v173, 16, v5
	v_and_b32_e32 v243, 0xffff0000, v5
	v_mul_f32_e32 v152, v148, v148
	v_mul_f32_e32 v156, v150, v150
	v_med3_f32 v148, v148, s78, v240
	v_med3_f32 v150, v150, s78, v240
	v_cvt_pk_fp8_f32 v244, v148, v150 op_sel:[0,0,1]
	v_med3_f32 v148, v173, s78, v240
	v_med3_f32 v150, v243, s78, v240
	v_cvt_pk_fp8_f32 v245, v148, v150 op_sel:[0,0,1]
	global_store_dwordx2 v[130:131], v[158:159], off offset:960
	global_store_dwordx2 v[130:131], v[244:245], off offset:992
	global_load_dword v158, v[168:169], off
	s_nop 0
	global_load_dword v159, v[168:169], off offset:64
	v_pk_mul_f32 v[130:131], v[142:143], v[142:143]
	v_mul_f32_e32 v150, v173, v173
	v_pk_fma_f32 v[130:131], v[140:141], v[140:141], v[130:131]
	v_pk_add_f32 v[140:141], v[152:153], v[156:157]
	v_mul_f32_e32 v148, v243, v243
	v_pk_add_f32 v[130:131], v[130:131], v[140:141]
	v_pk_mul_f32 v[140:141], v[160:161], v[160:161]
	s_waitcnt lgkmcnt(0)
	v_mfma_f32_16x16x32_bf16 v[136:139], v[6:9], v[144:147], v[136:139]
	v_fma_f32 v140, v154, v154, v140
	v_fma_f32 v141, v155, v155, v141
	v_add_u32_e32 v144, v175, v226
	v_pk_add_f32 v[130:131], v[140:141], v[130:131]
	v_pk_add_f32 v[140:141], v[150:151], v[148:149]
	v_and_b32_e32 v148, 64, v241
	v_pk_add_f32 v[130:131], v[130:131], v[140:141]
	v_add_u32_e32 v149, 64, v148
	v_add_f32_e32 v130, v130, v131
	v_xor_b32_e32 v131, 16, v241
	v_cmp_lt_i32_e32 vcc, v131, v149
	ds_read_b128 v[140:143], v144
	s_mov_b32 s0, 0xf800000
	v_cndmask_b32_e32 v131, v241, v131, vcc
	v_lshlrev_b32_e32 v131, 2, v131
	ds_bpermute_b32 v131, v131, v130
	s_waitcnt lgkmcnt(1)
	v_mfma_f32_16x16x32_bf16 v[132:135], v[2:5], v[140:143], v[132:135]
	ds_read_b128 v[144:147], v144 offset:32768
	v_mov_b32_e32 v243, 0
	v_mov_b32_e32 v244, 0
	s_waitcnt lgkmcnt(1)
	v_add_f32_e32 v130, v130, v131
	v_xor_b32_e32 v131, 32, v241
	v_cmp_lt_i32_e32 vcc, v131, v149
	v_mov_b32_e32 v245, 0
	s_nop 0
	v_cndmask_b32_e32 v131, v241, v131, vcc
	v_lshlrev_b32_e32 v131, 2, v131
	ds_bpermute_b32 v149, v131, v130
	v_mov_b32_e32 v131, 0
	s_waitcnt lgkmcnt(0)
	v_add_f32_e32 v130, v130, v149
	v_fmamk_f32 v130, v130, 0x3a800000, v166
	v_mul_f32_e32 v140, 0x4f800000, v130
	v_cmp_gt_f32_e32 vcc, s0, v130
	s_nop 1
	v_cndmask_b32_e32 v130, v130, v140, vcc
	v_sqrt_f32_e32 v149, v130
	v_add_u32_e32 v140, v176, v226
	ds_read_b128 v[140:143], v140
	v_mfma_f32_16x16x32_bf16 v[136:139], v[2:5], v[144:147], v[136:139]
	v_add_u32_e32 v144, -1, v149
	v_fma_f32 v145, -v144, v149, v130
	v_cmp_ge_f32_e64 s[0:1], 0, v145
	v_add_u32_e32 v145, 1, v149
	v_fma_f32 v146, -v145, v149, v130
	v_cndmask_b32_e64 v144, v149, v144, s[0:1]
	v_cmp_lt_f32_e64 s[0:1], 0, v146
	s_waitcnt lgkmcnt(0)
	v_mfma_f32_16x16x32_bf16 v[132:135], v[2:5], v[140:143], v[132:135]
	v_cndmask_b32_e64 v144, v144, v145, s[0:1]
	v_mul_f32_e32 v145, 0x37800000, v144
	v_cndmask_b32_e32 v144, v144, v145, vcc
	v_cmp_class_f32_e32 vcc, v130, v237
	s_nop 1
	v_cndmask_b32_e32 v130, v144, v130, vcc
	v_div_scale_f32 v149, s[0:1], v130, v130, 1.0
	v_rcp_f32_e32 v150, v149
	v_add_u32_e32 v144, v177, v226
	ds_read_b128 v[144:147], v144
	v_fma_f32 v140, -v149, v150, 1.0
	v_fmac_f32_e32 v150, v140, v150
	v_div_scale_f32 v140, vcc, 1.0, v130, 1.0
	v_mul_f32_e32 v141, v140, v150
	v_fma_f32 v142, -v149, v141, v140
	v_fmac_f32_e32 v141, v142, v150
	v_fma_f32 v140, -v149, v141, v140
	v_div_fmas_f32 v140, v140, v150, v141
	v_div_fixup_f32 v173, v140, v130, 1.0
	v_or_b32_e32 v130, v148, v227
	v_lshlrev_b32_e32 v130, 2, v130
	v_or_b32_e32 v140, v148, v229
	ds_bpermute_b32 v130, v130, v173
	v_lshlrev_b32_e32 v140, 2, v140
	ds_bpermute_b32 v140, v140, v173
	s_waitcnt lgkmcnt(2)
	v_mfma_f32_16x16x32_bf16 v[136:139], v[2:5], v[144:147], v[136:139]
	s_waitcnt vmcnt(1) lgkmcnt(1)
	v_fma_f32 v132, v132, v130, v158
	s_waitcnt vmcnt(0)
	s_nop 4
	v_fma_f32 v130, v136, v130, v159
	ds_write2_b32 v228, v132, v130 offset1:16
	s_waitcnt lgkmcnt(1)
	v_fma_f32 v130, v133, v140, v158
	v_or_b32_e32 v133, v148, v231
	v_or_b32_e32 v136, v148, v233
	v_lshlrev_b32_e32 v133, 2, v133
	v_lshlrev_b32_e32 v136, 2, v136
	ds_bpermute_b32 v133, v133, v173
	ds_bpermute_b32 v136, v136, v173
	v_fma_f32 v132, v137, v140, v159
	ds_write2_b32 v230, v130, v132 offset1:16
	v_mov_b32_e32 v137, 0
	s_waitcnt lgkmcnt(2)
	v_fma_f32 v130, v134, v133, v158
	v_fma_f32 v132, v138, v133, v159
	s_waitcnt lgkmcnt(1)
	v_fmac_f32_e32 v158, v135, v136
	v_fmac_f32_e32 v159, v139, v136
	ds_write2_b32 v232, v130, v132 offset1:16
	ds_write2_b32 v234, v158, v159 offset1:16
	s_waitcnt lgkmcnt(0)
	v_mov_b32_e32 v130, 0
	v_mov_b32_e32 v134, 0
	v_mov_b32_e32 v133, 0
	v_mov_b32_e32 v132, 0
	v_mov_b32_e32 v135, 0
	v_mov_b32_e32 v136, 0
	v_mov_b32_e32 v138, 0
	s_and_saveexec_b64 s[54:55], s[4:5]
	s_cbranch_execz .LBB0_1720
	ds_read_b128 v[158:161], v238
	ds_read_b128 v[154:157], v238 offset:16
	ds_read_b128 v[150:153], v238 offset:32
	ds_read_b128 v[146:149], v238 offset:48
	ds_read_b128 v[142:145], v238 offset:64
	ds_read_b128 v[138:141], v238 offset:80
	ds_read_b128 v[134:137], v238 offset:96
	ds_read_b128 v[130:133], v238 offset:112
	s_waitcnt lgkmcnt(7)
	v_max_f32_e32 v243, v158, v158
	s_mov_b32 s0, 0xff61b1e6
	v_max_f32_e32 v243, 0xff61b1e6, v243
	v_cmp_lt_f32_e32 vcc, s0, v158
	v_cmp_gt_f32_e64 s[0:1], v159, v243
	s_nop 1
	v_cndmask_b32_e64 v243, v243, v159, s[0:1]
	v_cndmask_b32_e64 v244, 0, 1, s[0:1]
	v_cmp_gt_f32_e64 s[0:1], v160, v243
	s_nop 1
	v_cndmask_b32_e64 v243, v243, v160, s[0:1]
	v_cndmask_b32_e64 v244, v244, 2, s[0:1]
	v_cmp_gt_f32_e64 s[0:1], v161, v243
	s_nop 1
	v_cndmask_b32_e64 v243, v243, v161, s[0:1]
	v_cndmask_b32_e64 v244, v244, 3, s[0:1]
	s_waitcnt lgkmcnt(6)
	v_cmp_gt_f32_e64 s[0:1], v154, v243
	s_nop 1
	v_cndmask_b32_e64 v243, v243, v154, s[0:1]
	v_cndmask_b32_e64 v244, v244, 4, s[0:1]
	v_cmp_gt_f32_e64 s[0:1], v155, v243
	s_nop 1
	v_cndmask_b32_e64 v243, v243, v155, s[0:1]
	v_cndmask_b32_e64 v244, v244, 5, s[0:1]
	v_cmp_gt_f32_e64 s[0:1], v156, v243
	s_nop 1
	v_cndmask_b32_e64 v243, v243, v156, s[0:1]
	v_cndmask_b32_e64 v244, v244, 6, s[0:1]
	v_cmp_gt_f32_e64 s[0:1], v157, v243
	s_nop 1
	v_cndmask_b32_e64 v243, v243, v157, s[0:1]
	v_cndmask_b32_e64 v244, v244, 7, s[0:1]
	s_waitcnt lgkmcnt(5)
	v_cmp_gt_f32_e64 s[0:1], v150, v243
	s_nop 1
	v_cndmask_b32_e64 v243, v243, v150, s[0:1]
	v_cndmask_b32_e64 v244, v244, 8, s[0:1]
	v_cmp_gt_f32_e64 s[0:1], v151, v243
	s_nop 1
	v_cndmask_b32_e64 v243, v243, v151, s[0:1]
	v_cndmask_b32_e64 v244, v244, 9, s[0:1]
	v_cmp_gt_f32_e64 s[0:1], v152, v243
	s_nop 1
	v_cndmask_b32_e64 v243, v243, v152, s[0:1]
	v_cndmask_b32_e64 v244, v244, 10, s[0:1]
	v_cmp_gt_f32_e64 s[0:1], v153, v243
	s_nop 1
	v_cndmask_b32_e64 v243, v243, v153, s[0:1]
	v_cndmask_b32_e64 v244, v244, 11, s[0:1]
	s_waitcnt lgkmcnt(4)
	v_cmp_gt_f32_e64 s[0:1], v146, v243
	s_nop 1
	v_cndmask_b32_e64 v243, v243, v146, s[0:1]
	v_cndmask_b32_e64 v244, v244, 12, s[0:1]
	v_cmp_gt_f32_e64 s[0:1], v147, v243
	s_nop 1
	v_cndmask_b32_e64 v243, v243, v147, s[0:1]
	v_cndmask_b32_e64 v244, v244, 13, s[0:1]
	v_cmp_gt_f32_e64 s[0:1], v148, v243
	s_nop 1
	v_cndmask_b32_e64 v243, v243, v148, s[0:1]
	v_cndmask_b32_e64 v244, v244, 14, s[0:1]
	v_cmp_gt_f32_e64 s[0:1], v149, v243
	s_nop 1
	v_cndmask_b32_e64 v243, v243, v149, s[0:1]
	v_cndmask_b32_e64 v244, v244, 15, s[0:1]
	s_waitcnt lgkmcnt(3)
	v_cmp_gt_f32_e64 s[0:1], v142, v243
	s_nop 1
	v_cndmask_b32_e64 v243, v243, v142, s[0:1]
	v_cndmask_b32_e64 v244, v244, 16, s[0:1]
	v_cmp_gt_f32_e64 s[0:1], v143, v243
	s_nop 1
	v_cndmask_b32_e64 v243, v243, v143, s[0:1]
	v_cndmask_b32_e64 v244, v244, 17, s[0:1]
	v_cmp_gt_f32_e64 s[0:1], v144, v243
	s_nop 1
	v_cndmask_b32_e64 v243, v243, v144, s[0:1]
	v_cndmask_b32_e64 v244, v244, 18, s[0:1]
	v_cmp_gt_f32_e64 s[0:1], v145, v243
	s_nop 1
	v_cndmask_b32_e64 v243, v243, v145, s[0:1]
	v_cndmask_b32_e64 v244, v244, 19, s[0:1]
	s_waitcnt lgkmcnt(2)
	v_cmp_gt_f32_e64 s[0:1], v138, v243
	s_nop 1
	v_cndmask_b32_e64 v243, v243, v138, s[0:1]
	v_cndmask_b32_e64 v244, v244, 20, s[0:1]
	v_cmp_gt_f32_e64 s[0:1], v139, v243
	s_nop 1
	v_cndmask_b32_e64 v243, v243, v139, s[0:1]
	v_cndmask_b32_e64 v244, v244, 21, s[0:1]
	v_cmp_gt_f32_e64 s[0:1], v140, v243
	s_nop 1
	v_cndmask_b32_e64 v243, v243, v140, s[0:1]
	v_cndmask_b32_e64 v244, v244, 22, s[0:1]
	v_cmp_gt_f32_e64 s[0:1], v141, v243
	s_nop 1
	v_cndmask_b32_e64 v243, v243, v141, s[0:1]
	v_cndmask_b32_e64 v244, v244, 23, s[0:1]
	s_waitcnt lgkmcnt(1)
	v_cmp_gt_f32_e64 s[0:1], v134, v243
	s_nop 1
	v_cndmask_b32_e64 v243, v243, v134, s[0:1]
	v_cndmask_b32_e64 v244, v244, 24, s[0:1]
	v_cmp_gt_f32_e64 s[0:1], v135, v243
	s_nop 1
	v_cndmask_b32_e64 v243, v243, v135, s[0:1]
	v_cndmask_b32_e64 v244, v244, 25, s[0:1]
	v_cmp_gt_f32_e64 s[0:1], v136, v243
	s_nop 1
	v_cndmask_b32_e64 v243, v243, v136, s[0:1]
	v_cndmask_b32_e64 v244, v244, 26, s[0:1]
	v_cmp_gt_f32_e64 s[0:1], v137, v243
	s_nop 1
	v_cndmask_b32_e64 v243, v243, v137, s[0:1]
	v_cndmask_b32_e64 v244, v244, 27, s[0:1]
	s_waitcnt lgkmcnt(0)
	v_cmp_gt_f32_e64 s[0:1], v130, v243
	s_nop 1
	v_cndmask_b32_e64 v243, v243, v130, s[0:1]
	v_cndmask_b32_e64 v244, v244, 28, s[0:1]
	v_cmp_gt_f32_e64 s[0:1], v131, v243
	s_nop 1
	v_cndmask_b32_e64 v243, v243, v131, s[0:1]
	v_cndmask_b32_e64 v244, v244, 29, s[0:1]
	v_cmp_gt_f32_e64 s[0:1], v132, v243
	s_nop 1
	v_cndmask_b32_e64 v245, v243, v132, s[0:1]
	v_cndmask_b32_e64 v244, v244, 30, s[0:1]
	v_cmp_gt_f32_e64 s[0:1], v133, v245
	s_nop 1
	v_cndmask_b32_e64 v243, v244, 31, s[0:1]
	v_cndmask_b32_e64 v246, v245, v133, s[0:1]
	v_cmp_ne_u32_e64 s[0:1], 0, v243
	v_lshlrev_b32_e64 v245, v243, 1
	s_and_b64 s[0:1], s[0:1], vcc
	v_cndmask_b32_e64 v244, v242, v158, s[0:1]
	v_and_b32_e32 v247, 2, v245
	v_cmp_eq_u32_e64 s[0:1], 0, v247
	v_cmp_gt_f32_e64 s[8:9], v159, v244
	s_and_b64 s[0:1], s[0:1], s[8:9]
	v_cndmask_b32_e64 v244, v244, v159, s[0:1]
	v_and_b32_e32 v248, 4, v245
	v_cndmask_b32_e64 v247, 0, 1, s[0:1]
	v_cmp_eq_u32_e64 s[0:1], 0, v248
	v_cmp_gt_f32_e64 s[8:9], v160, v244
	s_and_b64 s[0:1], s[0:1], s[8:9]
	v_cndmask_b32_e64 v244, v244, v160, s[0:1]
	v_and_b32_e32 v248, 8, v245
	v_cndmask_b32_e64 v247, v247, 2, s[0:1]
	v_cmp_eq_u32_e64 s[0:1], 0, v248
	v_cmp_gt_f32_e64 s[8:9], v161, v244
	s_and_b64 s[0:1], s[0:1], s[8:9]
	v_cndmask_b32_e64 v244, v244, v161, s[0:1]
	v_and_b32_e32 v248, 16, v245
	v_cndmask_b32_e64 v247, v247, 3, s[0:1]
	v_cmp_eq_u32_e64 s[0:1], 0, v248
	v_cmp_gt_f32_e64 s[8:9], v154, v244
	s_and_b64 s[0:1], s[0:1], s[8:9]
	v_cndmask_b32_e64 v244, v244, v154, s[0:1]
	v_and_b32_e32 v248, 32, v245
	v_cndmask_b32_e64 v247, v247, 4, s[0:1]
	v_cmp_eq_u32_e64 s[0:1], 0, v248
	v_cmp_gt_f32_e64 s[8:9], v155, v244
	s_and_b64 s[0:1], s[0:1], s[8:9]
	v_cndmask_b32_e64 v244, v244, v155, s[0:1]
	v_and_b32_e32 v248, 64, v245
	v_cndmask_b32_e64 v247, v247, 5, s[0:1]
	v_cmp_eq_u32_e64 s[0:1], 0, v248
	v_cmp_gt_f32_e64 s[8:9], v156, v244
	s_and_b64 s[0:1], s[0:1], s[8:9]
	v_cndmask_b32_e64 v244, v244, v156, s[0:1]
	v_and_b32_e32 v248, 0x80, v245
	v_cndmask_b32_e64 v247, v247, 6, s[0:1]
	v_cmp_eq_u32_e64 s[0:1], 0, v248
	v_cmp_gt_f32_e64 s[8:9], v157, v244
	s_and_b64 s[0:1], s[0:1], s[8:9]
	v_cndmask_b32_e64 v244, v244, v157, s[0:1]
	v_and_b32_e32 v248, 0x100, v245
	v_cndmask_b32_e64 v247, v247, 7, s[0:1]
	v_cmp_eq_u32_e64 s[0:1], 0, v248
	v_cmp_gt_f32_e64 s[8:9], v150, v244
	s_and_b64 s[0:1], s[0:1], s[8:9]
	v_cndmask_b32_e64 v244, v244, v150, s[0:1]
	v_and_b32_e32 v248, 0x200, v245
	v_cndmask_b32_e64 v247, v247, 8, s[0:1]
	v_cmp_eq_u32_e64 s[0:1], 0, v248
	v_cmp_gt_f32_e64 s[8:9], v151, v244
	s_and_b64 s[0:1], s[0:1], s[8:9]
	v_cndmask_b32_e64 v244, v244, v151, s[0:1]
	v_and_b32_e32 v248, 0x400, v245
	v_cndmask_b32_e64 v247, v247, 9, s[0:1]
	v_cmp_eq_u32_e64 s[0:1], 0, v248
	v_cmp_gt_f32_e64 s[8:9], v152, v244
	s_and_b64 s[0:1], s[0:1], s[8:9]
	v_cndmask_b32_e64 v244, v244, v152, s[0:1]
	v_and_b32_e32 v248, 0x800, v245
	v_cndmask_b32_e64 v247, v247, 10, s[0:1]
	v_cmp_eq_u32_e64 s[0:1], 0, v248
	v_cmp_gt_f32_e64 s[8:9], v153, v244
	s_and_b64 s[0:1], s[0:1], s[8:9]
	v_cndmask_b32_e64 v244, v244, v153, s[0:1]
	v_and_b32_e32 v248, 0x1000, v245
	v_cndmask_b32_e64 v247, v247, 11, s[0:1]
	v_cmp_eq_u32_e64 s[0:1], 0, v248
	v_cmp_gt_f32_e64 s[8:9], v146, v244
	s_and_b64 s[0:1], s[0:1], s[8:9]
	v_cndmask_b32_e64 v244, v244, v146, s[0:1]
	v_and_b32_e32 v248, 0x2000, v245
	v_cndmask_b32_e64 v247, v247, 12, s[0:1]
	v_cmp_eq_u32_e64 s[0:1], 0, v248
	v_cmp_gt_f32_e64 s[8:9], v147, v244
	s_and_b64 s[0:1], s[0:1], s[8:9]
	v_cndmask_b32_e64 v244, v244, v147, s[0:1]
	v_and_b32_e32 v248, 0x4000, v245
	v_cndmask_b32_e64 v247, v247, 13, s[0:1]
	v_cmp_eq_u32_e64 s[0:1], 0, v248
	v_cmp_gt_f32_e64 s[8:9], v148, v244
	s_and_b64 s[0:1], s[0:1], s[8:9]
	v_cndmask_b32_e64 v244, v244, v148, s[0:1]
	v_and_b32_e32 v248, 0x8000, v245
	v_cndmask_b32_e64 v247, v247, 14, s[0:1]
	v_cmp_eq_u32_e64 s[0:1], 0, v248
	v_cmp_gt_f32_e64 s[8:9], v149, v244
	s_and_b64 s[0:1], s[0:1], s[8:9]
	v_cndmask_b32_e64 v244, v244, v149, s[0:1]
	v_and_b32_e32 v248, 0x10000, v245
	v_cndmask_b32_e64 v247, v247, 15, s[0:1]
	v_cmp_eq_u32_e64 s[0:1], 0, v248
	v_cmp_gt_f32_e64 s[8:9], v142, v244
	s_and_b64 s[0:1], s[0:1], s[8:9]
	v_cndmask_b32_e64 v244, v244, v142, s[0:1]
	v_and_b32_e32 v248, 0x20000, v245
	v_cndmask_b32_e64 v247, v247, 16, s[0:1]
	v_cmp_eq_u32_e64 s[0:1], 0, v248
	v_cmp_gt_f32_e64 s[8:9], v143, v244
	s_and_b64 s[0:1], s[0:1], s[8:9]
	v_cndmask_b32_e64 v244, v244, v143, s[0:1]
	v_and_b32_e32 v248, 0x40000, v245
	v_cndmask_b32_e64 v247, v247, 17, s[0:1]
	v_cmp_eq_u32_e64 s[0:1], 0, v248
	v_cmp_gt_f32_e64 s[8:9], v144, v244
	s_and_b64 s[0:1], s[0:1], s[8:9]
	v_cndmask_b32_e64 v244, v244, v144, s[0:1]
	v_and_b32_e32 v248, 0x80000, v245
	v_cndmask_b32_e64 v247, v247, 18, s[0:1]
	v_cmp_eq_u32_e64 s[0:1], 0, v248
	v_cmp_gt_f32_e64 s[8:9], v145, v244
	s_and_b64 s[0:1], s[0:1], s[8:9]
	v_cndmask_b32_e64 v244, v244, v145, s[0:1]
	v_and_b32_e32 v248, 0x100000, v245
	v_cndmask_b32_e64 v247, v247, 19, s[0:1]
	v_cmp_eq_u32_e64 s[0:1], 0, v248
	v_cmp_gt_f32_e64 s[8:9], v138, v244
	s_and_b64 s[0:1], s[0:1], s[8:9]
	v_cndmask_b32_e64 v244, v244, v138, s[0:1]
	v_and_b32_e32 v248, 0x200000, v245
	v_cndmask_b32_e64 v247, v247, 20, s[0:1]
	v_cmp_eq_u32_e64 s[0:1], 0, v248
	v_cmp_gt_f32_e64 s[8:9], v139, v244
	s_and_b64 s[0:1], s[0:1], s[8:9]
	v_cndmask_b32_e64 v244, v244, v139, s[0:1]
	v_and_b32_e32 v248, 0x400000, v245
	v_cndmask_b32_e64 v247, v247, 21, s[0:1]
	v_cmp_eq_u32_e64 s[0:1], 0, v248
	v_cmp_gt_f32_e64 s[8:9], v140, v244
	s_and_b64 s[0:1], s[0:1], s[8:9]
	v_cndmask_b32_e64 v244, v244, v140, s[0:1]
	v_and_b32_e32 v248, 0x800000, v245
	v_cndmask_b32_e64 v247, v247, 22, s[0:1]
	v_cmp_eq_u32_e64 s[0:1], 0, v248
	v_cmp_gt_f32_e64 s[8:9], v141, v244
	s_and_b64 s[0:1], s[0:1], s[8:9]
	v_cndmask_b32_e64 v244, v244, v141, s[0:1]
	v_and_b32_e32 v248, 0x1000000, v245
	v_cndmask_b32_e64 v247, v247, 23, s[0:1]
	v_cmp_eq_u32_e64 s[0:1], 0, v248
	v_cmp_gt_f32_e64 s[8:9], v134, v244
	s_and_b64 s[0:1], s[0:1], s[8:9]
	v_cndmask_b32_e64 v244, v244, v134, s[0:1]
	v_and_b32_e32 v248, 0x2000000, v245
	v_cndmask_b32_e64 v247, v247, 24, s[0:1]
	v_cmp_eq_u32_e64 s[0:1], 0, v248
	v_cmp_gt_f32_e64 s[8:9], v135, v244
	s_and_b64 s[0:1], s[0:1], s[8:9]
	v_cndmask_b32_e64 v244, v244, v135, s[0:1]
	v_and_b32_e32 v248, 0x4000000, v245
	v_cndmask_b32_e64 v247, v247, 25, s[0:1]
	v_cmp_eq_u32_e64 s[0:1], 0, v248
	v_cmp_gt_f32_e64 s[8:9], v136, v244
	s_and_b64 s[0:1], s[0:1], s[8:9]
	v_cndmask_b32_e64 v244, v244, v136, s[0:1]
	v_and_b32_e32 v248, 0x8000000, v245
	v_cndmask_b32_e64 v247, v247, 26, s[0:1]
	v_cmp_eq_u32_e64 s[0:1], 0, v248
	v_cmp_gt_f32_e64 s[8:9], v137, v244
	s_and_b64 s[0:1], s[0:1], s[8:9]
	v_cndmask_b32_e64 v244, v244, v137, s[0:1]
	v_and_b32_e32 v248, 0x10000000, v245
	v_cndmask_b32_e64 v247, v247, 27, s[0:1]
	v_cmp_eq_u32_e64 s[0:1], 0, v248
	v_cmp_gt_f32_e64 s[8:9], v130, v244
	s_and_b64 s[0:1], s[0:1], s[8:9]
	v_cndmask_b32_e64 v244, v244, v130, s[0:1]
	v_and_b32_e32 v248, 0x20000000, v245
	v_cndmask_b32_e64 v247, v247, 28, s[0:1]
	v_cmp_eq_u32_e64 s[0:1], 0, v248
	v_cmp_gt_f32_e64 s[8:9], v131, v244
	s_and_b64 s[0:1], s[0:1], s[8:9]
	v_cndmask_b32_e64 v244, v244, v131, s[0:1]
	v_and_b32_e32 v248, 2.0, v245
	v_cndmask_b32_e64 v247, v247, 29, s[0:1]
	v_cmp_eq_u32_e64 s[0:1], 0, v248
	v_cmp_gt_f32_e64 s[8:9], v132, v244
	s_and_b64 s[0:1], s[0:1], s[8:9]
	v_cndmask_b32_e64 v248, v244, v132, s[0:1]
	v_cndmask_b32_e64 v247, v247, 30, s[0:1]
	v_cmp_ne_u32_e64 s[0:1], 31, v243
	v_cmp_gt_f32_e64 s[8:9], v133, v248
	s_and_b64 s[0:1], s[0:1], s[8:9]
	v_cndmask_b32_e64 v244, v247, 31, s[0:1]
	v_cndmask_b32_e64 v247, v248, v133, s[0:1]
	v_lshl_or_b32 v248, 1, v244, v245
	v_and_b32_e32 v245, 1, v248
	v_cmp_eq_u32_e64 s[0:1], 0, v245
	s_and_b64 s[0:1], s[0:1], vcc
	v_and_b32_e32 v249, 2, v248
	v_cndmask_b32_e64 v245, v242, v158, s[0:1]
	v_cmp_eq_u32_e64 s[0:1], 0, v249
	v_cmp_gt_f32_e64 s[8:9], v159, v245
	s_and_b64 s[0:1], s[0:1], s[8:9]
	v_cndmask_b32_e64 v245, v245, v159, s[0:1]
	v_and_b32_e32 v250, 4, v248
	v_cndmask_b32_e64 v249, 0, 1, s[0:1]
	v_cmp_eq_u32_e64 s[0:1], 0, v250
	v_cmp_gt_f32_e64 s[8:9], v160, v245
	s_and_b64 s[0:1], s[0:1], s[8:9]
	v_cndmask_b32_e64 v245, v245, v160, s[0:1]
	v_and_b32_e32 v250, 8, v248
	v_cndmask_b32_e64 v249, v249, 2, s[0:1]
	v_cmp_eq_u32_e64 s[0:1], 0, v250
	v_cmp_gt_f32_e64 s[8:9], v161, v245
	s_and_b64 s[0:1], s[0:1], s[8:9]
	v_cndmask_b32_e64 v245, v245, v161, s[0:1]
	v_and_b32_e32 v250, 16, v248
	v_cndmask_b32_e64 v249, v249, 3, s[0:1]
	v_cmp_eq_u32_e64 s[0:1], 0, v250
	v_cmp_gt_f32_e64 s[8:9], v154, v245
	s_and_b64 s[0:1], s[0:1], s[8:9]
	v_cndmask_b32_e64 v245, v245, v154, s[0:1]
	v_and_b32_e32 v250, 32, v248
	v_cndmask_b32_e64 v249, v249, 4, s[0:1]
	v_cmp_eq_u32_e64 s[0:1], 0, v250
	v_cmp_gt_f32_e64 s[8:9], v155, v245
	s_and_b64 s[0:1], s[0:1], s[8:9]
	v_cndmask_b32_e64 v245, v245, v155, s[0:1]
	v_and_b32_e32 v250, 64, v248
	v_cndmask_b32_e64 v249, v249, 5, s[0:1]
	v_cmp_eq_u32_e64 s[0:1], 0, v250
	v_cmp_gt_f32_e64 s[8:9], v156, v245
	s_and_b64 s[0:1], s[0:1], s[8:9]
	v_cndmask_b32_e64 v245, v245, v156, s[0:1]
	v_and_b32_e32 v250, 0x80, v248
	v_cndmask_b32_e64 v249, v249, 6, s[0:1]
	v_cmp_eq_u32_e64 s[0:1], 0, v250
	v_cmp_gt_f32_e64 s[8:9], v157, v245
	s_and_b64 s[0:1], s[0:1], s[8:9]
	v_cndmask_b32_e64 v245, v245, v157, s[0:1]
	v_and_b32_e32 v250, 0x100, v248
	v_cndmask_b32_e64 v249, v249, 7, s[0:1]
	v_cmp_eq_u32_e64 s[0:1], 0, v250
	v_cmp_gt_f32_e64 s[8:9], v150, v245
	s_and_b64 s[0:1], s[0:1], s[8:9]
	v_cndmask_b32_e64 v245, v245, v150, s[0:1]
	v_and_b32_e32 v250, 0x200, v248
	v_cndmask_b32_e64 v249, v249, 8, s[0:1]
	v_cmp_eq_u32_e64 s[0:1], 0, v250
	v_cmp_gt_f32_e64 s[8:9], v151, v245
	s_and_b64 s[0:1], s[0:1], s[8:9]
	v_cndmask_b32_e64 v245, v245, v151, s[0:1]
	v_and_b32_e32 v250, 0x400, v248
	v_cndmask_b32_e64 v249, v249, 9, s[0:1]
	v_cmp_eq_u32_e64 s[0:1], 0, v250
	v_cmp_gt_f32_e64 s[8:9], v152, v245
	s_and_b64 s[0:1], s[0:1], s[8:9]
	v_cndmask_b32_e64 v245, v245, v152, s[0:1]
	v_and_b32_e32 v250, 0x800, v248
	v_cndmask_b32_e64 v249, v249, 10, s[0:1]
	v_cmp_eq_u32_e64 s[0:1], 0, v250
	v_cmp_gt_f32_e64 s[8:9], v153, v245
	s_and_b64 s[0:1], s[0:1], s[8:9]
	v_cndmask_b32_e64 v245, v245, v153, s[0:1]
	v_and_b32_e32 v250, 0x1000, v248
	v_cndmask_b32_e64 v249, v249, 11, s[0:1]
	v_cmp_eq_u32_e64 s[0:1], 0, v250
	v_cmp_gt_f32_e64 s[8:9], v146, v245
	s_and_b64 s[0:1], s[0:1], s[8:9]
	v_cndmask_b32_e64 v245, v245, v146, s[0:1]
	v_and_b32_e32 v250, 0x2000, v248
	v_cndmask_b32_e64 v249, v249, 12, s[0:1]
	v_cmp_eq_u32_e64 s[0:1], 0, v250
	v_cmp_gt_f32_e64 s[8:9], v147, v245
	s_and_b64 s[0:1], s[0:1], s[8:9]
	v_cndmask_b32_e64 v245, v245, v147, s[0:1]
	v_and_b32_e32 v250, 0x4000, v248
	v_cndmask_b32_e64 v249, v249, 13, s[0:1]
	v_cmp_eq_u32_e64 s[0:1], 0, v250
	v_cmp_gt_f32_e64 s[8:9], v148, v245
	s_and_b64 s[0:1], s[0:1], s[8:9]
	v_cndmask_b32_e64 v245, v245, v148, s[0:1]
	v_and_b32_e32 v250, 0x8000, v248
	v_cndmask_b32_e64 v249, v249, 14, s[0:1]
	v_cmp_eq_u32_e64 s[0:1], 0, v250
	v_cmp_gt_f32_e64 s[8:9], v149, v245
	s_and_b64 s[0:1], s[0:1], s[8:9]
	v_cndmask_b32_e64 v245, v245, v149, s[0:1]
	v_and_b32_e32 v250, 0x10000, v248
	v_cndmask_b32_e64 v249, v249, 15, s[0:1]
	v_cmp_eq_u32_e64 s[0:1], 0, v250
	v_cmp_gt_f32_e64 s[8:9], v142, v245
	s_and_b64 s[0:1], s[0:1], s[8:9]
	v_cndmask_b32_e64 v245, v245, v142, s[0:1]
	v_and_b32_e32 v250, 0x20000, v248
	v_cndmask_b32_e64 v249, v249, 16, s[0:1]
	v_cmp_eq_u32_e64 s[0:1], 0, v250
	v_cmp_gt_f32_e64 s[8:9], v143, v245
	s_and_b64 s[0:1], s[0:1], s[8:9]
	v_cndmask_b32_e64 v245, v245, v143, s[0:1]
	v_and_b32_e32 v250, 0x40000, v248
	v_cndmask_b32_e64 v249, v249, 17, s[0:1]
	v_cmp_eq_u32_e64 s[0:1], 0, v250
	v_cmp_gt_f32_e64 s[8:9], v144, v245
	s_and_b64 s[0:1], s[0:1], s[8:9]
	v_cndmask_b32_e64 v245, v245, v144, s[0:1]
	v_and_b32_e32 v250, 0x80000, v248
	v_cndmask_b32_e64 v249, v249, 18, s[0:1]
	v_cmp_eq_u32_e64 s[0:1], 0, v250
	v_cmp_gt_f32_e64 s[8:9], v145, v245
	s_and_b64 s[0:1], s[0:1], s[8:9]
	v_cndmask_b32_e64 v245, v245, v145, s[0:1]
	v_and_b32_e32 v250, 0x100000, v248
	v_cndmask_b32_e64 v249, v249, 19, s[0:1]
	v_cmp_eq_u32_e64 s[0:1], 0, v250
	v_cmp_gt_f32_e64 s[8:9], v138, v245
	s_and_b64 s[0:1], s[0:1], s[8:9]
	v_cndmask_b32_e64 v245, v245, v138, s[0:1]
	v_and_b32_e32 v250, 0x200000, v248
	v_cndmask_b32_e64 v249, v249, 20, s[0:1]
	v_cmp_eq_u32_e64 s[0:1], 0, v250
	v_cmp_gt_f32_e64 s[8:9], v139, v245
	s_and_b64 s[0:1], s[0:1], s[8:9]
	v_cndmask_b32_e64 v245, v245, v139, s[0:1]
	v_and_b32_e32 v250, 0x400000, v248
	v_cndmask_b32_e64 v249, v249, 21, s[0:1]
	v_cmp_eq_u32_e64 s[0:1], 0, v250
	v_cmp_gt_f32_e64 s[8:9], v140, v245
	s_and_b64 s[0:1], s[0:1], s[8:9]
	v_cndmask_b32_e64 v245, v245, v140, s[0:1]
	v_and_b32_e32 v250, 0x800000, v248
	v_cndmask_b32_e64 v249, v249, 22, s[0:1]
	v_cmp_eq_u32_e64 s[0:1], 0, v250
	v_cmp_gt_f32_e64 s[8:9], v141, v245
	s_and_b64 s[0:1], s[0:1], s[8:9]
	v_cndmask_b32_e64 v245, v245, v141, s[0:1]
	v_and_b32_e32 v250, 0x1000000, v248
	v_cndmask_b32_e64 v249, v249, 23, s[0:1]
	v_cmp_eq_u32_e64 s[0:1], 0, v250
	v_cmp_gt_f32_e64 s[8:9], v134, v245
	s_and_b64 s[0:1], s[0:1], s[8:9]
	v_cndmask_b32_e64 v245, v245, v134, s[0:1]
	v_and_b32_e32 v250, 0x2000000, v248
	v_cndmask_b32_e64 v249, v249, 24, s[0:1]
	v_cmp_eq_u32_e64 s[0:1], 0, v250
	v_cmp_gt_f32_e64 s[8:9], v135, v245
	s_and_b64 s[0:1], s[0:1], s[8:9]
	v_cndmask_b32_e64 v245, v245, v135, s[0:1]
	v_and_b32_e32 v250, 0x4000000, v248
	v_cndmask_b32_e64 v249, v249, 25, s[0:1]
	v_cmp_eq_u32_e64 s[0:1], 0, v250
	v_cmp_gt_f32_e64 s[8:9], v136, v245
	s_and_b64 s[0:1], s[0:1], s[8:9]
	v_cndmask_b32_e64 v245, v245, v136, s[0:1]
	v_and_b32_e32 v250, 0x8000000, v248
	v_cndmask_b32_e64 v249, v249, 26, s[0:1]
	v_cmp_eq_u32_e64 s[0:1], 0, v250
	v_cmp_gt_f32_e64 s[8:9], v137, v245
	s_and_b64 s[0:1], s[0:1], s[8:9]
	v_cndmask_b32_e64 v245, v245, v137, s[0:1]
	v_and_b32_e32 v250, 0x10000000, v248
	v_cndmask_b32_e64 v249, v249, 27, s[0:1]
	v_cmp_eq_u32_e64 s[0:1], 0, v250
	v_cmp_gt_f32_e64 s[8:9], v130, v245
	s_and_b64 s[0:1], s[0:1], s[8:9]
	v_cndmask_b32_e64 v245, v245, v130, s[0:1]
	v_and_b32_e32 v250, 0x20000000, v248
	v_cndmask_b32_e64 v249, v249, 28, s[0:1]
	v_cmp_eq_u32_e64 s[0:1], 0, v250
	v_cmp_gt_f32_e64 s[8:9], v131, v245
	s_and_b64 s[0:1], s[0:1], s[8:9]
	v_cndmask_b32_e64 v245, v245, v131, s[0:1]
	v_and_b32_e32 v250, 2.0, v248
	v_cndmask_b32_e64 v249, v249, 29, s[0:1]
	v_cmp_eq_u32_e64 s[0:1], 0, v250
	v_cmp_gt_f32_e64 s[8:9], v132, v245
	s_and_b64 s[0:1], s[0:1], s[8:9]
	v_cndmask_b32_e64 v250, v245, v132, s[0:1]
	v_cndmask_b32_e64 v249, v249, 30, s[0:1]
	v_cmp_lt_i32_e64 s[0:1], -1, v248
	v_cmp_gt_f32_e64 s[8:9], v133, v250
	s_and_b64 s[0:1], s[0:1], s[8:9]
	v_cndmask_b32_e64 v245, v249, 31, s[0:1]
	v_cndmask_b32_e64 v249, v250, v133, s[0:1]
	v_lshlrev_b32_e64 v250, v245, 1
	v_bitop3_b32 v252, v250, 1, v248 bitop3:0xc8
	v_cmp_eq_u32_e64 s[0:1], 0, v252
	s_and_b64 vcc, s[0:1], vcc
	v_cndmask_b32_e32 v158, v242, v158, vcc
	v_bitop3_b32 v252, v250, 2, v248 bitop3:0xc8
	v_cmp_eq_u32_e32 vcc, 0, v252
	v_cmp_gt_f32_e64 s[0:1], v159, v158
	s_and_b64 vcc, vcc, s[0:1]
	v_cndmask_b32_e32 v158, v158, v159, vcc
	v_bitop3_b32 v159, v250, 4, v248 bitop3:0xc8
	v_cndmask_b32_e64 v252, 0, 1, vcc
	v_cmp_eq_u32_e32 vcc, 0, v159
	v_cmp_gt_f32_e64 s[0:1], v160, v158
	s_and_b64 vcc, vcc, s[0:1]
	v_cndmask_b32_e32 v158, v158, v160, vcc
	v_bitop3_b32 v160, v250, 8, v248 bitop3:0xc8
	v_cndmask_b32_e64 v159, v252, 2, vcc
	v_cmp_eq_u32_e32 vcc, 0, v160
	v_cmp_gt_f32_e64 s[0:1], v161, v158
	s_and_b64 vcc, vcc, s[0:1]
	v_cndmask_b32_e32 v158, v158, v161, vcc
	v_bitop3_b32 v160, v250, 16, v248 bitop3:0xc8
	v_cndmask_b32_e64 v159, v159, 3, vcc
	v_cmp_eq_u32_e32 vcc, 0, v160
	v_cmp_gt_f32_e64 s[0:1], v154, v158
	s_and_b64 vcc, vcc, s[0:1]
	v_cndmask_b32_e32 v154, v158, v154, vcc
	v_bitop3_b32 v158, v250, 32, v248 bitop3:0xc8
	v_cndmask_b32_e64 v159, v159, 4, vcc
	v_cmp_eq_u32_e32 vcc, 0, v158
	v_cmp_gt_f32_e64 s[0:1], v155, v154
	s_and_b64 vcc, vcc, s[0:1]
	v_cndmask_b32_e32 v154, v154, v155, vcc
	v_bitop3_b32 v155, v250, 64, v248 bitop3:0xc8
	v_cndmask_b32_e64 v158, v159, 5, vcc
	v_cmp_eq_u32_e32 vcc, 0, v155
	v_cmp_gt_f32_e64 s[0:1], v156, v154
	s_and_b64 vcc, vcc, s[0:1]
	s_movk_i32 s0, 0x80
	v_cndmask_b32_e32 v154, v154, v156, vcc
	v_bitop3_b32 v156, v250, s0, v248 bitop3:0xc8
	v_cndmask_b32_e64 v155, v158, 6, vcc
	v_cmp_eq_u32_e32 vcc, 0, v156
	v_cmp_gt_f32_e64 s[0:1], v157, v154
	s_and_b64 vcc, vcc, s[0:1]
	s_movk_i32 s0, 0x100
	v_cndmask_b32_e32 v154, v154, v157, vcc
	v_bitop3_b32 v156, v250, s0, v248 bitop3:0xc8
	v_cndmask_b32_e64 v155, v155, 7, vcc
	v_cmp_eq_u32_e32 vcc, 0, v156
	v_cmp_gt_f32_e64 s[0:1], v150, v154
	s_and_b64 vcc, vcc, s[0:1]
	s_movk_i32 s0, 0x200
	v_cndmask_b32_e32 v150, v154, v150, vcc
	v_bitop3_b32 v154, v250, s0, v248 bitop3:0xc8
	v_cndmask_b32_e64 v155, v155, 8, vcc
	v_cmp_eq_u32_e32 vcc, 0, v154
	v_cmp_gt_f32_e64 s[0:1], v151, v150
	s_and_b64 vcc, vcc, s[0:1]
	s_movk_i32 s0, 0x400
	v_cndmask_b32_e32 v150, v150, v151, vcc
	v_bitop3_b32 v151, v250, s0, v248 bitop3:0xc8
	v_cndmask_b32_e64 v154, v155, 9, vcc
	v_cmp_eq_u32_e32 vcc, 0, v151
	v_cmp_gt_f32_e64 s[0:1], v152, v150
	s_and_b64 vcc, vcc, s[0:1]
	s_movk_i32 s0, 0x800
	v_cndmask_b32_e32 v150, v150, v152, vcc
	v_bitop3_b32 v152, v250, s0, v248 bitop3:0xc8
	v_cndmask_b32_e64 v151, v154, 10, vcc
	v_cmp_eq_u32_e32 vcc, 0, v152
	v_cmp_gt_f32_e64 s[0:1], v153, v150
	s_and_b64 vcc, vcc, s[0:1]
	s_movk_i32 s0, 0x1000
	v_cndmask_b32_e32 v150, v150, v153, vcc
	v_bitop3_b32 v152, v250, s0, v248 bitop3:0xc8
	v_cndmask_b32_e64 v151, v151, 11, vcc
	v_cmp_eq_u32_e32 vcc, 0, v152
	v_cmp_gt_f32_e64 s[0:1], v146, v150
	s_and_b64 vcc, vcc, s[0:1]
	s_movk_i32 s0, 0x2000
	v_cndmask_b32_e32 v146, v150, v146, vcc
	v_bitop3_b32 v150, v250, s0, v248 bitop3:0xc8
	v_cndmask_b32_e64 v151, v151, 12, vcc
	v_cmp_eq_u32_e32 vcc, 0, v150
	v_cmp_gt_f32_e64 s[0:1], v147, v146
	s_and_b64 vcc, vcc, s[0:1]
	s_movk_i32 s0, 0x4000
	v_cndmask_b32_e32 v146, v146, v147, vcc
	v_bitop3_b32 v147, v250, s0, v248 bitop3:0xc8
	v_cndmask_b32_e64 v150, v151, 13, vcc
	v_cmp_eq_u32_e32 vcc, 0, v147
	v_cmp_gt_f32_e64 s[0:1], v148, v146
	s_and_b64 vcc, vcc, s[0:1]
	s_mov_b32 s0, 0x8000
	v_cndmask_b32_e32 v146, v146, v148, vcc
	v_bitop3_b32 v148, v250, s0, v248 bitop3:0xc8
	v_cndmask_b32_e64 v147, v150, 14, vcc
	v_cmp_eq_u32_e32 vcc, 0, v148
	v_cmp_gt_f32_e64 s[0:1], v149, v146
	s_and_b64 vcc, vcc, s[0:1]
	s_mov_b32 s0, 0x10000
	v_cndmask_b32_e32 v146, v146, v149, vcc
	v_bitop3_b32 v148, v250, s0, v248 bitop3:0xc8
	v_cndmask_b32_e64 v147, v147, 15, vcc
	v_cmp_eq_u32_e32 vcc, 0, v148
	v_cmp_gt_f32_e64 s[0:1], v142, v146
	s_and_b64 vcc, vcc, s[0:1]
	s_mov_b32 s0, 0x20000
	v_cndmask_b32_e32 v142, v146, v142, vcc
	v_bitop3_b32 v146, v250, s0, v248 bitop3:0xc8
	v_cndmask_b32_e64 v147, v147, 16, vcc
	v_cmp_eq_u32_e32 vcc, 0, v146
	v_cmp_gt_f32_e64 s[0:1], v143, v142
	s_and_b64 vcc, vcc, s[0:1]
	v_cndmask_b32_e32 v142, v142, v143, vcc
	v_bitop3_b32 v143, v250, s79, v248 bitop3:0xc8
	v_cndmask_b32_e64 v146, v147, 17, vcc
	v_cmp_eq_u32_e32 vcc, 0, v143
	v_cmp_gt_f32_e64 s[0:1], v144, v142
	s_and_b64 vcc, vcc, s[0:1]
	v_cndmask_b32_e32 v142, v142, v144, vcc
	v_bitop3_b32 v144, v250, s80, v248 bitop3:0xc8
	v_cndmask_b32_e64 v143, v146, 18, vcc
	v_cmp_eq_u32_e32 vcc, 0, v144
	v_cmp_gt_f32_e64 s[0:1], v145, v142
	s_and_b64 vcc, vcc, s[0:1]
	v_cndmask_b32_e32 v142, v142, v145, vcc
	v_bitop3_b32 v144, v250, s81, v248 bitop3:0xc8
	v_cndmask_b32_e64 v143, v143, 19, vcc
	v_cmp_eq_u32_e32 vcc, 0, v144
	v_cmp_gt_f32_e64 s[0:1], v138, v142
	s_and_b64 vcc, vcc, s[0:1]
	v_cndmask_b32_e32 v138, v142, v138, vcc
	v_bitop3_b32 v142, v250, s82, v248 bitop3:0xc8
	v_cndmask_b32_e64 v143, v143, 20, vcc
	v_cmp_eq_u32_e32 vcc, 0, v142
	v_cmp_gt_f32_e64 s[0:1], v139, v138
	s_and_b64 vcc, vcc, s[0:1]
	v_cndmask_b32_e32 v138, v138, v139, vcc
	v_bitop3_b32 v139, v250, s83, v248 bitop3:0xc8
	v_cndmask_b32_e64 v142, v143, 21, vcc
	v_cmp_eq_u32_e32 vcc, 0, v139
	v_cmp_gt_f32_e64 s[0:1], v140, v138
	s_and_b64 vcc, vcc, s[0:1]
	v_cndmask_b32_e32 v138, v138, v140, vcc
	v_bitop3_b32 v140, v250, s84, v248 bitop3:0xc8
	v_cndmask_b32_e64 v139, v142, 22, vcc
	v_cmp_eq_u32_e32 vcc, 0, v140
	v_cmp_gt_f32_e64 s[0:1], v141, v138
	s_and_b64 vcc, vcc, s[0:1]
	v_cndmask_b32_e32 v138, v138, v141, vcc
	v_bitop3_b32 v140, v250, s85, v248 bitop3:0xc8
	v_cndmask_b32_e64 v139, v139, 23, vcc
	v_cmp_eq_u32_e32 vcc, 0, v140
	v_cmp_gt_f32_e64 s[0:1], v134, v138
	s_and_b64 vcc, vcc, s[0:1]
	v_cndmask_b32_e32 v134, v138, v134, vcc
	v_bitop3_b32 v138, v250, s86, v248 bitop3:0xc8
	v_cndmask_b32_e64 v139, v139, 24, vcc
	v_cmp_eq_u32_e32 vcc, 0, v138
	v_cmp_gt_f32_e64 s[0:1], v135, v134
	s_and_b64 vcc, vcc, s[0:1]
	v_cndmask_b32_e32 v134, v134, v135, vcc
	v_bitop3_b32 v135, v250, s87, v248 bitop3:0xc8
	v_cndmask_b32_e64 v138, v139, 25, vcc
	v_cmp_eq_u32_e32 vcc, 0, v135
	v_cmp_gt_f32_e64 s[0:1], v136, v134
	s_and_b64 vcc, vcc, s[0:1]
	v_cndmask_b32_e32 v134, v134, v136, vcc
	v_bitop3_b32 v136, v250, s91, v248 bitop3:0xc8
	v_cndmask_b32_e64 v135, v138, 26, vcc
	v_cmp_eq_u32_e32 vcc, 0, v136
	v_cmp_gt_f32_e64 s[0:1], v137, v134
	s_and_b64 vcc, vcc, s[0:1]
	v_cndmask_b32_e32 v134, v134, v137, vcc
	v_bitop3_b32 v136, v250, s92, v248 bitop3:0xc8
	v_cndmask_b32_e64 v135, v135, 27, vcc
	v_cmp_eq_u32_e32 vcc, 0, v136
	v_cmp_gt_f32_e64 s[0:1], v130, v134
	s_and_b64 vcc, vcc, s[0:1]
	v_cndmask_b32_e32 v130, v134, v130, vcc
	v_bitop3_b32 v134, v250, s93, v248 bitop3:0xc8
	v_cndmask_b32_e64 v135, v135, 28, vcc
	v_cmp_eq_u32_e32 vcc, 0, v134
	v_cmp_gt_f32_e64 s[0:1], v131, v130
	s_and_b64 vcc, vcc, s[0:1]
	v_cndmask_b32_e32 v130, v130, v131, vcc
	v_bitop3_b32 v131, v250, 2.0, v248 bitop3:0xc8
	v_cndmask_b32_e64 v134, v135, 29, vcc
	v_cmp_eq_u32_e32 vcc, 0, v131
	v_cmp_gt_f32_e64 s[0:1], v132, v130
	s_and_b64 vcc, vcc, s[0:1]
	v_or_b32_e32 v251, v250, v248
	v_cndmask_b32_e32 v130, v130, v132, vcc
	v_cndmask_b32_e64 v131, v134, 30, vcc
	v_cmp_lt_i32_e32 vcc, -1, v251
	v_cmp_gt_f32_e64 s[0:1], v133, v130
	s_and_b64 vcc, vcc, s[0:1]
	v_cndmask_b32_e32 v132, v130, v133, vcc
	v_sub_f32_e32 v130, v247, v246
	v_cndmask_b32_e64 v134, v131, 31, vcc
	v_mul_f32_e32 v130, 0x3fb8aa3b, v130
	v_sub_f32_e32 v131, v249, v246
	v_exp_f32_e32 v130, v130
	v_mul_f32_e32 v131, 0x3fb8aa3b, v131
	v_sub_f32_e32 v132, v132, v246
	v_exp_f32_e32 v131, v131
	v_mul_f32_e32 v132, 0x3fb8aa3b, v132
	v_exp_f32_e32 v133, v132
	v_add_f32_e32 v132, 1.0, v130
	v_add_f32_e32 v132, v132, v131
	v_add_f32_e32 v132, v132, v133
	v_div_scale_f32 v135, s[0:1], v132, v132, 1.0
	v_rcp_f32_e32 v139, v135
	s_nop 0
	v_fma_f32 v136, -v135, v139, 1.0
	v_fmac_f32_e32 v139, v136, v139
	v_div_scale_f32 v136, vcc, 1.0, v132, 1.0
	v_mul_f32_e32 v140, v136, v139
	v_fma_f32 v137, -v135, v140, v136
	v_fmac_f32_e32 v140, v137, v139
	v_fma_f32 v141, -v135, v140, v136
	v_lshl_add_u32 v135, v243, 2, s67
	ds_add_rtn_u32 v138, v135, v239
	v_lshl_add_u32 v135, v244, 2, s67
	ds_add_rtn_u32 v137, v135, v239
	v_lshl_add_u32 v135, v245, 2, s67
	ds_add_rtn_u32 v136, v135, v239
	v_lshl_add_u32 v135, v134, 2, s67
	ds_add_rtn_u32 v135, v135, v239
	v_div_fmas_f32 v139, v141, v139, v140
	v_div_fixup_f32 v132, v139, v132, 1.0
	v_pk_mul_f32 v[130:131], v[130:131], v[132:133] op_sel_hi:[1,0]
	v_mul_f32_e32 v133, v133, v132

.LBB0_1896:
	s_cmp_eq_u32 s40, 0
	s_cbranch_scc1 .Lpeel6
	s_add_u32 s33, s74, s40
	s_addc_u32 s44, s75, s41
	s_add_u32 s56, s33, 0x1d800080
	s_addc_u32 s57, s44, 0
	s_add_u32 s33, s33, 0x1d800100
	s_addc_u32 s52, s44, 0
	v_add_u32_e32 v2, 0x10000, v173
	v_add_u32_e32 v14, 0x14000, v173
	s_and_b64 s[44:45], s[42:43], exec
	ds_read_b128 v[18:21], v2
	ds_read_b128 v[22:25], v2 offset:1024
	ds_read_b128 v[26:29], v2 offset:2048
	ds_read_b128 v[30:33], v2 offset:3072
	ds_read_b128 v[2:5], v14
	ds_read_b128 v[6:9], v14 offset:1024
	ds_read_b128 v[10:13], v14 offset:2048
	ds_read_b128 v[14:17], v14 offset:3072
	s_cselect_b32 s55, s11, s52
	s_cselect_b32 s54, s10, s33
	s_add_u32 s33, s2, s40
	s_addc_u32 s44, s23, s41
	s_and_b64 s[42:43], s[42:43], exec
	s_cselect_b32 s43, s39, s44
	s_cselect_b32 s42, s38, s33
	s_add_u32 s44, s54, 0x80
	s_addc_u32 s45, s55, 0
	s_add_u32 s52, s42, 0x80
	s_addc_u32 s53, s43, 0
	ds_read_b128 v[180:183], v174
	ds_read_b128 v[184:187], v174 offset:1024
	ds_read_b128 v[188:191], v174 offset:2048
	ds_read_b128 v[192:195], v174 offset:3072
	ds_read_b128 v[196:199], v174 offset:4096
	ds_read_b128 v[200:203], v174 offset:5120
	ds_read_b128 v[204:207], v174 offset:6144
	ds_read_b128 v[208:211], v174 offset:7168
	s_mov_b32 s33, m0
	s_mov_b32 m0, s93
	s_nop 2
	global_load_lds_dwordx4 v178, s[56:57]
	s_mov_b32 m0, s33
	s_nop 0
	s_mov_b32 s33, m0
	s_mov_b32 m0, s94
	s_nop 2
	global_load_lds_dwordx4 v177, s[56:57]
	s_mov_b32 m0, s33
	s_waitcnt vmcnt(8) lgkmcnt(0)
	s_barrier
	s_setprio 1
	v_mfma_f32_16x16x128_f8f6f4 v[158:161], v[18:25], v[180:187], v[158:161]
	v_mfma_f32_16x16x128_f8f6f4 v[154:157], v[26:33], v[180:187], v[154:157]
	v_mfma_f32_16x16x128_f8f6f4 v[150:153], v[18:25], v[188:195], v[150:153]
	v_mfma_f32_16x16x128_f8f6f4 v[146:149], v[26:33], v[188:195], v[146:149]
	v_mfma_f32_16x16x128_f8f6f4 v[142:145], v[18:25], v[196:203], v[142:145]
	v_mfma_f32_16x16x128_f8f6f4 v[138:141], v[26:33], v[196:203], v[138:141]
	v_mfma_f32_16x16x128_f8f6f4 v[134:137], v[18:25], v[204:211], v[134:137]
	v_mfma_f32_16x16x128_f8f6f4 v[130:133], v[26:33], v[204:211], v[130:133]
	v_mfma_f32_16x16x128_f8f6f4 v[126:129], v[2:9], v[180:187], v[126:129]
	v_mfma_f32_16x16x128_f8f6f4 v[122:125], v[10:17], v[180:187], v[122:125]
	v_mfma_f32_16x16x128_f8f6f4 v[118:121], v[2:9], v[188:195], v[118:121]
	v_mfma_f32_16x16x128_f8f6f4 v[114:117], v[10:17], v[188:195], v[114:117]
	v_mfma_f32_16x16x128_f8f6f4 v[110:113], v[2:9], v[196:203], v[110:113]
	v_mfma_f32_16x16x128_f8f6f4 v[106:109], v[10:17], v[196:203], v[106:109]
	v_mfma_f32_16x16x128_f8f6f4 v[102:105], v[2:9], v[204:211], v[102:105]
	v_mfma_f32_16x16x128_f8f6f4 v[98:101], v[10:17], v[204:211], v[98:101]
	s_setprio 0
	s_barrier
	ds_read_b128 v[180:183], v174 offset:16384
	ds_read_b128 v[184:187], v174 offset:17408
	ds_read_b128 v[188:191], v174 offset:18432
	ds_read_b128 v[192:195], v174 offset:19456
	ds_read_b128 v[196:199], v174 offset:20480
	ds_read_b128 v[200:203], v174 offset:21504
	ds_read_b128 v[204:207], v174 offset:22528
	ds_read_b128 v[208:211], v174 offset:23552
	s_mov_b32 s33, m0
	s_mov_b32 m0, s67
	s_nop 2
	global_load_lds_dwordx4 v1, s[42:43]
	s_mov_b32 m0, s33
	s_add_u32 s56, s42, 0x20000
	s_mov_b32 s33, m0
	s_mov_b32 m0, s68
	s_nop 2
	global_load_lds_dwordx4 v163, s[42:43]
	s_mov_b32 m0, s33
	s_addc_u32 s57, s43, 0
	s_mov_b32 s33, m0
	s_mov_b32 m0, s69
	s_nop 2
	global_load_lds_dwordx4 v1, s[56:57]
	s_mov_b32 m0, s33
	s_nop 0
	s_mov_b32 s33, m0
	s_mov_b32 m0, s76
	s_nop 2
	global_load_lds_dwordx4 v163, s[56:57]
	s_mov_b32 m0, s33
	s_nop 0
	s_mov_b32 s33, m0
	s_mov_b32 m0, s15
	s_nop 2
	global_load_lds_dwordx4 v168, s[54:55]
	s_mov_b32 m0, s33
	s_nop 0
	s_mov_b32 s33, m0
	s_mov_b32 m0, s79
	s_nop 2
	global_load_lds_dwordx4 v172, s[54:55]
	s_mov_b32 m0, s33
	s_waitcnt vmcnt(8) lgkmcnt(0)
	s_barrier
	s_setprio 1
	v_mfma_f32_16x16x128_f8f6f4 v[94:97], v[18:25], v[180:187], v[94:97]
	v_mfma_f32_16x16x128_f8f6f4 v[90:93], v[26:33], v[180:187], v[90:93]
	v_mfma_f32_16x16x128_f8f6f4 v[86:89], v[18:25], v[188:195], v[86:89]
	v_mfma_f32_16x16x128_f8f6f4 v[82:85], v[26:33], v[188:195], v[82:85]
	v_mfma_f32_16x16x128_f8f6f4 v[78:81], v[18:25], v[196:203], v[78:81]
	v_mfma_f32_16x16x128_f8f6f4 v[74:77], v[26:33], v[196:203], v[74:77]
	v_mfma_f32_16x16x128_f8f6f4 v[70:73], v[18:25], v[204:211], v[70:73]
	v_mfma_f32_16x16x128_f8f6f4 v[66:69], v[26:33], v[204:211], v[66:69]
	v_mfma_f32_16x16x128_f8f6f4 v[62:65], v[2:9], v[180:187], v[62:65]
	v_mfma_f32_16x16x128_f8f6f4 v[58:61], v[10:17], v[180:187], v[58:61]
	v_mfma_f32_16x16x128_f8f6f4 v[54:57], v[2:9], v[188:195], v[54:57]
	v_mfma_f32_16x16x128_f8f6f4 v[50:53], v[10:17], v[188:195], v[50:53]
	v_mfma_f32_16x16x128_f8f6f4 v[46:49], v[2:9], v[196:203], v[46:49]
	v_mfma_f32_16x16x128_f8f6f4 v[42:45], v[10:17], v[196:203], v[42:45]
	v_mfma_f32_16x16x128_f8f6f4 v[38:41], v[2:9], v[204:211], v[38:41]
	v_mfma_f32_16x16x128_f8f6f4 v[34:37], v[10:17], v[204:211], v[34:37]
	s_setprio 0
	s_barrier
.Lmid6:
	v_add_u32_e32 v14, 0x18000, v173
	v_add_u32_e32 v30, 0x1c000, v173
	ds_read_b128 v[2:5], v14
	ds_read_b128 v[6:9], v14 offset:1024
	ds_read_b128 v[10:13], v14 offset:2048
	ds_read_b128 v[14:17], v14 offset:3072
	ds_read_b128 v[18:21], v30
	ds_read_b128 v[22:25], v30 offset:1024
	ds_read_b128 v[26:29], v30 offset:2048
	ds_read_b128 v[30:33], v30 offset:3072
	ds_read_b128 v[180:183], v174 offset:32768
	ds_read_b128 v[184:187], v174 offset:33792
	ds_read_b128 v[188:191], v174 offset:34816
	ds_read_b128 v[192:195], v174 offset:35840
	ds_read_b128 v[196:199], v174 offset:36864
	ds_read_b128 v[200:203], v174 offset:37888
	ds_read_b128 v[204:207], v174 offset:38912
	ds_read_b128 v[208:211], v174 offset:39936
	s_mov_b32 s33, m0
	s_mov_b32 m0, s80
	s_nop 2
	global_load_lds_dwordx4 v169, s[54:55]
	s_mov_b32 m0, s33
	s_nop 0
	s_mov_b32 s33, m0
	s_mov_b32 m0, s81
	s_nop 2
	global_load_lds_dwordx4 v175, s[54:55]
	s_mov_b32 m0, s33
	s_waitcnt vmcnt(8) lgkmcnt(0)
	s_barrier
	s_setprio 1
	v_mfma_f32_16x16x128_f8f6f4 v[158:161], v[2:9], v[180:187], v[158:161]
	v_mfma_f32_16x16x128_f8f6f4 v[154:157], v[10:17], v[180:187], v[154:157]
	v_mfma_f32_16x16x128_f8f6f4 v[150:153], v[2:9], v[188:195], v[150:153]
	v_mfma_f32_16x16x128_f8f6f4 v[146:149], v[10:17], v[188:195], v[146:149]
	v_mfma_f32_16x16x128_f8f6f4 v[142:145], v[2:9], v[196:203], v[142:145]
	v_mfma_f32_16x16x128_f8f6f4 v[138:141], v[10:17], v[196:203], v[138:141]
	v_mfma_f32_16x16x128_f8f6f4 v[134:137], v[2:9], v[204:211], v[134:137]
	v_mfma_f32_16x16x128_f8f6f4 v[130:133], v[10:17], v[204:211], v[130:133]
	v_mfma_f32_16x16x128_f8f6f4 v[126:129], v[18:25], v[180:187], v[126:129]
	v_mfma_f32_16x16x128_f8f6f4 v[122:125], v[26:33], v[180:187], v[122:125]
	v_mfma_f32_16x16x128_f8f6f4 v[118:121], v[18:25], v[188:195], v[118:121]
	v_mfma_f32_16x16x128_f8f6f4 v[114:117], v[26:33], v[188:195], v[114:117]
	v_mfma_f32_16x16x128_f8f6f4 v[110:113], v[18:25], v[196:203], v[110:113]
	v_mfma_f32_16x16x128_f8f6f4 v[106:109], v[26:33], v[196:203], v[106:109]
	v_mfma_f32_16x16x128_f8f6f4 v[102:105], v[18:25], v[204:211], v[102:105]
	v_mfma_f32_16x16x128_f8f6f4 v[98:101], v[26:33], v[204:211], v[98:101]
	s_setprio 0
	s_barrier
	ds_read_b128 v[180:183], v174 offset:49152
	ds_read_b128 v[184:187], v174 offset:50176
	ds_read_b128 v[188:191], v174 offset:51200
	ds_read_b128 v[192:195], v174 offset:52224
	ds_read_b128 v[196:199], v174 offset:53248
	ds_read_b128 v[200:203], v174 offset:54272
	ds_read_b128 v[204:207], v174 offset:55296
	ds_read_b128 v[208:211], v174 offset:56320
	s_mov_b32 s33, m0
	s_mov_b32 m0, s84
	s_nop 2
	global_load_lds_dwordx4 v1, s[52:53]
	s_mov_b32 m0, s33
	s_add_u32 s42, s42, 0x20080
	s_mov_b32 s33, m0
	s_mov_b32 m0, s85
	s_nop 2
	global_load_lds_dwordx4 v163, s[52:53]
	s_mov_b32 m0, s33
	s_addc_u32 s43, s43, 0
	s_mov_b32 s33, m0
	s_mov_b32 m0, s91
	s_nop 2
	global_load_lds_dwordx4 v1, s[42:43]
	s_mov_b32 m0, s33
	s_nop 0
	s_mov_b32 s33, m0
	s_mov_b32 m0, s92
	s_nop 2
	global_load_lds_dwordx4 v163, s[42:43]
	s_mov_b32 m0, s33
	s_nop 0
	s_mov_b32 s33, m0
	s_mov_b32 m0, s86
	s_nop 2
	global_load_lds_dwordx4 v168, s[44:45]
	s_mov_b32 m0, s33
	s_nop 0
	s_mov_b32 s33, m0
	s_mov_b32 m0, s87
	s_nop 2
	global_load_lds_dwordx4 v172, s[44:45]
	s_mov_b32 m0, s33
	s_waitcnt vmcnt(8) lgkmcnt(0)
	s_barrier
	s_setprio 1
	v_mfma_f32_16x16x128_f8f6f4 v[94:97], v[2:9], v[180:187], v[94:97]
	v_mfma_f32_16x16x128_f8f6f4 v[90:93], v[10:17], v[180:187], v[90:93]
	v_mfma_f32_16x16x128_f8f6f4 v[86:89], v[2:9], v[188:195], v[86:89]
	v_mfma_f32_16x16x128_f8f6f4 v[82:85], v[10:17], v[188:195], v[82:85]
	v_mfma_f32_16x16x128_f8f6f4 v[78:81], v[2:9], v[196:203], v[78:81]
	v_mfma_f32_16x16x128_f8f6f4 v[74:77], v[10:17], v[196:203], v[74:77]
	v_mfma_f32_16x16x128_f8f6f4 v[70:73], v[2:9], v[204:211], v[70:73]
	v_mfma_f32_16x16x128_f8f6f4 v[66:69], v[10:17], v[204:211], v[66:69]
	v_mfma_f32_16x16x128_f8f6f4 v[62:65], v[18:25], v[180:187], v[62:65]
	v_mfma_f32_16x16x128_f8f6f4 v[58:61], v[26:33], v[180:187], v[58:61]
	v_mfma_f32_16x16x128_f8f6f4 v[54:57], v[18:25], v[188:195], v[54:57]
	v_mfma_f32_16x16x128_f8f6f4 v[50:53], v[26:33], v[188:195], v[50:53]
	v_mfma_f32_16x16x128_f8f6f4 v[46:49], v[18:25], v[196:203], v[46:49]
	v_mfma_f32_16x16x128_f8f6f4 v[42:45], v[26:33], v[196:203], v[42:45]
	v_mfma_f32_16x16x128_f8f6f4 v[38:41], v[18:25], v[204:211], v[38:41]
	v_mfma_f32_16x16x128_f8f6f4 v[34:37], v[26:33], v[204:211], v[34:37]
	s_setprio 0
	s_cmp_lt_i32 s9, 4
	s_cbranch_scc1 .Lkb6_do
	s_cmp_lg_u64 s[16:17], 0
	s_cbranch_scc0 .Lkb6_skip

.Lpeel6:
	s_add_u32 s33, s74, s40
	s_addc_u32 s44, s75, s41
	s_add_u32 s56, s33, 0x1d800080
	s_addc_u32 s57, s44, 0
	s_add_u32 s33, s33, 0x1d800100
	s_addc_u32 s52, s44, 0
	v_add_u32_e32 v2, 0x10000, v173
	v_add_u32_e32 v14, 0x14000, v173
	s_and_b64 s[44:45], s[42:43], exec
	ds_read_b128 v[18:21], v2
	ds_read_b128 v[22:25], v2 offset:1024
	ds_read_b128 v[26:29], v2 offset:2048
	ds_read_b128 v[30:33], v2 offset:3072
	ds_read_b128 v[2:5], v14
	ds_read_b128 v[6:9], v14 offset:1024
	ds_read_b128 v[10:13], v14 offset:2048
	ds_read_b128 v[14:17], v14 offset:3072
	s_cselect_b32 s55, s11, s52
	s_cselect_b32 s54, s10, s33
	s_add_u32 s33, s2, s40
	s_addc_u32 s44, s23, s41
	s_and_b64 s[42:43], s[42:43], exec
	s_cselect_b32 s43, s39, s44
	s_cselect_b32 s42, s38, s33
	s_add_u32 s44, s54, 0x80
	s_addc_u32 s45, s55, 0
	s_add_u32 s52, s42, 0x80
	s_addc_u32 s53, s43, 0
	ds_read_b128 v[180:183], v174
	ds_read_b128 v[184:187], v174 offset:1024
	ds_read_b128 v[188:191], v174 offset:2048
	ds_read_b128 v[192:195], v174 offset:3072
	ds_read_b128 v[196:199], v174 offset:4096
	ds_read_b128 v[200:203], v174 offset:5120
	ds_read_b128 v[204:207], v174 offset:6144
	ds_read_b128 v[208:211], v174 offset:7168
	s_mov_b32 s33, m0
	s_mov_b32 m0, s93
	s_nop 2
	global_load_lds_dwordx4 v178, s[56:57]
	s_mov_b32 m0, s33
	s_nop 0
	s_mov_b32 s33, m0
	s_mov_b32 m0, s94
	s_nop 2
	global_load_lds_dwordx4 v177, s[56:57]
	s_mov_b32 m0, s33
	s_waitcnt vmcnt(8) lgkmcnt(0)
	s_barrier
	s_setprio 1
	v_mfma_f32_16x16x128_f8f6f4 v[158:161], v[18:25], v[180:187], 0
	v_mfma_f32_16x16x128_f8f6f4 v[154:157], v[26:33], v[180:187], 0
	v_mfma_f32_16x16x128_f8f6f4 v[150:153], v[18:25], v[188:195], 0
	v_mfma_f32_16x16x128_f8f6f4 v[146:149], v[26:33], v[188:195], 0
	v_mfma_f32_16x16x128_f8f6f4 v[142:145], v[18:25], v[196:203], 0
	v_mfma_f32_16x16x128_f8f6f4 v[138:141], v[26:33], v[196:203], 0
	v_mfma_f32_16x16x128_f8f6f4 v[134:137], v[18:25], v[204:211], 0
	v_mfma_f32_16x16x128_f8f6f4 v[130:133], v[26:33], v[204:211], 0
	v_mfma_f32_16x16x128_f8f6f4 v[126:129], v[2:9], v[180:187], 0
	v_mfma_f32_16x16x128_f8f6f4 v[122:125], v[10:17], v[180:187], 0
	v_mfma_f32_16x16x128_f8f6f4 v[118:121], v[2:9], v[188:195], 0
	v_mfma_f32_16x16x128_f8f6f4 v[114:117], v[10:17], v[188:195], 0
	v_mfma_f32_16x16x128_f8f6f4 v[110:113], v[2:9], v[196:203], 0
	v_mfma_f32_16x16x128_f8f6f4 v[106:109], v[10:17], v[196:203], 0
	v_mfma_f32_16x16x128_f8f6f4 v[102:105], v[2:9], v[204:211], 0
	v_mfma_f32_16x16x128_f8f6f4 v[98:101], v[10:17], v[204:211], 0
	s_setprio 0
	s_barrier
	ds_read_b128 v[180:183], v174 offset:16384
	ds_read_b128 v[184:187], v174 offset:17408
	ds_read_b128 v[188:191], v174 offset:18432
	ds_read_b128 v[192:195], v174 offset:19456
	ds_read_b128 v[196:199], v174 offset:20480
	ds_read_b128 v[200:203], v174 offset:21504
	ds_read_b128 v[204:207], v174 offset:22528
	ds_read_b128 v[208:211], v174 offset:23552
	s_mov_b32 s33, m0
	s_mov_b32 m0, s67
	s_nop 2
	global_load_lds_dwordx4 v1, s[42:43]
	s_mov_b32 m0, s33
	s_add_u32 s56, s42, 0x20000
	s_mov_b32 s33, m0
	s_mov_b32 m0, s68
	s_nop 2
	global_load_lds_dwordx4 v163, s[42:43]
	s_mov_b32 m0, s33
	s_addc_u32 s57, s43, 0
	s_mov_b32 s33, m0
	s_mov_b32 m0, s69
	s_nop 2
	global_load_lds_dwordx4 v1, s[56:57]
	s_mov_b32 m0, s33
	s_nop 0
	s_mov_b32 s33, m0
	s_mov_b32 m0, s76
	s_nop 2
	global_load_lds_dwordx4 v163, s[56:57]
	s_mov_b32 m0, s33
	s_nop 0
	s_mov_b32 s33, m0
	s_mov_b32 m0, s15
	s_nop 2
	global_load_lds_dwordx4 v168, s[54:55]
	s_mov_b32 m0, s33
	s_nop 0
	s_mov_b32 s33, m0
	s_mov_b32 m0, s79
	s_nop 2
	global_load_lds_dwordx4 v172, s[54:55]
	s_mov_b32 m0, s33
	s_waitcnt vmcnt(8) lgkmcnt(0)
	s_barrier
	s_setprio 1
	v_mfma_f32_16x16x128_f8f6f4 v[94:97], v[18:25], v[180:187], 0
	v_mfma_f32_16x16x128_f8f6f4 v[90:93], v[26:33], v[180:187], 0
	v_mfma_f32_16x16x128_f8f6f4 v[86:89], v[18:25], v[188:195], 0
	v_mfma_f32_16x16x128_f8f6f4 v[82:85], v[26:33], v[188:195], 0
	v_mfma_f32_16x16x128_f8f6f4 v[78:81], v[18:25], v[196:203], 0
	v_mfma_f32_16x16x128_f8f6f4 v[74:77], v[26:33], v[196:203], 0
	v_mfma_f32_16x16x128_f8f6f4 v[70:73], v[18:25], v[204:211], 0
	v_mfma_f32_16x16x128_f8f6f4 v[66:69], v[26:33], v[204:211], 0
	v_mfma_f32_16x16x128_f8f6f4 v[62:65], v[2:9], v[180:187], 0
	v_mfma_f32_16x16x128_f8f6f4 v[58:61], v[10:17], v[180:187], 0
	v_mfma_f32_16x16x128_f8f6f4 v[54:57], v[2:9], v[188:195], 0
	v_mfma_f32_16x16x128_f8f6f4 v[50:53], v[10:17], v[188:195], 0
	v_mfma_f32_16x16x128_f8f6f4 v[46:49], v[2:9], v[196:203], 0
	v_mfma_f32_16x16x128_f8f6f4 v[42:45], v[10:17], v[196:203], 0
	v_mfma_f32_16x16x128_f8f6f4 v[38:41], v[2:9], v[204:211], 0
	v_mfma_f32_16x16x128_f8f6f4 v[34:37], v[10:17], v[204:211], 0
	s_setprio 0
	s_barrier
	s_branch .Lmid6

.LBB0_1943:
	s_add_u32 s54, s38, 0x80
	s_addc_u32 s55, s39, 0
	v_add_u32_e32 v2, 0x10000, v174
	v_add_u32_e32 v14, 0x14000, v174
	s_add_u32 s38, s38, 0x100
	ds_read_b128 v[18:21], v2
	ds_read_b128 v[22:25], v2 offset:1024
	ds_read_b128 v[26:29], v2 offset:2048
	ds_read_b128 v[30:33], v2 offset:3072
	ds_read_b128 v[2:5], v14
	ds_read_b128 v[6:9], v14 offset:1024
	ds_read_b128 v[10:13], v14 offset:2048
	ds_read_b128 v[14:17], v14 offset:3072
	s_addc_u32 s39, s39, 0
	s_and_b64 s[40:41], s[40:41], exec
	s_cselect_b32 s52, s10, s38
	s_cselect_b32 s53, s11, s39
	s_cselect_b32 s41, s1, s87
	s_cselect_b32 s40, s0, s86
	s_add_u32 s42, s52, 0x80
	s_addc_u32 s43, s53, 0
	s_add_u32 s44, s40, 0x80
	s_addc_u32 s45, s41, 0
	ds_read_b128 v[180:183], v175
	ds_read_b128 v[184:187], v175 offset:1024
	ds_read_b128 v[188:191], v175 offset:2048
	ds_read_b128 v[192:195], v175 offset:3072
	ds_read_b128 v[196:199], v175 offset:4096
	ds_read_b128 v[200:203], v175 offset:5120
	ds_read_b128 v[204:207], v175 offset:6144
	ds_read_b128 v[208:211], v175 offset:7168
	s_mov_b32 s33, m0
	s_mov_b32 m0, s78
	s_nop 2
	global_load_lds_dwordx4 v164, s[54:55]
	s_mov_b32 m0, s33
	s_nop 0
	s_mov_b32 s33, m0
	s_mov_b32 m0, s79
	s_nop 2
	global_load_lds_dwordx4 v166, s[54:55]
	s_mov_b32 m0, s33
	s_waitcnt vmcnt(8) lgkmcnt(0)
	s_barrier
	s_setprio 1
	v_mfma_f32_16x16x128_f8f6f4 v[158:161], v[18:25], v[180:187], v[158:161]
	v_mfma_f32_16x16x128_f8f6f4 v[150:153], v[26:33], v[180:187], v[150:153]
	v_mfma_f32_16x16x128_f8f6f4 v[142:145], v[18:25], v[188:195], v[142:145]
	v_mfma_f32_16x16x128_f8f6f4 v[134:137], v[26:33], v[188:195], v[134:137]
	v_mfma_f32_16x16x128_f8f6f4 v[126:129], v[18:25], v[196:203], v[126:129]
	v_mfma_f32_16x16x128_f8f6f4 v[118:121], v[26:33], v[196:203], v[118:121]
	v_mfma_f32_16x16x128_f8f6f4 v[110:113], v[18:25], v[204:211], v[110:113]
	v_mfma_f32_16x16x128_f8f6f4 v[102:105], v[26:33], v[204:211], v[102:105]
	v_mfma_f32_16x16x128_f8f6f4 v[154:157], v[2:9], v[180:187], v[154:157]
	v_mfma_f32_16x16x128_f8f6f4 v[146:149], v[10:17], v[180:187], v[146:149]
	v_mfma_f32_16x16x128_f8f6f4 v[138:141], v[2:9], v[188:195], v[138:141]
	v_mfma_f32_16x16x128_f8f6f4 v[130:133], v[10:17], v[188:195], v[130:133]
	v_mfma_f32_16x16x128_f8f6f4 v[122:125], v[2:9], v[196:203], v[122:125]
	v_mfma_f32_16x16x128_f8f6f4 v[114:117], v[10:17], v[196:203], v[114:117]
	v_mfma_f32_16x16x128_f8f6f4 v[106:109], v[2:9], v[204:211], v[106:109]
	v_mfma_f32_16x16x128_f8f6f4 v[98:101], v[10:17], v[204:211], v[98:101]
	s_setprio 0
	s_barrier
	ds_read_b128 v[180:183], v175 offset:16384
	ds_read_b128 v[184:187], v175 offset:17408
	ds_read_b128 v[188:191], v175 offset:18432
	ds_read_b128 v[192:195], v175 offset:19456
	ds_read_b128 v[196:199], v175 offset:20480
	ds_read_b128 v[200:203], v175 offset:21504
	ds_read_b128 v[204:207], v175 offset:22528
	ds_read_b128 v[208:211], v175 offset:23552
	s_mov_b32 s33, m0
	s_mov_b32 m0, s34
	s_nop 2
	global_load_lds_dwordx4 v165, s[40:41]
	s_mov_b32 m0, s33
	s_add_u32 s54, s40, 0x20000
	s_mov_b32 s33, m0
	s_mov_b32 m0, s35
	s_nop 2
	global_load_lds_dwordx4 v167, s[40:41]
	s_mov_b32 m0, s33
	s_addc_u32 s55, s41, 0
	s_mov_b32 s33, m0
	s_mov_b32 m0, s36
	s_nop 2
	global_load_lds_dwordx4 v165, s[54:55]
	s_mov_b32 m0, s33
	s_nop 0
	s_mov_b32 s33, m0
	s_mov_b32 m0, s37
	s_nop 2
	global_load_lds_dwordx4 v167, s[54:55]
	s_mov_b32 m0, s33
	s_nop 0
	s_mov_b32 s33, m0
	s_mov_b32 m0, s31
	s_nop 2
	global_load_lds_dwordx4 v171, s[52:53]
	s_mov_b32 m0, s33
	s_nop 0
	s_mov_b32 s33, m0
	s_mov_b32 m0, s56
	s_nop 2
	global_load_lds_dwordx4 v173, s[52:53]
	s_mov_b32 m0, s33
	s_waitcnt vmcnt(8) lgkmcnt(0)
	s_barrier
	s_setprio 1
	v_mfma_f32_16x16x128_f8f6f4 v[94:97], v[18:25], v[180:187], v[94:97]
	v_mfma_f32_16x16x128_f8f6f4 v[86:89], v[26:33], v[180:187], v[86:89]
	v_mfma_f32_16x16x128_f8f6f4 v[78:81], v[18:25], v[188:195], v[78:81]
	v_mfma_f32_16x16x128_f8f6f4 v[70:73], v[26:33], v[188:195], v[70:73]
	v_mfma_f32_16x16x128_f8f6f4 v[62:65], v[18:25], v[196:203], v[62:65]
	v_mfma_f32_16x16x128_f8f6f4 v[54:57], v[26:33], v[196:203], v[54:57]
	v_mfma_f32_16x16x128_f8f6f4 v[46:49], v[18:25], v[204:211], v[46:49]
	v_mfma_f32_16x16x128_f8f6f4 v[38:41], v[26:33], v[204:211], v[38:41]
	v_mfma_f32_16x16x128_f8f6f4 v[90:93], v[2:9], v[180:187], v[90:93]
	v_mfma_f32_16x16x128_f8f6f4 v[82:85], v[10:17], v[180:187], v[82:85]
	v_mfma_f32_16x16x128_f8f6f4 v[74:77], v[2:9], v[188:195], v[74:77]
	v_mfma_f32_16x16x128_f8f6f4 v[66:69], v[10:17], v[188:195], v[66:69]
	v_mfma_f32_16x16x128_f8f6f4 v[58:61], v[2:9], v[196:203], v[58:61]
	v_mfma_f32_16x16x128_f8f6f4 v[50:53], v[10:17], v[196:203], v[50:53]
	v_mfma_f32_16x16x128_f8f6f4 v[42:45], v[2:9], v[204:211], v[42:45]
	v_mfma_f32_16x16x128_f8f6f4 v[34:37], v[10:17], v[204:211], v[34:37]
	s_setprio 0
	s_barrier
	v_add_u32_e32 v14, 0x18000, v174
	v_add_u32_e32 v30, 0x1c000, v174
	ds_read_b128 v[2:5], v14
	ds_read_b128 v[6:9], v14 offset:1024
	ds_read_b128 v[10:13], v14 offset:2048
	ds_read_b128 v[14:17], v14 offset:3072
	ds_read_b128 v[18:21], v30
	ds_read_b128 v[22:25], v30 offset:1024
	ds_read_b128 v[26:29], v30 offset:2048
	ds_read_b128 v[30:33], v30 offset:3072
	ds_read_b128 v[180:183], v175 offset:32768
	ds_read_b128 v[184:187], v175 offset:33792
	ds_read_b128 v[188:191], v175 offset:34816
	ds_read_b128 v[192:195], v175 offset:35840
	ds_read_b128 v[196:199], v175 offset:36864
	ds_read_b128 v[200:203], v175 offset:37888
	ds_read_b128 v[204:207], v175 offset:38912
	ds_read_b128 v[208:211], v175 offset:39936
	s_mov_b32 s33, m0
	s_mov_b32 m0, s57
	s_nop 2
	global_load_lds_dwordx4 v177, s[52:53]
	s_mov_b32 m0, s33
	s_nop 0
	s_mov_b32 s33, m0
	s_mov_b32 m0, s63
	s_nop 2
	global_load_lds_dwordx4 v178, s[52:53]
	s_mov_b32 m0, s33
	s_waitcnt vmcnt(8) lgkmcnt(0)
	s_barrier
	s_setprio 1
	v_mfma_f32_16x16x128_f8f6f4 v[158:161], v[2:9], v[180:187], v[158:161]
	v_mfma_f32_16x16x128_f8f6f4 v[150:153], v[10:17], v[180:187], v[150:153]
	v_mfma_f32_16x16x128_f8f6f4 v[142:145], v[2:9], v[188:195], v[142:145]
	v_mfma_f32_16x16x128_f8f6f4 v[134:137], v[10:17], v[188:195], v[134:137]
	v_mfma_f32_16x16x128_f8f6f4 v[126:129], v[2:9], v[196:203], v[126:129]
	v_mfma_f32_16x16x128_f8f6f4 v[118:121], v[10:17], v[196:203], v[118:121]
	v_mfma_f32_16x16x128_f8f6f4 v[110:113], v[2:9], v[204:211], v[110:113]
	v_mfma_f32_16x16x128_f8f6f4 v[102:105], v[10:17], v[204:211], v[102:105]
	v_mfma_f32_16x16x128_f8f6f4 v[154:157], v[18:25], v[180:187], v[154:157]
	v_mfma_f32_16x16x128_f8f6f4 v[146:149], v[26:33], v[180:187], v[146:149]
	v_mfma_f32_16x16x128_f8f6f4 v[138:141], v[18:25], v[188:195], v[138:141]
	v_mfma_f32_16x16x128_f8f6f4 v[130:133], v[26:33], v[188:195], v[130:133]
	v_mfma_f32_16x16x128_f8f6f4 v[122:125], v[18:25], v[196:203], v[122:125]
	v_mfma_f32_16x16x128_f8f6f4 v[114:117], v[26:33], v[196:203], v[114:117]
	v_mfma_f32_16x16x128_f8f6f4 v[106:109], v[18:25], v[204:211], v[106:109]
	v_mfma_f32_16x16x128_f8f6f4 v[98:101], v[26:33], v[204:211], v[98:101]
	s_setprio 0
	s_barrier
	ds_read_b128 v[180:183], v175 offset:49152
	ds_read_b128 v[184:187], v175 offset:50176
	ds_read_b128 v[188:191], v175 offset:51200
	ds_read_b128 v[192:195], v175 offset:52224
	ds_read_b128 v[196:199], v175 offset:53248
	ds_read_b128 v[200:203], v175 offset:54272
	ds_read_b128 v[204:207], v175 offset:55296
	ds_read_b128 v[208:211], v175 offset:56320
	s_mov_b32 s33, m0
	s_mov_b32 m0, s66
	s_nop 2
	global_load_lds_dwordx4 v165, s[44:45]
	s_mov_b32 m0, s33
	s_add_u32 s40, s40, 0x20080
	s_mov_b32 s33, m0
	s_mov_b32 m0, s67
	s_nop 2
	global_load_lds_dwordx4 v167, s[44:45]
	s_mov_b32 m0, s33
	s_addc_u32 s41, s41, 0
	s_mov_b32 s33, m0
	s_mov_b32 m0, s76
	s_nop 2
	global_load_lds_dwordx4 v165, s[40:41]
	s_mov_b32 m0, s33
	s_nop 0
	s_mov_b32 s33, m0
	s_mov_b32 m0, s77
	s_nop 2
	global_load_lds_dwordx4 v167, s[40:41]
	s_mov_b32 m0, s33
	s_nop 0
	s_mov_b32 s33, m0
	s_mov_b32 m0, s68
	s_nop 2
	global_load_lds_dwordx4 v171, s[42:43]
	s_mov_b32 m0, s33
	s_nop 0
	s_mov_b32 s33, m0
	s_mov_b32 m0, s69
	s_nop 2
	global_load_lds_dwordx4 v173, s[42:43]
	s_mov_b32 m0, s33
	s_waitcnt vmcnt(8) lgkmcnt(0)
	s_barrier
	s_setprio 1
	v_mfma_f32_16x16x128_f8f6f4 v[94:97], v[2:9], v[180:187], v[94:97]
	v_mfma_f32_16x16x128_f8f6f4 v[86:89], v[10:17], v[180:187], v[86:89]
	v_mfma_f32_16x16x128_f8f6f4 v[78:81], v[2:9], v[188:195], v[78:81]
	v_mfma_f32_16x16x128_f8f6f4 v[70:73], v[10:17], v[188:195], v[70:73]
	v_mfma_f32_16x16x128_f8f6f4 v[62:65], v[2:9], v[196:203], v[62:65]
	v_mfma_f32_16x16x128_f8f6f4 v[54:57], v[10:17], v[196:203], v[54:57]
	v_mfma_f32_16x16x128_f8f6f4 v[46:49], v[2:9], v[204:211], v[46:49]
	v_mfma_f32_16x16x128_f8f6f4 v[38:41], v[10:17], v[204:211], v[38:41]
	v_mfma_f32_16x16x128_f8f6f4 v[90:93], v[18:25], v[180:187], v[90:93]
	v_mfma_f32_16x16x128_f8f6f4 v[82:85], v[26:33], v[180:187], v[82:85]
	v_mfma_f32_16x16x128_f8f6f4 v[74:77], v[18:25], v[188:195], v[74:77]
	v_mfma_f32_16x16x128_f8f6f4 v[66:69], v[26:33], v[188:195], v[66:69]
	v_mfma_f32_16x16x128_f8f6f4 v[58:61], v[18:25], v[196:203], v[58:61]
	v_mfma_f32_16x16x128_f8f6f4 v[50:53], v[26:33], v[196:203], v[50:53]
	v_mfma_f32_16x16x128_f8f6f4 v[42:45], v[18:25], v[204:211], v[42:45]
	v_mfma_f32_16x16x128_f8f6f4 v[34:37], v[26:33], v[204:211], v[34:37]
	s_setprio 0
	s_barrier
	s_add_i32 s88, s88, 2
	s_add_u32 s86, s86, 0x100
	s_addc_u32 s87, s87, 0
	s_cmp_gt_u32 s88, 5
	s_cbranch_scc1 .LBB0_1957

.LBB0_2092:
	s_cmp_eq_u32 s91, 0
	s_cbranch_scc1 .Lpeel7
	s_lshl_b32 s33, s91, 7
	s_add_u32 s52, s36, s33
	s_addc_u32 s53, s37, 0
	s_add_u32 s46, s52, 0x100
	s_addc_u32 s47, s53, 0
	s_and_b64 s[44:45], s[42:43], exec
	s_cselect_b32 s49, s15, s47
	s_cselect_b32 s48, s17, s46
	s_add_u32 s33, s26, s33
	v_add_u32_e32 v2, 0x10000, v171
	v_add_u32_e32 v14, 0x14000, v171
	s_addc_u32 s44, s27, 0
	ds_read_b128 v[18:21], v2
	ds_read_b128 v[22:25], v2 offset:1024
	ds_read_b128 v[26:29], v2 offset:2048
	ds_read_b128 v[30:33], v2 offset:3072
	ds_read_b128 v[2:5], v14
	ds_read_b128 v[6:9], v14 offset:1024
	ds_read_b128 v[10:13], v14 offset:2048
	ds_read_b128 v[14:17], v14 offset:3072
	s_add_u32 s33, s33, 0x100
	s_addc_u32 s44, s44, 0
	s_and_b64 s[42:43], s[42:43], exec
	s_cselect_b32 s43, s19, s44
	s_cselect_b32 s42, s18, s33
	s_add_u32 s44, s48, 0x80
	s_addc_u32 s45, s49, 0
	s_add_u32 s46, s42, 0x80
	s_addc_u32 s47, s43, 0
	ds_read_b128 v[176:179], v172
	ds_read_b128 v[180:183], v172 offset:1024
	ds_read_b128 v[184:187], v172 offset:2048
	ds_read_b128 v[188:191], v172 offset:3072
	ds_read_b128 v[192:195], v172 offset:4096
	ds_read_b128 v[196:199], v172 offset:5120
	ds_read_b128 v[200:203], v172 offset:6144
	ds_read_b128 v[204:207], v172 offset:7168
	s_add_u32 s52, s52, 0x20080
	s_addc_u32 s53, s53, 0
	s_mov_b32 s33, m0
	s_mov_b32 m0, s79
	s_nop 2
	global_load_lds_dwordx4 v163, s[52:53]
	s_mov_b32 m0, s33
	s_nop 0
	s_mov_b32 s33, m0
	s_mov_b32 m0, s80
	s_nop 2
	global_load_lds_dwordx4 v164, s[52:53]
	s_mov_b32 m0, s33
	s_waitcnt vmcnt(8) lgkmcnt(0)
	s_barrier
	s_setprio 1
	v_mfma_f32_16x16x128_f8f6f4 v[158:161], v[18:25], v[176:183], v[158:161]
	v_mfma_f32_16x16x128_f8f6f4 v[154:157], v[26:33], v[176:183], v[154:157]
	v_mfma_f32_16x16x128_f8f6f4 v[142:145], v[18:25], v[184:191], v[142:145]
	v_mfma_f32_16x16x128_f8f6f4 v[138:141], v[26:33], v[184:191], v[138:141]
	v_mfma_f32_16x16x128_f8f6f4 v[126:129], v[18:25], v[192:199], v[126:129]
	v_mfma_f32_16x16x128_f8f6f4 v[122:125], v[26:33], v[192:199], v[122:125]
	v_mfma_f32_16x16x128_f8f6f4 v[110:113], v[18:25], v[200:207], v[110:113]
	v_mfma_f32_16x16x128_f8f6f4 v[106:109], v[26:33], v[200:207], v[106:109]
	v_mfma_f32_16x16x128_f8f6f4 v[150:153], v[2:9], v[176:183], v[150:153]
	v_mfma_f32_16x16x128_f8f6f4 v[146:149], v[10:17], v[176:183], v[146:149]
	v_mfma_f32_16x16x128_f8f6f4 v[134:137], v[2:9], v[184:191], v[134:137]
	v_mfma_f32_16x16x128_f8f6f4 v[130:133], v[10:17], v[184:191], v[130:133]
	v_mfma_f32_16x16x128_f8f6f4 v[118:121], v[2:9], v[192:199], v[118:121]
	v_mfma_f32_16x16x128_f8f6f4 v[114:117], v[10:17], v[192:199], v[114:117]
	v_mfma_f32_16x16x128_f8f6f4 v[102:105], v[2:9], v[200:207], v[102:105]
	v_mfma_f32_16x16x128_f8f6f4 v[98:101], v[10:17], v[200:207], v[98:101]
	s_setprio 0
	s_barrier
	ds_read_b128 v[176:179], v172 offset:16384
	ds_read_b128 v[180:183], v172 offset:17408
	ds_read_b128 v[184:187], v172 offset:18432
	ds_read_b128 v[188:191], v172 offset:19456
	ds_read_b128 v[192:195], v172 offset:20480
	ds_read_b128 v[196:199], v172 offset:21504
	ds_read_b128 v[200:203], v172 offset:22528
	ds_read_b128 v[204:207], v172 offset:23552
	s_mov_b32 s33, m0
	s_mov_b32 m0, s64
	s_nop 2
	global_load_lds_dwordx4 v1, s[42:43]
	s_mov_b32 m0, s33
	s_add_u32 s52, s42, 0x20000
	s_mov_b32 s33, m0
	s_mov_b32 m0, s65
	s_nop 2
	global_load_lds_dwordx4 v162, s[42:43]
	s_mov_b32 m0, s33
	s_addc_u32 s53, s43, 0
	s_mov_b32 s33, m0
	s_mov_b32 m0, s24
	s_nop 2
	global_load_lds_dwordx4 v1, s[52:53]
	s_mov_b32 m0, s33
	s_nop 0
	s_mov_b32 s33, m0
	s_mov_b32 m0, s25
	s_nop 2
	global_load_lds_dwordx4 v162, s[52:53]
	s_mov_b32 m0, s33
	s_nop 0
	s_mov_b32 s33, m0
	s_mov_b32 m0, s63
	s_nop 2
	global_load_lds_dwordx4 v163, s[48:49]
	s_mov_b32 m0, s33
	s_nop 0
	s_mov_b32 s33, m0
	s_mov_b32 m0, s2
	s_nop 2
	global_load_lds_dwordx4 v164, s[48:49]
	s_mov_b32 m0, s33
	s_waitcnt vmcnt(8) lgkmcnt(0)
	s_barrier
	s_setprio 1
	v_mfma_f32_16x16x128_f8f6f4 v[94:97], v[18:25], v[176:183], v[94:97]
	v_mfma_f32_16x16x128_f8f6f4 v[90:93], v[26:33], v[176:183], v[90:93]
	v_mfma_f32_16x16x128_f8f6f4 v[78:81], v[18:25], v[184:191], v[78:81]
	v_mfma_f32_16x16x128_f8f6f4 v[74:77], v[26:33], v[184:191], v[74:77]
	v_mfma_f32_16x16x128_f8f6f4 v[62:65], v[18:25], v[192:199], v[62:65]
	v_mfma_f32_16x16x128_f8f6f4 v[58:61], v[26:33], v[192:199], v[58:61]
	v_mfma_f32_16x16x128_f8f6f4 v[46:49], v[18:25], v[200:207], v[46:49]
	v_mfma_f32_16x16x128_f8f6f4 v[42:45], v[26:33], v[200:207], v[42:45]
	v_mfma_f32_16x16x128_f8f6f4 v[86:89], v[2:9], v[176:183], v[86:89]
	v_mfma_f32_16x16x128_f8f6f4 v[82:85], v[10:17], v[176:183], v[82:85]
	v_mfma_f32_16x16x128_f8f6f4 v[70:73], v[2:9], v[184:191], v[70:73]
	v_mfma_f32_16x16x128_f8f6f4 v[66:69], v[10:17], v[184:191], v[66:69]
	v_mfma_f32_16x16x128_f8f6f4 v[54:57], v[2:9], v[192:199], v[54:57]
	v_mfma_f32_16x16x128_f8f6f4 v[50:53], v[10:17], v[192:199], v[50:53]
	v_mfma_f32_16x16x128_f8f6f4 v[38:41], v[2:9], v[200:207], v[38:41]
	v_mfma_f32_16x16x128_f8f6f4 v[34:37], v[10:17], v[200:207], v[34:37]
	s_setprio 0
	s_barrier
.Lmid7:
	v_add_u32_e32 v14, 0x18000, v171
	v_add_u32_e32 v30, 0x1c000, v171
	ds_read_b128 v[2:5], v14
	ds_read_b128 v[6:9], v14 offset:1024
	ds_read_b128 v[10:13], v14 offset:2048
	ds_read_b128 v[14:17], v14 offset:3072
	ds_read_b128 v[18:21], v30
	ds_read_b128 v[22:25], v30 offset:1024
	ds_read_b128 v[26:29], v30 offset:2048
	ds_read_b128 v[30:33], v30 offset:3072
	ds_read_b128 v[176:179], v172 offset:32768
	ds_read_b128 v[180:183], v172 offset:33792
	ds_read_b128 v[184:187], v172 offset:34816
	ds_read_b128 v[188:191], v172 offset:35840
	ds_read_b128 v[192:195], v172 offset:36864
	ds_read_b128 v[196:199], v172 offset:37888
	ds_read_b128 v[200:203], v172 offset:38912
	ds_read_b128 v[204:207], v172 offset:39936
	s_add_u32 s48, s48, 0x20000
	s_addc_u32 s49, s49, 0
	s_mov_b32 s33, m0
	s_mov_b32 m0, s23
	s_nop 2
	global_load_lds_dwordx4 v163, s[48:49]
	s_mov_b32 m0, s33
	s_nop 0
	s_mov_b32 s33, m0
	s_mov_b32 m0, s28
	s_nop 2
	global_load_lds_dwordx4 v164, s[48:49]
	s_mov_b32 m0, s33
	s_waitcnt vmcnt(8) lgkmcnt(0)
	s_barrier
	s_setprio 1
	v_mfma_f32_16x16x128_f8f6f4 v[158:161], v[2:9], v[176:183], v[158:161]
	v_mfma_f32_16x16x128_f8f6f4 v[154:157], v[10:17], v[176:183], v[154:157]
	v_mfma_f32_16x16x128_f8f6f4 v[142:145], v[2:9], v[184:191], v[142:145]
	v_mfma_f32_16x16x128_f8f6f4 v[138:141], v[10:17], v[184:191], v[138:141]
	v_mfma_f32_16x16x128_f8f6f4 v[126:129], v[2:9], v[192:199], v[126:129]
	v_mfma_f32_16x16x128_f8f6f4 v[122:125], v[10:17], v[192:199], v[122:125]
	v_mfma_f32_16x16x128_f8f6f4 v[110:113], v[2:9], v[200:207], v[110:113]
	v_mfma_f32_16x16x128_f8f6f4 v[106:109], v[10:17], v[200:207], v[106:109]
	v_mfma_f32_16x16x128_f8f6f4 v[150:153], v[18:25], v[176:183], v[150:153]
	v_mfma_f32_16x16x128_f8f6f4 v[146:149], v[26:33], v[176:183], v[146:149]
	v_mfma_f32_16x16x128_f8f6f4 v[134:137], v[18:25], v[184:191], v[134:137]
	v_mfma_f32_16x16x128_f8f6f4 v[130:133], v[26:33], v[184:191], v[130:133]
	v_mfma_f32_16x16x128_f8f6f4 v[118:121], v[18:25], v[192:199], v[118:121]
	v_mfma_f32_16x16x128_f8f6f4 v[114:117], v[26:33], v[192:199], v[114:117]
	v_mfma_f32_16x16x128_f8f6f4 v[102:105], v[18:25], v[200:207], v[102:105]
	v_mfma_f32_16x16x128_f8f6f4 v[98:101], v[26:33], v[200:207], v[98:101]
	s_setprio 0
	s_barrier
	ds_read_b128 v[176:179], v172 offset:49152
	ds_read_b128 v[180:183], v172 offset:50176
	ds_read_b128 v[184:187], v172 offset:51200
	ds_read_b128 v[188:191], v172 offset:52224
	ds_read_b128 v[192:195], v172 offset:53248
	ds_read_b128 v[196:199], v172 offset:54272
	ds_read_b128 v[200:203], v172 offset:55296
	ds_read_b128 v[204:207], v172 offset:56320
	s_mov_b32 s33, m0
	s_mov_b32 m0, s67
	s_nop 2
	global_load_lds_dwordx4 v1, s[46:47]
	s_mov_b32 m0, s33
	s_add_u32 s42, s42, 0x20080
	s_mov_b32 s33, m0
	s_mov_b32 m0, s68
	s_nop 2
	global_load_lds_dwordx4 v162, s[46:47]
	s_mov_b32 m0, s33
	s_addc_u32 s43, s43, 0
	s_mov_b32 s33, m0
	s_mov_b32 m0, s77
	s_nop 2
	global_load_lds_dwordx4 v1, s[42:43]
	s_mov_b32 m0, s33
	s_nop 0
	s_mov_b32 s33, m0
	s_mov_b32 m0, s78
	s_nop 2
	global_load_lds_dwordx4 v162, s[42:43]
	s_mov_b32 m0, s33
	s_nop 0
	s_mov_b32 s33, m0
	s_mov_b32 m0, s69
	s_nop 2
	global_load_lds_dwordx4 v163, s[44:45]
	s_mov_b32 m0, s33
	s_nop 0
	s_mov_b32 s33, m0
	s_mov_b32 m0, s76
	s_nop 2
	global_load_lds_dwordx4 v164, s[44:45]
	s_mov_b32 m0, s33
	s_waitcnt vmcnt(8) lgkmcnt(0)
	s_barrier
	s_setprio 1
	v_mfma_f32_16x16x128_f8f6f4 v[94:97], v[2:9], v[176:183], v[94:97]
	v_mfma_f32_16x16x128_f8f6f4 v[90:93], v[10:17], v[176:183], v[90:93]
	v_mfma_f32_16x16x128_f8f6f4 v[78:81], v[2:9], v[184:191], v[78:81]
	v_mfma_f32_16x16x128_f8f6f4 v[74:77], v[10:17], v[184:191], v[74:77]
	v_mfma_f32_16x16x128_f8f6f4 v[62:65], v[2:9], v[192:199], v[62:65]
	v_mfma_f32_16x16x128_f8f6f4 v[58:61], v[10:17], v[192:199], v[58:61]
	v_mfma_f32_16x16x128_f8f6f4 v[46:49], v[2:9], v[200:207], v[46:49]
	v_mfma_f32_16x16x128_f8f6f4 v[42:45], v[10:17], v[200:207], v[42:45]
	v_mfma_f32_16x16x128_f8f6f4 v[86:89], v[18:25], v[176:183], v[86:89]
	v_mfma_f32_16x16x128_f8f6f4 v[82:85], v[26:33], v[176:183], v[82:85]
	v_mfma_f32_16x16x128_f8f6f4 v[70:73], v[18:25], v[184:191], v[70:73]
	v_mfma_f32_16x16x128_f8f6f4 v[66:69], v[26:33], v[184:191], v[66:69]
	v_mfma_f32_16x16x128_f8f6f4 v[54:57], v[18:25], v[192:199], v[54:57]
	v_mfma_f32_16x16x128_f8f6f4 v[50:53], v[26:33], v[192:199], v[50:53]
	v_mfma_f32_16x16x128_f8f6f4 v[38:41], v[18:25], v[200:207], v[38:41]
	v_mfma_f32_16x16x128_f8f6f4 v[34:37], v[26:33], v[200:207], v[34:37]
	s_setprio 0
	s_cmp_lt_u32 s91, 6
	s_cbranch_scc1 .Lkb7_do
	s_cmp_lg_u64 s[12:13], 0
	s_cbranch_scc0 .Lkb7_skip

.Lpeel7:
	s_lshl_b32 s33, s91, 7
	s_add_u32 s52, s36, s33
	s_addc_u32 s53, s37, 0
	s_add_u32 s46, s52, 0x100
	s_addc_u32 s47, s53, 0
	s_and_b64 s[44:45], s[42:43], exec
	s_cselect_b32 s49, s15, s47
	s_cselect_b32 s48, s17, s46
	s_add_u32 s33, s26, s33
	v_add_u32_e32 v2, 0x10000, v171
	v_add_u32_e32 v14, 0x14000, v171
	s_addc_u32 s44, s27, 0
	ds_read_b128 v[18:21], v2
	ds_read_b128 v[22:25], v2 offset:1024
	ds_read_b128 v[26:29], v2 offset:2048
	ds_read_b128 v[30:33], v2 offset:3072
	ds_read_b128 v[2:5], v14
	ds_read_b128 v[6:9], v14 offset:1024
	ds_read_b128 v[10:13], v14 offset:2048
	ds_read_b128 v[14:17], v14 offset:3072
	s_add_u32 s33, s33, 0x100
	s_addc_u32 s44, s44, 0
	s_and_b64 s[42:43], s[42:43], exec
	s_cselect_b32 s43, s19, s44
	s_cselect_b32 s42, s18, s33
	s_add_u32 s44, s48, 0x80
	s_addc_u32 s45, s49, 0
	s_add_u32 s46, s42, 0x80
	s_addc_u32 s47, s43, 0
	ds_read_b128 v[176:179], v172
	ds_read_b128 v[180:183], v172 offset:1024
	ds_read_b128 v[184:187], v172 offset:2048
	ds_read_b128 v[188:191], v172 offset:3072
	ds_read_b128 v[192:195], v172 offset:4096
	ds_read_b128 v[196:199], v172 offset:5120
	ds_read_b128 v[200:203], v172 offset:6144
	ds_read_b128 v[204:207], v172 offset:7168
	s_add_u32 s52, s52, 0x20080
	s_addc_u32 s53, s53, 0
	s_mov_b32 s33, m0
	s_mov_b32 m0, s79
	s_nop 2
	global_load_lds_dwordx4 v163, s[52:53]
	s_mov_b32 m0, s33
	s_nop 0
	s_mov_b32 s33, m0
	s_mov_b32 m0, s80
	s_nop 2
	global_load_lds_dwordx4 v164, s[52:53]
	s_mov_b32 m0, s33
	s_waitcnt vmcnt(8) lgkmcnt(0)
	s_barrier
	s_setprio 1
	v_mfma_f32_16x16x128_f8f6f4 v[158:161], v[18:25], v[176:183], 0
	v_mfma_f32_16x16x128_f8f6f4 v[154:157], v[26:33], v[176:183], 0
	v_mfma_f32_16x16x128_f8f6f4 v[142:145], v[18:25], v[184:191], 0
	v_mfma_f32_16x16x128_f8f6f4 v[138:141], v[26:33], v[184:191], 0
	v_mfma_f32_16x16x128_f8f6f4 v[126:129], v[18:25], v[192:199], 0
	v_mfma_f32_16x16x128_f8f6f4 v[122:125], v[26:33], v[192:199], 0
	v_mfma_f32_16x16x128_f8f6f4 v[110:113], v[18:25], v[200:207], 0
	v_mfma_f32_16x16x128_f8f6f4 v[106:109], v[26:33], v[200:207], 0
	v_mfma_f32_16x16x128_f8f6f4 v[150:153], v[2:9], v[176:183], 0
	v_mfma_f32_16x16x128_f8f6f4 v[146:149], v[10:17], v[176:183], 0
	v_mfma_f32_16x16x128_f8f6f4 v[134:137], v[2:9], v[184:191], 0
	v_mfma_f32_16x16x128_f8f6f4 v[130:133], v[10:17], v[184:191], 0
	v_mfma_f32_16x16x128_f8f6f4 v[118:121], v[2:9], v[192:199], 0
	v_mfma_f32_16x16x128_f8f6f4 v[114:117], v[10:17], v[192:199], 0
	v_mfma_f32_16x16x128_f8f6f4 v[102:105], v[2:9], v[200:207], 0
	v_mfma_f32_16x16x128_f8f6f4 v[98:101], v[10:17], v[200:207], 0
	s_setprio 0
	s_barrier
	ds_read_b128 v[176:179], v172 offset:16384
	ds_read_b128 v[180:183], v172 offset:17408
	ds_read_b128 v[184:187], v172 offset:18432
	ds_read_b128 v[188:191], v172 offset:19456
	ds_read_b128 v[192:195], v172 offset:20480
	ds_read_b128 v[196:199], v172 offset:21504
	ds_read_b128 v[200:203], v172 offset:22528
	ds_read_b128 v[204:207], v172 offset:23552
	s_mov_b32 s33, m0
	s_mov_b32 m0, s64
	s_nop 2
	global_load_lds_dwordx4 v1, s[42:43]
	s_mov_b32 m0, s33
	s_add_u32 s52, s42, 0x20000
	s_mov_b32 s33, m0
	s_mov_b32 m0, s65
	s_nop 2
	global_load_lds_dwordx4 v162, s[42:43]
	s_mov_b32 m0, s33
	s_addc_u32 s53, s43, 0
	s_mov_b32 s33, m0
	s_mov_b32 m0, s24
	s_nop 2
	global_load_lds_dwordx4 v1, s[52:53]
	s_mov_b32 m0, s33
	s_nop 0
	s_mov_b32 s33, m0
	s_mov_b32 m0, s25
	s_nop 2
	global_load_lds_dwordx4 v162, s[52:53]
	s_mov_b32 m0, s33
	s_nop 0
	s_mov_b32 s33, m0
	s_mov_b32 m0, s63
	s_nop 2
	global_load_lds_dwordx4 v163, s[48:49]
	s_mov_b32 m0, s33
	s_nop 0
	s_mov_b32 s33, m0
	s_mov_b32 m0, s2
	s_nop 2
	global_load_lds_dwordx4 v164, s[48:49]
	s_mov_b32 m0, s33
	s_waitcnt vmcnt(8) lgkmcnt(0)
	s_barrier
	s_setprio 1
	v_mfma_f32_16x16x128_f8f6f4 v[94:97], v[18:25], v[176:183], 0
	v_mfma_f32_16x16x128_f8f6f4 v[90:93], v[26:33], v[176:183], 0
	v_mfma_f32_16x16x128_f8f6f4 v[78:81], v[18:25], v[184:191], 0
	v_mfma_f32_16x16x128_f8f6f4 v[74:77], v[26:33], v[184:191], 0
	v_mfma_f32_16x16x128_f8f6f4 v[62:65], v[18:25], v[192:199], 0
	v_mfma_f32_16x16x128_f8f6f4 v[58:61], v[26:33], v[192:199], 0
	v_mfma_f32_16x16x128_f8f6f4 v[46:49], v[18:25], v[200:207], 0
	v_mfma_f32_16x16x128_f8f6f4 v[42:45], v[26:33], v[200:207], 0
	v_mfma_f32_16x16x128_f8f6f4 v[86:89], v[2:9], v[176:183], 0
	v_mfma_f32_16x16x128_f8f6f4 v[82:85], v[10:17], v[176:183], 0
	v_mfma_f32_16x16x128_f8f6f4 v[70:73], v[2:9], v[184:191], 0
	v_mfma_f32_16x16x128_f8f6f4 v[66:69], v[10:17], v[184:191], 0
	v_mfma_f32_16x16x128_f8f6f4 v[54:57], v[2:9], v[192:199], 0
	v_mfma_f32_16x16x128_f8f6f4 v[50:53], v[10:17], v[192:199], 0
	v_mfma_f32_16x16x128_f8f6f4 v[38:41], v[2:9], v[200:207], 0
	v_mfma_f32_16x16x128_f8f6f4 v[34:37], v[10:17], v[200:207], 0
	s_setprio 0
	s_barrier
	s_branch .Lmid7

.LBB0_2128:
	v_add_u32_e32 v0, 0x10000, v169
	v_add_u32_e32 v12, 0x14000, v169
	s_add_u32 s26, s22, 0x100
	ds_read_b128 v[16:19], v0
	ds_read_b128 v[20:23], v0 offset:1024
	ds_read_b128 v[24:27], v0 offset:2048
	ds_read_b128 v[28:31], v0 offset:3072
	ds_read_b128 v[0:3], v12
	ds_read_b128 v[4:7], v12 offset:1024
	ds_read_b128 v[8:11], v12 offset:2048
	ds_read_b128 v[12:15], v12 offset:3072
	s_addc_u32 s27, s23, 0
	s_cmp_eq_u32 s83, 4
	s_cselect_b32 s42, s15, s26
	s_cselect_b32 s43, s13, s27
	s_cselect_b32 s37, s17, s82
	s_cselect_b32 s36, s16, s81
	s_add_u32 s38, s42, 0x80
	s_addc_u32 s39, s43, 0
	s_add_u32 s40, s36, 0x80
	s_addc_u32 s41, s37, 0
	ds_read_b128 v[172:175], v170
	ds_read_b128 v[176:179], v170 offset:1024
	ds_read_b128 v[180:183], v170 offset:2048
	ds_read_b128 v[184:187], v170 offset:3072
	ds_read_b128 v[188:191], v170 offset:4096
	ds_read_b128 v[192:195], v170 offset:5120
	ds_read_b128 v[196:199], v170 offset:6144
	ds_read_b128 v[200:203], v170 offset:7168
	s_add_u32 s22, s22, 0x20080
	s_addc_u32 s23, s23, 0
	s_mov_b32 s33, m0
	s_mov_b32 m0, s64
	s_nop 2
	global_load_lds_dwordx4 v162, s[22:23]
	s_mov_b32 m0, s33
	s_nop 0
	s_mov_b32 s33, m0
	s_mov_b32 m0, s65
	s_nop 2
	global_load_lds_dwordx4 v164, s[22:23]
	s_mov_b32 m0, s33
	s_waitcnt vmcnt(8) lgkmcnt(0)
	s_barrier
	s_setprio 1
	v_mfma_f32_16x16x128_f8f6f4 v[156:159], v[16:23], v[172:179], v[156:159]
	v_mfma_f32_16x16x128_f8f6f4 v[152:155], v[24:31], v[172:179], v[152:155]
	v_mfma_f32_16x16x128_f8f6f4 v[140:143], v[16:23], v[180:187], v[140:143]
	v_mfma_f32_16x16x128_f8f6f4 v[136:139], v[24:31], v[180:187], v[136:139]
	v_mfma_f32_16x16x128_f8f6f4 v[124:127], v[16:23], v[188:195], v[124:127]
	v_mfma_f32_16x16x128_f8f6f4 v[120:123], v[24:31], v[188:195], v[120:123]
	v_mfma_f32_16x16x128_f8f6f4 v[108:111], v[16:23], v[196:203], v[108:111]
	v_mfma_f32_16x16x128_f8f6f4 v[104:107], v[24:31], v[196:203], v[104:107]
	v_mfma_f32_16x16x128_f8f6f4 v[148:151], v[0:7], v[172:179], v[148:151]
	v_mfma_f32_16x16x128_f8f6f4 v[144:147], v[8:15], v[172:179], v[144:147]
	v_mfma_f32_16x16x128_f8f6f4 v[132:135], v[0:7], v[180:187], v[132:135]
	v_mfma_f32_16x16x128_f8f6f4 v[128:131], v[8:15], v[180:187], v[128:131]
	v_mfma_f32_16x16x128_f8f6f4 v[116:119], v[0:7], v[188:195], v[116:119]
	v_mfma_f32_16x16x128_f8f6f4 v[112:115], v[8:15], v[188:195], v[112:115]
	v_mfma_f32_16x16x128_f8f6f4 v[100:103], v[0:7], v[196:203], v[100:103]
	v_mfma_f32_16x16x128_f8f6f4 v[96:99], v[8:15], v[196:203], v[96:99]
	s_setprio 0
	s_barrier
	ds_read_b128 v[172:175], v170 offset:16384
	ds_read_b128 v[176:179], v170 offset:17408
	ds_read_b128 v[180:183], v170 offset:18432
	ds_read_b128 v[184:187], v170 offset:19456
	ds_read_b128 v[188:191], v170 offset:20480
	ds_read_b128 v[192:195], v170 offset:21504
	ds_read_b128 v[196:199], v170 offset:22528
	ds_read_b128 v[200:203], v170 offset:23552
	s_mov_b32 s22, m0
	s_mov_b32 m0, s31
	s_nop 2
	global_load_lds_dwordx4 v163, s[36:37]
	s_mov_b32 m0, s22
	s_nop 0
	s_mov_b32 s22, m0
	s_mov_b32 m0, s44
	s_nop 2
	global_load_lds_dwordx4 v165, s[36:37]
	s_mov_b32 m0, s22
	s_add_u32 s22, s36, 0x20000
	s_addc_u32 s23, s37, 0
	s_mov_b32 s33, m0
	s_mov_b32 m0, s45
	s_nop 2
	global_load_lds_dwordx4 v163, s[22:23]
	s_mov_b32 m0, s33
	s_nop 0
	s_mov_b32 s33, m0
	s_mov_b32 m0, s46
	s_nop 2
	global_load_lds_dwordx4 v165, s[22:23]
	s_mov_b32 m0, s33
	s_mov_b32 s22, m0
	s_mov_b32 m0, s21
	s_nop 2
	global_load_lds_dwordx4 v162, s[42:43]
	s_mov_b32 m0, s22
	s_nop 0
	s_mov_b32 s22, m0
	s_mov_b32 m0, s47
	s_nop 2
	global_load_lds_dwordx4 v164, s[42:43]
	s_mov_b32 m0, s22
	s_waitcnt vmcnt(8) lgkmcnt(0)
	s_barrier
	s_setprio 1
	v_mfma_f32_16x16x128_f8f6f4 v[92:95], v[16:23], v[172:179], v[92:95]
	v_mfma_f32_16x16x128_f8f6f4 v[88:91], v[24:31], v[172:179], v[88:91]
	v_mfma_f32_16x16x128_f8f6f4 v[76:79], v[16:23], v[180:187], v[76:79]
	v_mfma_f32_16x16x128_f8f6f4 v[72:75], v[24:31], v[180:187], v[72:75]
	v_mfma_f32_16x16x128_f8f6f4 v[60:63], v[16:23], v[188:195], v[60:63]
	v_mfma_f32_16x16x128_f8f6f4 v[56:59], v[24:31], v[188:195], v[56:59]
	v_mfma_f32_16x16x128_f8f6f4 v[44:47], v[16:23], v[196:203], v[44:47]
	v_mfma_f32_16x16x128_f8f6f4 v[40:43], v[24:31], v[196:203], v[40:43]
	v_mfma_f32_16x16x128_f8f6f4 v[84:87], v[0:7], v[172:179], v[84:87]
	v_mfma_f32_16x16x128_f8f6f4 v[80:83], v[8:15], v[172:179], v[80:83]
	v_mfma_f32_16x16x128_f8f6f4 v[68:71], v[0:7], v[180:187], v[68:71]
	v_mfma_f32_16x16x128_f8f6f4 v[64:67], v[8:15], v[180:187], v[64:67]
	v_mfma_f32_16x16x128_f8f6f4 v[52:55], v[0:7], v[188:195], v[52:55]
	v_mfma_f32_16x16x128_f8f6f4 v[48:51], v[8:15], v[188:195], v[48:51]
	v_mfma_f32_16x16x128_f8f6f4 v[36:39], v[0:7], v[196:203], v[36:39]
	v_mfma_f32_16x16x128_f8f6f4 v[32:35], v[8:15], v[196:203], v[32:35]
	s_setprio 0
	s_barrier
	v_add_u32_e32 v12, 0x18000, v169
	v_add_u32_e32 v28, 0x1c000, v169
	ds_read_b128 v[0:3], v12
	ds_read_b128 v[4:7], v12 offset:1024
	ds_read_b128 v[8:11], v12 offset:2048
	ds_read_b128 v[12:15], v12 offset:3072
	ds_read_b128 v[16:19], v28
	ds_read_b128 v[20:23], v28 offset:1024
	ds_read_b128 v[24:27], v28 offset:2048
	ds_read_b128 v[28:31], v28 offset:3072
	ds_read_b128 v[172:175], v170 offset:32768
	ds_read_b128 v[176:179], v170 offset:33792
	ds_read_b128 v[180:183], v170 offset:34816
	ds_read_b128 v[184:187], v170 offset:35840
	ds_read_b128 v[188:191], v170 offset:36864
	ds_read_b128 v[192:195], v170 offset:37888
	ds_read_b128 v[196:199], v170 offset:38912
	ds_read_b128 v[200:203], v170 offset:39936
	s_add_u32 s22, s42, 0x20000
	s_addc_u32 s23, s43, 0
	s_mov_b32 s33, m0
	s_mov_b32 m0, s48
	s_nop 2
	global_load_lds_dwordx4 v162, s[22:23]
	s_mov_b32 m0, s33
	s_nop 0
	s_mov_b32 s33, m0
	s_mov_b32 m0, s49
	s_nop 2
	global_load_lds_dwordx4 v164, s[22:23]
	s_mov_b32 m0, s33
	s_waitcnt vmcnt(8) lgkmcnt(0)
	s_barrier
	s_setprio 1
	v_mfma_f32_16x16x128_f8f6f4 v[156:159], v[0:7], v[172:179], v[156:159]
	v_mfma_f32_16x16x128_f8f6f4 v[152:155], v[8:15], v[172:179], v[152:155]
	v_mfma_f32_16x16x128_f8f6f4 v[140:143], v[0:7], v[180:187], v[140:143]
	v_mfma_f32_16x16x128_f8f6f4 v[136:139], v[8:15], v[180:187], v[136:139]
	v_mfma_f32_16x16x128_f8f6f4 v[124:127], v[0:7], v[188:195], v[124:127]
	v_mfma_f32_16x16x128_f8f6f4 v[120:123], v[8:15], v[188:195], v[120:123]
	v_mfma_f32_16x16x128_f8f6f4 v[108:111], v[0:7], v[196:203], v[108:111]
	v_mfma_f32_16x16x128_f8f6f4 v[104:107], v[8:15], v[196:203], v[104:107]
	v_mfma_f32_16x16x128_f8f6f4 v[148:151], v[16:23], v[172:179], v[148:151]
	v_mfma_f32_16x16x128_f8f6f4 v[144:147], v[24:31], v[172:179], v[144:147]
	v_mfma_f32_16x16x128_f8f6f4 v[132:135], v[16:23], v[180:187], v[132:135]
	v_mfma_f32_16x16x128_f8f6f4 v[128:131], v[24:31], v[180:187], v[128:131]
	v_mfma_f32_16x16x128_f8f6f4 v[116:119], v[16:23], v[188:195], v[116:119]
	v_mfma_f32_16x16x128_f8f6f4 v[112:115], v[24:31], v[188:195], v[112:115]
	v_mfma_f32_16x16x128_f8f6f4 v[100:103], v[16:23], v[196:203], v[100:103]
	v_mfma_f32_16x16x128_f8f6f4 v[96:99], v[24:31], v[196:203], v[96:99]
	s_setprio 0
	s_barrier
	ds_read_b128 v[172:175], v170 offset:49152
	ds_read_b128 v[176:179], v170 offset:50176
	ds_read_b128 v[180:183], v170 offset:51200
	ds_read_b128 v[184:187], v170 offset:52224
	ds_read_b128 v[188:191], v170 offset:53248
	ds_read_b128 v[192:195], v170 offset:54272
	ds_read_b128 v[196:199], v170 offset:55296
	ds_read_b128 v[200:203], v170 offset:56320
	s_mov_b32 s22, m0
	s_mov_b32 m0, s58
	s_nop 2
	global_load_lds_dwordx4 v163, s[40:41]
	s_mov_b32 m0, s22
	s_nop 0
	s_mov_b32 s22, m0
	s_mov_b32 m0, s59
	s_nop 2
	global_load_lds_dwordx4 v165, s[40:41]
	s_mov_b32 m0, s22
	s_add_u32 s22, s36, 0x20080
	s_addc_u32 s23, s37, 0
	s_mov_b32 s33, m0
	s_mov_b32 m0, s62
	s_nop 2
	global_load_lds_dwordx4 v163, s[22:23]
	s_mov_b32 m0, s33
	s_nop 0
	s_mov_b32 s33, m0
	s_mov_b32 m0, s63
	s_nop 2
	global_load_lds_dwordx4 v165, s[22:23]
	s_mov_b32 m0, s33
	s_mov_b32 s22, m0
	s_mov_b32 m0, s60
	s_nop 2
	global_load_lds_dwordx4 v162, s[38:39]
	s_mov_b32 m0, s22
	s_nop 0
	s_mov_b32 s22, m0
	s_mov_b32 m0, s61
	s_nop 2
	global_load_lds_dwordx4 v164, s[38:39]
	s_mov_b32 m0, s22
	s_waitcnt vmcnt(8) lgkmcnt(0)
	s_barrier
	s_setprio 1
	v_mfma_f32_16x16x128_f8f6f4 v[92:95], v[0:7], v[172:179], v[92:95]
	v_mfma_f32_16x16x128_f8f6f4 v[88:91], v[8:15], v[172:179], v[88:91]
	v_mfma_f32_16x16x128_f8f6f4 v[76:79], v[0:7], v[180:187], v[76:79]
	v_mfma_f32_16x16x128_f8f6f4 v[72:75], v[8:15], v[180:187], v[72:75]
	v_mfma_f32_16x16x128_f8f6f4 v[60:63], v[0:7], v[188:195], v[60:63]
	v_mfma_f32_16x16x128_f8f6f4 v[56:59], v[8:15], v[188:195], v[56:59]
	v_mfma_f32_16x16x128_f8f6f4 v[44:47], v[0:7], v[196:203], v[44:47]
	v_mfma_f32_16x16x128_f8f6f4 v[40:43], v[8:15], v[196:203], v[40:43]
	v_mfma_f32_16x16x128_f8f6f4 v[84:87], v[16:23], v[172:179], v[84:87]
	v_mfma_f32_16x16x128_f8f6f4 v[80:83], v[24:31], v[172:179], v[80:83]
	v_mfma_f32_16x16x128_f8f6f4 v[68:71], v[16:23], v[180:187], v[68:71]
	v_mfma_f32_16x16x128_f8f6f4 v[64:67], v[24:31], v[180:187], v[64:67]
	v_mfma_f32_16x16x128_f8f6f4 v[52:55], v[16:23], v[188:195], v[52:55]
	v_mfma_f32_16x16x128_f8f6f4 v[48:51], v[24:31], v[188:195], v[48:51]
	v_mfma_f32_16x16x128_f8f6f4 v[36:39], v[16:23], v[196:203], v[36:39]
	v_mfma_f32_16x16x128_f8f6f4 v[32:35], v[24:31], v[196:203], v[32:35]
	s_setprio 0
	s_barrier
	s_add_i32 s83, s83, 2
	s_add_u32 s81, s81, 0x100
	s_addc_u32 s82, s82, 0
	s_cmp_gt_u32 s83, 5
	s_cbranch_scc1 .LBB0_2130
	s_mov_b64 s[22:23], s[26:27]
	s_cmp_lg_u32 s83, -2
	s_cbranch_scc0 .LBB0_2121
	s_branch .LBB0_2128
